# attention loop: one barrier per tile, three K/V stages, waves 4-7 run MFMA block first
# baseline (speedup 1.0000x reference)
; #define AT_LOADK(t) do { const int kr_ = AT_KROW(t); _Pragma("unroll") for (int i_ = 0; i_ < 2; ++i_) kreg[i_] = *(const u32x4*)(Kp + (size_t)(kr_ + prow0 + 32 * i_) * 512 + pch * 8); } while (0)
; #define AT_LOADV(t) do { const int kr_ = AT_KROW(t); _Pragma("unroll") for (int i_ = 0; i_ < 2; ++i_) vreg[i_] = *(const u32x4*)(Vp + (size_t)(kr_ + prow0 + 32 * i_) * 512 + pch * 8); } while (0)
; #define AT_STOREK(st) do { _Pragma("unroll") for (int i_ = 0; i_ < 2; ++i_) *(LAS u32x4*)(L + AT_K + (st) * AT_KBYTES + (prow0 + 32 * i_) * AT_KSTR + pch * 16) = kreg[i_]; } while (0)
; #define AT_STOREV(st) do { _Pragma("unroll") for (int i_ = 0; i_ < 2; ++i_) *(LAS u32x4*)(L + AT_V + (st) * AT_VBYTES + (prow0 + 32 * i_) * AT_VSTR + pch * 16) = vreg[i_]; } while (0)
; __device__ __forceinline__ void attn_unit(const Frame& F, int layer, int qrow0, int ntiles, int b, int head, float lam, float m2, float lam_init) {
;     ...
;     if (wave >= 4) __builtin_amdgcn_s_setprio(1);
;     AT_LOADK(0); AT_LOADV(0); AT_STOREK(0); AT_STOREV(0);
;     if (ntiles > 1) { AT_LOADK(1); AT_STOREK(1); }
;     __syncthreads();
.LBB0_549:
	s_add_u32 s42, s4, s30
	s_addc_u32 s43, s5, 0
	s_add_u32 s2, s2, s30
	s_addc_u32 s3, s3, 0
	s_lshl_b32 s4, s16, 8
	v_ashrrev_i32_e32 v186, 4, v32
	s_add_i32 s5, s4, 0x8000
	s_add_i32 s16, s4, 0x8040
	v_lshlrev_b32_e32 v3, 4, v32
	v_add_u32_e32 v128, s5, v186
	v_and_b32_e32 v144, 0xf0, v3
	v_add_u32_e32 v20, s16, v186
	v_lshl_add_u64 v[4:5], s[2:3], 0, v[144:145]
	s_mov_b64 s[2:3], 0x31534800
	v_ashrrev_i32_e32 v129, 31, v128
	v_ashrrev_i32_e32 v21, 31, v20
	v_lshl_add_u64 v[180:181], v[4:5], 0, s[2:3]
	v_lshlrev_b64 v[12:13], 10, v[128:129]
	s_mov_b64 s[2:3], 0x8000
	v_lshl_add_u64 v[16:17], s[42:43], 0, v[144:145]
	s_mov_b64 s[42:43], 0x33934800
	v_lshlrev_b64 v[62:63], 10, v[20:21]
	v_lshl_add_u64 v[14:15], v[12:13], 0, s[2:3]
	v_lshl_add_u64 v[182:183], v[16:17], 0, s[42:43]
	v_lshl_add_u64 v[96:97], v[62:63], 0, s[2:3]
	v_lshl_add_u64 v[4:5], v[180:181], 0, v[12:13]
	v_lshl_add_u64 v[8:9], v[180:181], 0, v[14:15]
	v_lshl_add_u64 v[12:13], v[182:183], 0, v[12:13]
	v_lshl_add_u64 v[16:17], v[182:183], 0, v[14:15]
	v_lshl_add_u64 v[20:21], v[180:181], 0, v[62:63]
	v_lshl_add_u64 v[24:25], v[180:181], 0, v[96:97]
	global_load_dwordx4 v[4:7], v[4:5], off
	s_nop 0
	global_load_dwordx4 v[8:11], v[8:9], off
	s_nop 0
	global_load_dwordx4 v[12:15], v[12:13], off
	s_nop 0
	global_load_dwordx4 v[16:19], v[16:17], off
	s_nop 0
	global_load_dwordx4 v[20:23], v[20:21], off
	s_nop 0
	global_load_dwordx4 v[24:27], v[24:25], off
	v_or_b32_e32 v1, s15, v1
	s_movk_i32 s16, 0x140
	v_mul_u32_u24_e32 v0, 0x110, v0
	v_mul_lo_u32 v198, v186, s24
	v_mul_lo_u32 v199, v186, s16
	v_lshlrev_b32_e32 v1, 1, v1
	v_add_u32_e32 v200, 0, v144
	v_xor_b32_e32 v64, 0x80000000, v2
	v_add_u32_e32 v2, 0x2800, v199
	v_add3_u32 v197, 0, v0, v1
	v_add_u32_e32 v144, v200, v198
	v_add_u32_e32 v194, v200, v199
	v_add_u32_e32 v195, v200, v2
	v_mov_b32_e32 v65, v64
	v_mov_b32_e32 v66, v64
	v_mov_b32_e32 v67, v64
	v_mov_b32_e32 v68, v64
	v_mov_b32_e32 v69, v64
	v_mov_b32_e32 v70, v64
	v_mov_b32_e32 v71, v64
	v_mov_b32_e32 v72, v64
	v_mov_b32_e32 v73, v64
	v_mov_b32_e32 v74, v64
	v_mov_b32_e32 v75, v64
	v_mov_b32_e32 v76, v64
	v_mov_b32_e32 v77, v64
	v_mov_b32_e32 v78, v64
	v_mov_b32_e32 v79, v64
	v_and_b32_e32 v193, 63, v32
	v_and_b32_e32 v33, 16, v32
	s_mov_b32 s15, 0x8000
	s_mov_b32 s2, 4
	s_mov_b32 s3, 0
	s_add_i32 s5, s4, 0x8080
	s_add_i32 s4, s4, 0x80c0
	s_waitcnt vmcnt(5)
	ds_write_b128 v144, v[4:7]
	s_waitcnt vmcnt(4)
	ds_write_b128 v144, v[8:11] offset:8704
	s_waitcnt vmcnt(3)
	ds_write_b128 v194, v[12:15] offset:34816
	s_waitcnt vmcnt(2)
	ds_write_b128 v195, v[16:19] offset:34816
	s_waitcnt vmcnt(1)
	ds_write_b128 v144, v[20:23] offset:17408
	s_waitcnt vmcnt(0)
	ds_write_b128 v144, v[24:27] offset:26112
	s_waitcnt lgkmcnt(0)
	s_barrier
	v_readfirstlane_b32 s72, v180
	v_readfirstlane_b32 s73, v181
	v_readfirstlane_b32 s74, v182
	v_readfirstlane_b32 s75, v183
	v_lshl_add_u32 v178, v186, 10, v200
	s_add_i32 s42, s4, 0xffffff40
	s_add_i32 s43, s4, 0xffff7f40
	s_lshl_b32 s43, s43, 3
	s_add_i32 s43, s43, 0xffffff00
	s_mov_b32 s2, 0
	s_add_i32 s5, s2, 2
	s_cmp_ge_u32 s5, 36
	s_cbranch_scc1 .Latt_nokload_pro
	s_cmp_lt_u32 s5, 4
	s_cselect_b32 s15, s42, s43
	s_lshl_b32 s45, s5, 6
	s_add_i32 s15, s15, s45
	s_lshl_b32 s15, s15, 10
	v_add_u32_e32 v186, s15, v178
	v_add_u32_e32 v187, 0x8000, v186
	global_load_dwordx4 v[162:165], v186, s[72:73]
	global_load_dwordx4 v[166:169], v187, s[72:73]

; __device__ __forceinline__ void lds_barrier() { asm volatile("s_waitcnt lgkmcnt(0)" ::: "memory"); __builtin_amdgcn_s_barrier(); asm volatile("" ::: "memory"); }
; #define AT_LOADK(t) do { const int kr_ = AT_KROW(t); _Pragma("unroll") for (int i_ = 0; i_ < 2; ++i_) kreg[i_] = *(const u32x4*)(Kp + (size_t)(kr_ + prow0 + 32 * i_) * 512 + pch * 8); } while (0)
; #define AT_LOADV(t) do { const int kr_ = AT_KROW(t); _Pragma("unroll") for (int i_ = 0; i_ < 2; ++i_) vreg[i_] = *(const u32x4*)(Vp + (size_t)(kr_ + prow0 + 32 * i_) * 512 + pch * 8); } while (0)
; #define AT_STOREK(st) do { _Pragma("unroll") for (int i_ = 0; i_ < 2; ++i_) *(LAS u32x4*)(L + AT_K + (st) * AT_KBYTES + (prow0 + 32 * i_) * AT_KSTR + pch * 16) = kreg[i_]; } while (0)
; #define AT_STOREV(st) do { _Pragma("unroll") for (int i_ = 0; i_ < 2; ++i_) *(LAS u32x4*)(L + AT_V + (st) * AT_VBYTES + (prow0 + 32 * i_) * AT_VSTR + pch * 16) = vreg[i_]; } while (0)
; __device__ __forceinline__ void attn_unit(const Frame& F, int layer, int qrow0, int ntiles, int b, int head, float lam, float m2, float lam_init) {
;     ...
;     if (wave >= 4) __builtin_amdgcn_s_setprio(1);
;     AT_LOADK(0); AT_LOADV(0); AT_STOREK(0); AT_STOREV(0);
;     if (ntiles > 1) { AT_LOADK(1); AT_STOREK(1); }
;     __syncthreads();
;     f32x16 sa, sb, na, nb;
;     AT_QK(sa, sb, 0);
;     lds_barrier();
.Latt_novload_pro:
	v_bfe_u32 v186, v193, 2, 2
	v_lshrrev_b32_e32 v187, 5, v193
	v_lshl_add_u32 v186, v187, 2, v186
	v_mul_u32_u24_e32 v196, 0x140, v186
	v_bfe_u32 v187, v193, 4, 1
	v_and_b32_e32 v188, 3, v193
	v_lshl_add_u32 v196, v188, 3, v196
	v_lshl_add_u32 v196, v187, 5, v196
	v_add_u32_e32 v191, 20480, v196
	v_add_u32_e32 v184, 60416, v196
	v_add_u32_e32 v185, 20480, v194
	v_add_u32_e32 v195, 60416, v194
	v_add_u32_e32 v190, 77824, v197
	v_add_u32_e32 v179, 77824, v144
	v_add_u32_e32 v198, 116000, v144
	v_add_u32_e32 v199, 98592, v194
	v_mov_b32_e32 v0, 0
	v_mov_b32_e32 v1, 0
	v_mov_b32_e32 v2, 0
	v_mov_b32_e32 v3, 0
	v_mov_b32_e32 v4, 0
	v_mov_b32_e32 v5, 0
	v_mov_b32_e32 v6, 0
	v_mov_b32_e32 v7, 0
	v_mov_b32_e32 v8, 0
	v_mov_b32_e32 v9, 0
	v_mov_b32_e32 v10, 0
	v_mov_b32_e32 v11, 0
	v_mov_b32_e32 v12, 0
	v_mov_b32_e32 v13, 0
	v_mov_b32_e32 v14, 0
	v_mov_b32_e32 v15, 0
	v_mov_b32_e32 v16, 0
	v_mov_b32_e32 v17, 0
	v_mov_b32_e32 v18, 0
	v_mov_b32_e32 v19, 0
	v_mov_b32_e32 v20, 0
	v_mov_b32_e32 v21, 0
	v_mov_b32_e32 v22, 0
	v_mov_b32_e32 v23, 0
	v_mov_b32_e32 v24, 0
	v_mov_b32_e32 v25, 0
	v_mov_b32_e32 v26, 0
	v_mov_b32_e32 v27, 0
	v_mov_b32_e32 v28, 0
	v_mov_b32_e32 v29, 0
	v_mov_b32_e32 v30, 0
	v_mov_b32_e32 v31, 0
	v_mov_b32_e32 v32, 0
	v_mov_b32_e32 v33, 0
	v_mov_b32_e32 v34, 0
	v_mov_b32_e32 v35, 0
	v_mov_b32_e32 v36, 0
	v_mov_b32_e32 v37, 0
	v_mov_b32_e32 v38, 0
	v_mov_b32_e32 v39, 0
	v_mov_b32_e32 v40, 0
	v_mov_b32_e32 v41, 0
	v_mov_b32_e32 v42, 0
	v_mov_b32_e32 v43, 0
	v_mov_b32_e32 v44, 0
	v_mov_b32_e32 v45, 0
	v_mov_b32_e32 v46, 0
	v_mov_b32_e32 v47, 0
	v_mov_b32_e32 v48, 0
	v_mov_b32_e32 v49, 0
	v_mov_b32_e32 v50, 0
	v_mov_b32_e32 v51, 0
	v_mov_b32_e32 v52, 0
	v_mov_b32_e32 v53, 0
	v_mov_b32_e32 v54, 0
	v_mov_b32_e32 v55, 0
	v_mov_b32_e32 v56, 0
	v_mov_b32_e32 v57, 0
	v_mov_b32_e32 v58, 0
	v_mov_b32_e32 v59, 0
	v_mov_b32_e32 v60, 0
	v_mov_b32_e32 v61, 0
	v_mov_b32_e32 v62, 0
	v_mov_b32_e32 v63, 0
	v_mov_b32_e32 v201, 0
	s_cmp_ge_u32 s12, 4
	s_cbranch_scc1 .Latt_pro_done
	ds_read_b128 v[128:131], v197 offset:0
	ds_read_b128 v[132:135], v197 offset:8704
	ds_read_b128 v[136:139], v197 offset:32
	ds_read_b128 v[140:143], v197 offset:8736
	s_waitcnt lgkmcnt(2)
	v_mfma_f32_32x32x16_bf16 v[80:95], v[128:131], v[158:161], v[64:79]
	v_mfma_f32_32x32x16_bf16 v[96:111], v[132:135], v[158:161], v[64:79]
	ds_read_b128 v[128:131], v197 offset:64
	ds_read_b128 v[132:135], v197 offset:8768
	s_waitcnt lgkmcnt(2)
	v_mfma_f32_32x32x16_bf16 v[80:95], v[136:139], v[154:157], v[80:95]
	v_mfma_f32_32x32x16_bf16 v[96:111], v[140:143], v[154:157], v[96:111]
	ds_read_b128 v[136:139], v197 offset:96
	ds_read_b128 v[140:143], v197 offset:8800
	s_waitcnt lgkmcnt(2)
	v_mfma_f32_32x32x16_bf16 v[80:95], v[128:131], v[150:153], v[80:95]
	v_mfma_f32_32x32x16_bf16 v[96:111], v[132:135], v[150:153], v[96:111]
	s_waitcnt lgkmcnt(0)
	v_mfma_f32_32x32x16_bf16 v[80:95], v[136:139], v[146:149], v[80:95]
	v_mfma_f32_32x32x16_bf16 v[96:111], v[140:143], v[146:149], v[96:111]
	s_nop 7
	s_nop 7
.Latt_pro_done:
	s_cmp_ge_u32 s12, 4
	s_cbranch_scc1 .Latt_lag_loop
	.p2align 6

; __device__ __forceinline__ unsigned pk2(float lo, float hi) { f32x2_t v = {lo, hi}; bf16x2_t b = __builtin_convertvector(v, bf16x2_t); return __builtin_bit_cast(unsigned, b); }
; __device__ __forceinline__ void attn_unit(const Frame& F, int layer, int qrow0, int ntiles, int b, int head, float lam, float m2, float lam_init) {
;     ...
;         float ls = 0.f;
; #pragma unroll
;         for (int i = 0; i < 16; ++i) { sa[i] = __builtin_amdgcn_exp2f(sa[i]); sb[i] = __builtin_amdgcn_exp2f(sb[i]); ls += sa[i] + sb[i]; }
;         lsum += ls;
;         bf16x8 pk[4];
;         { u32x4 w0, w1, w2, w3;
; #pragma unroll
;           for (int i = 0; i < 4; ++i) { w0[i] = pk2(sa[2 * i], sa[2 * i + 1]); w1[i] = pk2(sa[8 + 2 * i], sa[9 + 2 * i]); w2[i] = pk2(sb[2 * i], sb[2 * i + 1]); w3[i] = pk2(sb[8 + 2 * i], sb[9 + 2 * i]); }
;           pk[0] = __builtin_bit_cast(bf16x8, w0); pk[1] = __builtin_bit_cast(bf16x8, w1); pk[2] = __builtin_bit_cast(bf16x8, w2); pk[3] = __builtin_bit_cast(bf16x8, w3); }
.Latt_novload_a0:
	v_exp_f32_e32 v80, v80
	v_exp_f32_e32 v96, v96
	v_exp_f32_e32 v81, v81
	v_exp_f32_e32 v97, v97
	v_exp_f32_e32 v82, v82
	v_exp_f32_e32 v98, v98
	v_exp_f32_e32 v83, v83
	v_exp_f32_e32 v99, v99
	v_exp_f32_e32 v84, v84
	v_exp_f32_e32 v100, v100
	v_exp_f32_e32 v85, v85
	v_exp_f32_e32 v101, v101
	v_exp_f32_e32 v86, v86
	v_exp_f32_e32 v102, v102
	v_exp_f32_e32 v87, v87
	v_exp_f32_e32 v103, v103
	v_exp_f32_e32 v88, v88
	v_exp_f32_e32 v104, v104
	v_exp_f32_e32 v89, v89
	v_exp_f32_e32 v105, v105
	v_exp_f32_e32 v90, v90
	v_exp_f32_e32 v106, v106
	v_exp_f32_e32 v91, v91
	v_exp_f32_e32 v107, v107
	v_exp_f32_e32 v92, v92
	v_exp_f32_e32 v108, v108
	v_exp_f32_e32 v93, v93
	v_exp_f32_e32 v109, v109
	v_exp_f32_e32 v94, v94
	v_exp_f32_e32 v110, v110
	v_exp_f32_e32 v95, v95
	v_exp_f32_e32 v111, v111
	v_cvt_pk_bf16_f32 v112, v80, v81
	v_cvt_pk_bf16_f32 v113, v82, v83
	v_cvt_pk_bf16_f32 v114, v84, v85
	v_cvt_pk_bf16_f32 v115, v86, v87
	v_cvt_pk_bf16_f32 v116, v88, v89
	v_cvt_pk_bf16_f32 v117, v90, v91
	v_cvt_pk_bf16_f32 v118, v92, v93
	v_cvt_pk_bf16_f32 v119, v94, v95
	v_cvt_pk_bf16_f32 v120, v96, v97
	v_cvt_pk_bf16_f32 v121, v98, v99
	v_cvt_pk_bf16_f32 v122, v100, v101
	v_cvt_pk_bf16_f32 v123, v102, v103
	v_cvt_pk_bf16_f32 v124, v104, v105
	v_cvt_pk_bf16_f32 v125, v106, v107
	v_cvt_pk_bf16_f32 v126, v108, v109
	v_cvt_pk_bf16_f32 v127, v110, v111
	v_add_f32_e32 v80, v80, v96
	v_add_f32_e32 v81, v81, v97
	v_add_f32_e32 v82, v82, v98
	v_add_f32_e32 v83, v83, v99
	v_add_f32_e32 v84, v84, v100
	v_add_f32_e32 v85, v85, v101
	v_add_f32_e32 v86, v86, v102
	v_add_f32_e32 v87, v87, v103
	v_add_f32_e32 v88, v88, v104
	v_add_f32_e32 v89, v89, v105
	v_add_f32_e32 v90, v90, v106
	v_add_f32_e32 v91, v91, v107
	v_add_f32_e32 v92, v92, v108
	v_add_f32_e32 v93, v93, v109
	v_add_f32_e32 v94, v94, v110
	v_add_f32_e32 v95, v95, v111
	v_add_f32_e32 v80, v80, v88
	v_add_f32_e32 v81, v81, v89
	v_add_f32_e32 v82, v82, v90
	v_add_f32_e32 v83, v83, v91
	v_add_f32_e32 v84, v84, v92
	v_add_f32_e32 v85, v85, v93
	v_add_f32_e32 v86, v86, v94
	v_add_f32_e32 v87, v87, v95
	v_add_f32_e32 v80, v80, v84
	v_add_f32_e32 v81, v81, v85
	v_add_f32_e32 v82, v82, v86
	v_add_f32_e32 v83, v83, v87
	v_add_f32_e32 v80, v80, v82
	v_add_f32_e32 v81, v81, v83
	v_add_f32_e32 v80, v80, v81
	v_add_f32_e32 v201, v201, v80
	s_add_i32 s5, s2, 3
	s_cmp_ge_u32 s5, 36
	s_cbranch_scc1 .Latt_drain_a0
	s_waitcnt vmcnt(4)
	s_branch .Latt_stage_a0

; #define LAS __attribute__((address_space(3)))
; __device__ __forceinline__ unsigned pk2(float lo, float hi) { f32x2_t v = {lo, hi}; bf16x2_t b = __builtin_convertvector(v, bf16x2_t); return __builtin_bit_cast(unsigned, b); }
; #define MFMA32(a, b, c) __builtin_amdgcn_mfma_f32_32x32x16_bf16((a), (b), (c), 0, 0, 0)
; __device__ __forceinline__ void attn_unit(const Frame& F, int layer, int qrow0, int ntiles, int b, int head, float lam, float m2, float lam_init) {
;     ...
;         if (t + 1 < ntiles) AT_QK(na, nb, (t + 1) & 1);
;         float ls = 0.f;
; #pragma unroll
;         for (int i = 0; i < 16; ++i) { sa[i] = __builtin_amdgcn_exp2f(sa[i]); sb[i] = __builtin_amdgcn_exp2f(sb[i]); ls += sa[i] + sb[i]; }
;         lsum += ls;
;         bf16x8 pk[4];
;         { u32x4 w0, w1, w2, w3;
; #pragma unroll
;           for (int i = 0; i < 4; ++i) { w0[i] = pk2(sa[2 * i], sa[2 * i + 1]); w1[i] = pk2(sa[8 + 2 * i], sa[9 + 2 * i]); w2[i] = pk2(sb[2 * i], sb[2 * i + 1]); w3[i] = pk2(sb[8 + 2 * i], sb[9 + 2 * i]); }
;           pk[0] = __builtin_bit_cast(bf16x8, w0); pk[1] = __builtin_bit_cast(bf16x8, w1); pk[2] = __builtin_bit_cast(bf16x8, w2); pk[3] = __builtin_bit_cast(bf16x8, w3); }
;         LAS const unsigned char* Vt = L + AT_V + (t & 1) * AT_VBYTES;
;         __builtin_amdgcn_sched_barrier(0);
;         bf16x8 vfa[4], vfb[4];
; #pragma unroll
;         for (int j = 0; j < 4; ++j) vfa[j] = frag_tr_acc(Vt, AT_VSTR, 0, 32 * j, lane);
; #pragma unroll
;         for (int ks = 0; ks < 4; ks += 2) {
; #pragma unroll
;             for (int j = 0; j < 4; ++j) vfb[j] = frag_tr_acc(Vt, AT_VSTR, 16 * (ks + 1), 32 * j, lane);
; #pragma unroll
;             for (int j = 0; j < 4; ++j) o[j] = MFMA32(pk[ks], vfa[j], o[j]);
;             __builtin_amdgcn_sched_barrier(0);
;             if (ks + 2 < 4) {
; #pragma unroll
;                 for (int j = 0; j < 4; ++j) vfa[j] = frag_tr_acc(Vt, AT_VSTR, 16 * (ks + 2), 32 * j, lane);
;             }
; #pragma unroll
;             for (int j = 0; j < 4; ++j) o[j] = MFMA32(pk[ks + 1], vfb[j], o[j]);
;             __builtin_amdgcn_sched_barrier(0);
;         }
;         if (t + 2 < ntiles) AT_STOREK(t & 1);
;         if (t + 1 < ntiles) AT_STOREV((t + 1) & 1);
.Latt_stage_a0:
	s_add_i32 s5, s2, 2
	s_cmp_ge_u32 s5, 36
	s_cbranch_scc1 .Latt_kscr_a0
	ds_write_b128 v179, v[162:165] offset:0
	ds_write_b128 v179, v[166:169] offset:8704
	s_branch .Latt_kdone_a0
.Latt_kscr_a0:
	ds_write_b128 v198, v[162:165]
	ds_write_b128 v198, v[166:169] offset:8704
.Latt_kdone_a0:
	s_add_i32 s5, s2, 1
	s_cmp_ge_u32 s5, 36
	s_cbranch_scc1 .Latt_vscr_a0
	ds_write_b128 v185, v[170:173] offset:34816
	ds_write_b128 v185, v[174:177] offset:45056
	s_branch .Latt_vdone_a0
.Latt_vscr_a0:
	ds_write_b128 v199, v[170:173] offset:34816
	ds_write_b128 v199, v[174:177] offset:45056
.Latt_vdone_a0:
	s_add_i32 s5, s2, 1
	s_cmp_ge_u32 s5, 36
	s_cbranch_scc1 .Latt_noqkw_a0
	ds_read_b128 v[128:131], v197 offset:17408
	ds_read_b128 v[132:135], v197 offset:26112
	ds_read_b128 v[136:139], v197 offset:17440
	ds_read_b128 v[140:143], v197 offset:26144
	s_waitcnt lgkmcnt(2)
	v_mfma_f32_32x32x16_bf16 v[80:95], v[128:131], v[158:161], v[64:79]
	v_mfma_f32_32x32x16_bf16 v[96:111], v[132:135], v[158:161], v[64:79]
	ds_read_b128 v[128:131], v197 offset:17472
	ds_read_b128 v[132:135], v197 offset:26176
	s_waitcnt lgkmcnt(2)
	v_mfma_f32_32x32x16_bf16 v[80:95], v[136:139], v[154:157], v[80:95]
	v_mfma_f32_32x32x16_bf16 v[96:111], v[140:143], v[154:157], v[96:111]
	ds_read_b128 v[136:139], v197 offset:17504
	ds_read_b128 v[140:143], v197 offset:26208
	s_waitcnt lgkmcnt(2)
	v_mfma_f32_32x32x16_bf16 v[80:95], v[128:131], v[150:153], v[80:95]
	v_mfma_f32_32x32x16_bf16 v[96:111], v[132:135], v[150:153], v[96:111]
	s_waitcnt lgkmcnt(0)
	v_mfma_f32_32x32x16_bf16 v[80:95], v[136:139], v[146:149], v[80:95]
	v_mfma_f32_32x32x16_bf16 v[96:111], v[140:143], v[146:149], v[96:111]
.Latt_noqk_a0:
	ds_read_b64_tr_b16 v[202:203], v196 offset:34816
	ds_read_b64_tr_b16 v[206:207], v196 offset:34880
	ds_read_b64_tr_b16 v[210:211], v196 offset:34944
	ds_read_b64_tr_b16 v[214:215], v196 offset:35008
	ds_read_b64_tr_b16 v[204:205], v196 offset:37376
	ds_read_b64_tr_b16 v[208:209], v196 offset:37440
	ds_read_b64_tr_b16 v[212:213], v196 offset:37504
	ds_read_b64_tr_b16 v[216:217], v196 offset:37568
	ds_read_b64_tr_b16 v[218:219], v196 offset:39936
	ds_read_b64_tr_b16 v[222:223], v196 offset:40000
	ds_read_b64_tr_b16 v[226:227], v196 offset:40064
	ds_read_b64_tr_b16 v[230:231], v196 offset:40128
	ds_read_b64_tr_b16 v[220:221], v196 offset:42496
	ds_read_b64_tr_b16 v[224:225], v196 offset:42560
	ds_read_b64_tr_b16 v[228:229], v196 offset:42624
	s_waitcnt lgkmcnt(14)
	ds_read_b64_tr_b16 v[232:233], v196 offset:42688
	s_waitcnt lgkmcnt(8)
	v_mfma_f32_32x32x16_bf16 v[32:47], v[112:115], v[202:205], v[32:47]
	v_mfma_f32_32x32x16_bf16 v[48:63], v[112:115], v[206:209], v[48:63]
	v_mfma_f32_32x32x16_bf16 v[0:15], v[112:115], v[210:213], v[0:15]
	v_mfma_f32_32x32x16_bf16 v[16:31], v[112:115], v[214:217], v[16:31]
	ds_read_b64_tr_b16 v[202:203], v196 offset:45056
	ds_read_b64_tr_b16 v[206:207], v196 offset:45120
	ds_read_b64_tr_b16 v[210:211], v196 offset:45184
	ds_read_b64_tr_b16 v[214:215], v196 offset:45248
	ds_read_b64_tr_b16 v[204:205], v196 offset:47616
	ds_read_b64_tr_b16 v[208:209], v196 offset:47680
	ds_read_b64_tr_b16 v[212:213], v196 offset:47744
	s_waitcnt lgkmcnt(14)
	ds_read_b64_tr_b16 v[216:217], v196 offset:47808
	s_waitcnt lgkmcnt(8)
	v_mfma_f32_32x32x16_bf16 v[32:47], v[116:119], v[218:221], v[32:47]
	v_mfma_f32_32x32x16_bf16 v[48:63], v[116:119], v[222:225], v[48:63]
	v_mfma_f32_32x32x16_bf16 v[0:15], v[116:119], v[226:229], v[0:15]
	v_mfma_f32_32x32x16_bf16 v[16:31], v[116:119], v[230:233], v[16:31]
	ds_read_b64_tr_b16 v[218:219], v196 offset:50176
	ds_read_b64_tr_b16 v[222:223], v196 offset:50240
	ds_read_b64_tr_b16 v[226:227], v196 offset:50304
	ds_read_b64_tr_b16 v[230:231], v196 offset:50368
	ds_read_b64_tr_b16 v[220:221], v196 offset:52736
	ds_read_b64_tr_b16 v[224:225], v196 offset:52800
	ds_read_b64_tr_b16 v[228:229], v196 offset:52864
	s_waitcnt lgkmcnt(14)
	ds_read_b64_tr_b16 v[232:233], v196 offset:52928
	s_waitcnt lgkmcnt(8)
	v_mfma_f32_32x32x16_bf16 v[32:47], v[120:123], v[202:205], v[32:47]
	v_mfma_f32_32x32x16_bf16 v[48:63], v[120:123], v[206:209], v[48:63]
	v_mfma_f32_32x32x16_bf16 v[0:15], v[120:123], v[210:213], v[0:15]
	v_mfma_f32_32x32x16_bf16 v[16:31], v[120:123], v[214:217], v[16:31]
	s_waitcnt lgkmcnt(0)
	v_mfma_f32_32x32x16_bf16 v[32:47], v[124:127], v[218:221], v[32:47]
	v_mfma_f32_32x32x16_bf16 v[48:63], v[124:127], v[222:225], v[48:63]
	v_mfma_f32_32x32x16_bf16 v[0:15], v[124:127], v[226:229], v[0:15]
	v_mfma_f32_32x32x16_bf16 v[16:31], v[124:127], v[230:233], v[16:31]
	s_barrier
	s_add_i32 s5, s2, 4
	s_cmp_ge_u32 s5, 36
	s_cbranch_scc1 .Latt_nokload_a1
	s_cmp_lt_u32 s5, 4
	s_cselect_b32 s15, s42, s43
	s_lshl_b32 s45, s5, 6
	s_add_i32 s15, s15, s45
	s_lshl_b32 s15, s15, 10
	v_add_u32_e32 v186, s15, v178
	v_add_u32_e32 v187, 0x8000, v186
	global_load_dwordx4 v[162:165], v186, s[72:73]
	global_load_dwordx4 v[166:169], v187, s[72:73]

; __device__ __forceinline__ unsigned pk2(float lo, float hi) { f32x2_t v = {lo, hi}; bf16x2_t b = __builtin_convertvector(v, bf16x2_t); return __builtin_bit_cast(unsigned, b); }
; __device__ __forceinline__ void attn_unit(const Frame& F, int layer, int qrow0, int ntiles, int b, int head, float lam, float m2, float lam_init) {
;     ...
;         float ls = 0.f;
; #pragma unroll
;         for (int i = 0; i < 16; ++i) { sa[i] = __builtin_amdgcn_exp2f(sa[i]); sb[i] = __builtin_amdgcn_exp2f(sb[i]); ls += sa[i] + sb[i]; }
;         lsum += ls;
;         bf16x8 pk[4];
;         { u32x4 w0, w1, w2, w3;
; #pragma unroll
;           for (int i = 0; i < 4; ++i) { w0[i] = pk2(sa[2 * i], sa[2 * i + 1]); w1[i] = pk2(sa[8 + 2 * i], sa[9 + 2 * i]); w2[i] = pk2(sb[2 * i], sb[2 * i + 1]); w3[i] = pk2(sb[8 + 2 * i], sb[9 + 2 * i]); }
;           pk[0] = __builtin_bit_cast(bf16x8, w0); pk[1] = __builtin_bit_cast(bf16x8, w1); pk[2] = __builtin_bit_cast(bf16x8, w2); pk[3] = __builtin_bit_cast(bf16x8, w3); }
.Latt_novload_a1:
	v_exp_f32_e32 v80, v80
	v_exp_f32_e32 v96, v96
	v_exp_f32_e32 v81, v81
	v_exp_f32_e32 v97, v97
	v_exp_f32_e32 v82, v82
	v_exp_f32_e32 v98, v98
	v_exp_f32_e32 v83, v83
	v_exp_f32_e32 v99, v99
	v_exp_f32_e32 v84, v84
	v_exp_f32_e32 v100, v100
	v_exp_f32_e32 v85, v85
	v_exp_f32_e32 v101, v101
	v_exp_f32_e32 v86, v86
	v_exp_f32_e32 v102, v102
	v_exp_f32_e32 v87, v87
	v_exp_f32_e32 v103, v103
	v_exp_f32_e32 v88, v88
	v_exp_f32_e32 v104, v104
	v_exp_f32_e32 v89, v89
	v_exp_f32_e32 v105, v105
	v_exp_f32_e32 v90, v90
	v_exp_f32_e32 v106, v106
	v_exp_f32_e32 v91, v91
	v_exp_f32_e32 v107, v107
	v_exp_f32_e32 v92, v92
	v_exp_f32_e32 v108, v108
	v_exp_f32_e32 v93, v93
	v_exp_f32_e32 v109, v109
	v_exp_f32_e32 v94, v94
	v_exp_f32_e32 v110, v110
	v_exp_f32_e32 v95, v95
	v_exp_f32_e32 v111, v111
	v_cvt_pk_bf16_f32 v112, v80, v81
	v_cvt_pk_bf16_f32 v113, v82, v83
	v_cvt_pk_bf16_f32 v114, v84, v85
	v_cvt_pk_bf16_f32 v115, v86, v87
	v_cvt_pk_bf16_f32 v116, v88, v89
	v_cvt_pk_bf16_f32 v117, v90, v91
	v_cvt_pk_bf16_f32 v118, v92, v93
	v_cvt_pk_bf16_f32 v119, v94, v95
	v_cvt_pk_bf16_f32 v120, v96, v97
	v_cvt_pk_bf16_f32 v121, v98, v99
	v_cvt_pk_bf16_f32 v122, v100, v101
	v_cvt_pk_bf16_f32 v123, v102, v103
	v_cvt_pk_bf16_f32 v124, v104, v105
	v_cvt_pk_bf16_f32 v125, v106, v107
	v_cvt_pk_bf16_f32 v126, v108, v109
	v_cvt_pk_bf16_f32 v127, v110, v111
	v_add_f32_e32 v80, v80, v96
	v_add_f32_e32 v81, v81, v97
	v_add_f32_e32 v82, v82, v98
	v_add_f32_e32 v83, v83, v99
	v_add_f32_e32 v84, v84, v100
	v_add_f32_e32 v85, v85, v101
	v_add_f32_e32 v86, v86, v102
	v_add_f32_e32 v87, v87, v103
	v_add_f32_e32 v88, v88, v104
	v_add_f32_e32 v89, v89, v105
	v_add_f32_e32 v90, v90, v106
	v_add_f32_e32 v91, v91, v107
	v_add_f32_e32 v92, v92, v108
	v_add_f32_e32 v93, v93, v109
	v_add_f32_e32 v94, v94, v110
	v_add_f32_e32 v95, v95, v111
	v_add_f32_e32 v80, v80, v88
	v_add_f32_e32 v81, v81, v89
	v_add_f32_e32 v82, v82, v90
	v_add_f32_e32 v83, v83, v91
	v_add_f32_e32 v84, v84, v92
	v_add_f32_e32 v85, v85, v93
	v_add_f32_e32 v86, v86, v94
	v_add_f32_e32 v87, v87, v95
	v_add_f32_e32 v80, v80, v84
	v_add_f32_e32 v81, v81, v85
	v_add_f32_e32 v82, v82, v86
	v_add_f32_e32 v83, v83, v87
	v_add_f32_e32 v80, v80, v82
	v_add_f32_e32 v81, v81, v83
	v_add_f32_e32 v80, v80, v81
	v_add_f32_e32 v201, v201, v80
	s_add_i32 s5, s2, 4
	s_cmp_ge_u32 s5, 36
	s_cbranch_scc1 .Latt_drain_a1
	s_waitcnt vmcnt(4)
	s_branch .Latt_stage_a1

; #define LAS __attribute__((address_space(3)))
; __device__ __forceinline__ unsigned pk2(float lo, float hi) { f32x2_t v = {lo, hi}; bf16x2_t b = __builtin_convertvector(v, bf16x2_t); return __builtin_bit_cast(unsigned, b); }
; #define MFMA32(a, b, c) __builtin_amdgcn_mfma_f32_32x32x16_bf16((a), (b), (c), 0, 0, 0)
; __device__ __forceinline__ void attn_unit(const Frame& F, int layer, int qrow0, int ntiles, int b, int head, float lam, float m2, float lam_init) {
;     ...
;         if (t + 1 < ntiles) AT_QK(na, nb, (t + 1) & 1);
;         float ls = 0.f;
; #pragma unroll
;         for (int i = 0; i < 16; ++i) { sa[i] = __builtin_amdgcn_exp2f(sa[i]); sb[i] = __builtin_amdgcn_exp2f(sb[i]); ls += sa[i] + sb[i]; }
;         lsum += ls;
;         bf16x8 pk[4];
;         { u32x4 w0, w1, w2, w3;
; #pragma unroll
;           for (int i = 0; i < 4; ++i) { w0[i] = pk2(sa[2 * i], sa[2 * i + 1]); w1[i] = pk2(sa[8 + 2 * i], sa[9 + 2 * i]); w2[i] = pk2(sb[2 * i], sb[2 * i + 1]); w3[i] = pk2(sb[8 + 2 * i], sb[9 + 2 * i]); }
;           pk[0] = __builtin_bit_cast(bf16x8, w0); pk[1] = __builtin_bit_cast(bf16x8, w1); pk[2] = __builtin_bit_cast(bf16x8, w2); pk[3] = __builtin_bit_cast(bf16x8, w3); }
;         LAS const unsigned char* Vt = L + AT_V + (t & 1) * AT_VBYTES;
;         __builtin_amdgcn_sched_barrier(0);
;         bf16x8 vfa[4], vfb[4];
; #pragma unroll
;         for (int j = 0; j < 4; ++j) vfa[j] = frag_tr_acc(Vt, AT_VSTR, 0, 32 * j, lane);
; #pragma unroll
;         for (int ks = 0; ks < 4; ks += 2) {
; #pragma unroll
;             for (int j = 0; j < 4; ++j) vfb[j] = frag_tr_acc(Vt, AT_VSTR, 16 * (ks + 1), 32 * j, lane);
; #pragma unroll
;             for (int j = 0; j < 4; ++j) o[j] = MFMA32(pk[ks], vfa[j], o[j]);
;             __builtin_amdgcn_sched_barrier(0);
;             if (ks + 2 < 4) {
; #pragma unroll
;                 for (int j = 0; j < 4; ++j) vfa[j] = frag_tr_acc(Vt, AT_VSTR, 16 * (ks + 2), 32 * j, lane);
;             }
; #pragma unroll
;             for (int j = 0; j < 4; ++j) o[j] = MFMA32(pk[ks + 1], vfb[j], o[j]);
;             __builtin_amdgcn_sched_barrier(0);
;         }
;         if (t + 2 < ntiles) AT_STOREK(t & 1);
;         if (t + 1 < ntiles) AT_STOREV((t + 1) & 1);
.Latt_stage_a1:
	s_add_i32 s5, s2, 3
	s_cmp_ge_u32 s5, 36
	s_cbranch_scc1 .Latt_kscr_a1
	ds_write_b128 v144, v[234:237] offset:0
	ds_write_b128 v144, v[238:241] offset:8704
	s_branch .Latt_kdone_a1
.Latt_kscr_a1:
	ds_write_b128 v198, v[234:237]
	ds_write_b128 v198, v[238:241] offset:8704
.Latt_kdone_a1:
	s_add_i32 s5, s2, 2
	s_cmp_ge_u32 s5, 36
	s_cbranch_scc1 .Latt_vscr_a1
	ds_write_b128 v195, v[242:245] offset:34816
	ds_write_b128 v195, v[248:251] offset:45056
	s_branch .Latt_vdone_a1
.Latt_vscr_a1:
	ds_write_b128 v199, v[242:245] offset:34816
	ds_write_b128 v199, v[248:251] offset:45056
.Latt_vdone_a1:
	s_add_i32 s5, s2, 2
	s_cmp_ge_u32 s5, 36
	s_cbranch_scc1 .Latt_noqkw_a1
	ds_read_b128 v[128:131], v190 offset:0
	ds_read_b128 v[132:135], v190 offset:8704
	ds_read_b128 v[136:139], v190 offset:32
	ds_read_b128 v[140:143], v190 offset:8736
	s_waitcnt lgkmcnt(2)
	v_mfma_f32_32x32x16_bf16 v[80:95], v[128:131], v[158:161], v[64:79]
	v_mfma_f32_32x32x16_bf16 v[96:111], v[132:135], v[158:161], v[64:79]
	ds_read_b128 v[128:131], v190 offset:64
	ds_read_b128 v[132:135], v190 offset:8768
	s_waitcnt lgkmcnt(2)
	v_mfma_f32_32x32x16_bf16 v[80:95], v[136:139], v[154:157], v[80:95]
	v_mfma_f32_32x32x16_bf16 v[96:111], v[140:143], v[154:157], v[96:111]
	ds_read_b128 v[136:139], v190 offset:96
	ds_read_b128 v[140:143], v190 offset:8800
	s_waitcnt lgkmcnt(2)
	v_mfma_f32_32x32x16_bf16 v[80:95], v[128:131], v[150:153], v[80:95]
	v_mfma_f32_32x32x16_bf16 v[96:111], v[132:135], v[150:153], v[96:111]
	s_waitcnt lgkmcnt(0)
	v_mfma_f32_32x32x16_bf16 v[80:95], v[136:139], v[146:149], v[80:95]
	v_mfma_f32_32x32x16_bf16 v[96:111], v[140:143], v[146:149], v[96:111]
.Latt_noqk_a1:
	ds_read_b64_tr_b16 v[202:203], v191 offset:34816
	ds_read_b64_tr_b16 v[206:207], v191 offset:34880
	ds_read_b64_tr_b16 v[210:211], v191 offset:34944
	ds_read_b64_tr_b16 v[214:215], v191 offset:35008
	ds_read_b64_tr_b16 v[204:205], v191 offset:37376
	ds_read_b64_tr_b16 v[208:209], v191 offset:37440
	ds_read_b64_tr_b16 v[212:213], v191 offset:37504
	ds_read_b64_tr_b16 v[216:217], v191 offset:37568
	ds_read_b64_tr_b16 v[218:219], v191 offset:39936
	ds_read_b64_tr_b16 v[222:223], v191 offset:40000
	ds_read_b64_tr_b16 v[226:227], v191 offset:40064
	ds_read_b64_tr_b16 v[230:231], v191 offset:40128
	ds_read_b64_tr_b16 v[220:221], v191 offset:42496
	ds_read_b64_tr_b16 v[224:225], v191 offset:42560
	ds_read_b64_tr_b16 v[228:229], v191 offset:42624
	s_waitcnt lgkmcnt(14)
	ds_read_b64_tr_b16 v[232:233], v191 offset:42688
	s_waitcnt lgkmcnt(8)
	v_mfma_f32_32x32x16_bf16 v[32:47], v[112:115], v[202:205], v[32:47]
	v_mfma_f32_32x32x16_bf16 v[48:63], v[112:115], v[206:209], v[48:63]
	v_mfma_f32_32x32x16_bf16 v[0:15], v[112:115], v[210:213], v[0:15]
	v_mfma_f32_32x32x16_bf16 v[16:31], v[112:115], v[214:217], v[16:31]
	ds_read_b64_tr_b16 v[202:203], v191 offset:45056
	ds_read_b64_tr_b16 v[206:207], v191 offset:45120
	ds_read_b64_tr_b16 v[210:211], v191 offset:45184
	ds_read_b64_tr_b16 v[214:215], v191 offset:45248
	ds_read_b64_tr_b16 v[204:205], v191 offset:47616
	ds_read_b64_tr_b16 v[208:209], v191 offset:47680
	ds_read_b64_tr_b16 v[212:213], v191 offset:47744
	s_waitcnt lgkmcnt(14)
	ds_read_b64_tr_b16 v[216:217], v191 offset:47808
	s_waitcnt lgkmcnt(8)
	v_mfma_f32_32x32x16_bf16 v[32:47], v[116:119], v[218:221], v[32:47]
	v_mfma_f32_32x32x16_bf16 v[48:63], v[116:119], v[222:225], v[48:63]
	v_mfma_f32_32x32x16_bf16 v[0:15], v[116:119], v[226:229], v[0:15]
	v_mfma_f32_32x32x16_bf16 v[16:31], v[116:119], v[230:233], v[16:31]
	ds_read_b64_tr_b16 v[218:219], v191 offset:50176
	ds_read_b64_tr_b16 v[222:223], v191 offset:50240
	ds_read_b64_tr_b16 v[226:227], v191 offset:50304
	ds_read_b64_tr_b16 v[230:231], v191 offset:50368
	ds_read_b64_tr_b16 v[220:221], v191 offset:52736
	ds_read_b64_tr_b16 v[224:225], v191 offset:52800
	ds_read_b64_tr_b16 v[228:229], v191 offset:52864
	s_waitcnt lgkmcnt(14)
	ds_read_b64_tr_b16 v[232:233], v191 offset:52928
	s_waitcnt lgkmcnt(8)
	v_mfma_f32_32x32x16_bf16 v[32:47], v[120:123], v[202:205], v[32:47]
	v_mfma_f32_32x32x16_bf16 v[48:63], v[120:123], v[206:209], v[48:63]
	v_mfma_f32_32x32x16_bf16 v[0:15], v[120:123], v[210:213], v[0:15]
	v_mfma_f32_32x32x16_bf16 v[16:31], v[120:123], v[214:217], v[16:31]
	s_waitcnt lgkmcnt(0)
	v_mfma_f32_32x32x16_bf16 v[32:47], v[124:127], v[218:221], v[32:47]
	v_mfma_f32_32x32x16_bf16 v[48:63], v[124:127], v[222:225], v[48:63]
	v_mfma_f32_32x32x16_bf16 v[0:15], v[124:127], v[226:229], v[0:15]
	v_mfma_f32_32x32x16_bf16 v[16:31], v[124:127], v[230:233], v[16:31]
	s_barrier
	s_add_i32 s5, s2, 5
	s_cmp_ge_u32 s5, 36
	s_cbranch_scc1 .Latt_nokload_a2
	s_cmp_lt_u32 s5, 4
	s_cselect_b32 s15, s42, s43
	s_lshl_b32 s45, s5, 6
	s_add_i32 s15, s15, s45
	s_lshl_b32 s15, s15, 10
	v_add_u32_e32 v186, s15, v178
	v_add_u32_e32 v187, 0x8000, v186
	global_load_dwordx4 v[234:237], v186, s[72:73]
	global_load_dwordx4 v[238:241], v187, s[72:73]
; __device__ __forceinline__ unsigned pk2(float lo, float hi) { f32x2_t v = {lo, hi}; bf16x2_t b = __builtin_convertvector(v, bf16x2_t); return __builtin_bit_cast(unsigned, b); }
; #define AT_LOADK(t) do { const int kr_ = AT_KROW(t); _Pragma("unroll") for (int i_ = 0; i_ < 2; ++i_) kreg[i_] = *(const u32x4*)(Kp + (size_t)(kr_ + prow0 + 32 * i_) * 512 + pch * 8); } while (0)
; #define AT_LOADV(t) do { const int kr_ = AT_KROW(t); _Pragma("unroll") for (int i_ = 0; i_ < 2; ++i_) vreg[i_] = *(const u32x4*)(Vp + (size_t)(kr_ + prow0 + 32 * i_) * 512 + pch * 8); } while (0)
; __device__ __forceinline__ void attn_unit(const Frame& F, int layer, int qrow0, int ntiles, int b, int head, float lam, float m2, float lam_init) {
;     ...
;         if (t + 2 < ntiles) AT_LOADK(t + 2);
;         if (t + 1 < ntiles) AT_LOADV(t + 1);
;         if (t + 1 < ntiles) AT_QK(na, nb, (t + 1) & 1);
;         float ls = 0.f;
; #pragma unroll
;         for (int i = 0; i < 16; ++i) { sa[i] = __builtin_amdgcn_exp2f(sa[i]); sb[i] = __builtin_amdgcn_exp2f(sb[i]); ls += sa[i] + sb[i]; }
;         lsum += ls;
;         bf16x8 pk[4];
;         { u32x4 w0, w1, w2, w3;
; #pragma unroll
;           for (int i = 0; i < 4; ++i) { w0[i] = pk2(sa[2 * i], sa[2 * i + 1]); w1[i] = pk2(sa[8 + 2 * i], sa[9 + 2 * i]); w2[i] = pk2(sb[2 * i], sb[2 * i + 1]); w3[i] = pk2(sb[8 + 2 * i], sb[9 + 2 * i]); }
;           pk[0] = __builtin_bit_cast(bf16x8, w0); pk[1] = __builtin_bit_cast(bf16x8, w1); pk[2] = __builtin_bit_cast(bf16x8, w2); pk[3] = __builtin_bit_cast(bf16x8, w3); }
.Latt_nokload_a2:
	s_add_i32 s5, s2, 4
	s_cmp_ge_u32 s5, 36
	s_cbranch_scc1 .Latt_novload_a2
	s_cmp_lt_u32 s5, 4
	s_cselect_b32 s15, s42, s43
	s_lshl_b32 s45, s5, 6
	s_add_i32 s15, s15, s45
	s_lshl_b32 s15, s15, 10
	v_add_u32_e32 v188, s15, v178
	v_add_u32_e32 v189, 0x8000, v188
	global_load_dwordx4 v[242:245], v188, s[74:75]
	global_load_dwordx4 v[248:251], v189, s[74:75]
.Latt_novload_a2:
	v_exp_f32_e32 v80, v80
	v_exp_f32_e32 v96, v96
	v_exp_f32_e32 v81, v81
	v_exp_f32_e32 v97, v97
	v_exp_f32_e32 v82, v82
	v_exp_f32_e32 v98, v98
	v_exp_f32_e32 v83, v83
	v_exp_f32_e32 v99, v99
	v_exp_f32_e32 v84, v84
	v_exp_f32_e32 v100, v100
	v_exp_f32_e32 v85, v85
	v_exp_f32_e32 v101, v101
	v_exp_f32_e32 v86, v86
	v_exp_f32_e32 v102, v102
	v_exp_f32_e32 v87, v87
	v_exp_f32_e32 v103, v103
	v_exp_f32_e32 v88, v88
	v_exp_f32_e32 v104, v104
	v_exp_f32_e32 v89, v89
	v_exp_f32_e32 v105, v105
	v_exp_f32_e32 v90, v90
	v_exp_f32_e32 v106, v106
	v_exp_f32_e32 v91, v91
	v_exp_f32_e32 v107, v107
	v_exp_f32_e32 v92, v92
	v_exp_f32_e32 v108, v108
	v_exp_f32_e32 v93, v93
	v_exp_f32_e32 v109, v109
	v_exp_f32_e32 v94, v94
	v_exp_f32_e32 v110, v110
	v_exp_f32_e32 v95, v95
	v_exp_f32_e32 v111, v111
	v_cvt_pk_bf16_f32 v112, v80, v81
	v_cvt_pk_bf16_f32 v113, v82, v83
	v_cvt_pk_bf16_f32 v114, v84, v85
	v_cvt_pk_bf16_f32 v115, v86, v87
	v_cvt_pk_bf16_f32 v116, v88, v89
	v_cvt_pk_bf16_f32 v117, v90, v91
	v_cvt_pk_bf16_f32 v118, v92, v93
	v_cvt_pk_bf16_f32 v119, v94, v95
	v_cvt_pk_bf16_f32 v120, v96, v97
	v_cvt_pk_bf16_f32 v121, v98, v99
	v_cvt_pk_bf16_f32 v122, v100, v101
	v_cvt_pk_bf16_f32 v123, v102, v103
	v_cvt_pk_bf16_f32 v124, v104, v105
	v_cvt_pk_bf16_f32 v125, v106, v107
	v_cvt_pk_bf16_f32 v126, v108, v109
	v_cvt_pk_bf16_f32 v127, v110, v111
	v_add_f32_e32 v80, v80, v96
	v_add_f32_e32 v81, v81, v97
	v_add_f32_e32 v82, v82, v98
	v_add_f32_e32 v83, v83, v99
	v_add_f32_e32 v84, v84, v100
	v_add_f32_e32 v85, v85, v101
	v_add_f32_e32 v86, v86, v102
	v_add_f32_e32 v87, v87, v103
	v_add_f32_e32 v88, v88, v104
	v_add_f32_e32 v89, v89, v105
	v_add_f32_e32 v90, v90, v106
	v_add_f32_e32 v91, v91, v107
	v_add_f32_e32 v92, v92, v108
	v_add_f32_e32 v93, v93, v109
	v_add_f32_e32 v94, v94, v110
	v_add_f32_e32 v95, v95, v111
	v_add_f32_e32 v80, v80, v88
	v_add_f32_e32 v81, v81, v89
	v_add_f32_e32 v82, v82, v90
	v_add_f32_e32 v83, v83, v91
	v_add_f32_e32 v84, v84, v92
	v_add_f32_e32 v85, v85, v93
	v_add_f32_e32 v86, v86, v94
	v_add_f32_e32 v87, v87, v95
	v_add_f32_e32 v80, v80, v84
	v_add_f32_e32 v81, v81, v85
	v_add_f32_e32 v82, v82, v86
	v_add_f32_e32 v83, v83, v87
	v_add_f32_e32 v80, v80, v82
	v_add_f32_e32 v81, v81, v83
	v_add_f32_e32 v80, v80, v81
	v_add_f32_e32 v201, v201, v80
	s_add_i32 s5, s2, 5
	s_cmp_ge_u32 s5, 36
	s_cbranch_scc1 .Latt_drain_a2
	s_waitcnt vmcnt(4)
	s_branch .Latt_stage_a2

; #define AT_STOREK(st) do { _Pragma("unroll") for (int i_ = 0; i_ < 2; ++i_) *(LAS u32x4*)(L + AT_K + (st) * AT_KBYTES + (prow0 + 32 * i_) * AT_KSTR + pch * 16) = kreg[i_]; } while (0)
; #define AT_STOREV(st) do { _Pragma("unroll") for (int i_ = 0; i_ < 2; ++i_) *(LAS u32x4*)(L + AT_V + (st) * AT_VBYTES + (prow0 + 32 * i_) * AT_VSTR + pch * 16) = vreg[i_]; } while (0)
; __device__ __forceinline__ void attn_unit(const Frame& F, int layer, int qrow0, int ntiles, int b, int head, float lam, float m2, float lam_init) {
;     ...
;         if (t + 2 < ntiles) AT_STOREK(t & 1);
;         if (t + 1 < ntiles) AT_STOREV((t + 1) & 1);
.Latt_stage_a2:
	s_add_i32 s5, s2, 4
	s_cmp_ge_u32 s5, 36
	s_cbranch_scc1 .Latt_kscr_a2
	ds_write_b128 v144, v[162:165] offset:17408
	ds_write_b128 v144, v[166:169] offset:26112
	s_branch .Latt_kdone_a2

; #define AT_STOREK(st) do { _Pragma("unroll") for (int i_ = 0; i_ < 2; ++i_) *(LAS u32x4*)(L + AT_K + (st) * AT_KBYTES + (prow0 + 32 * i_) * AT_KSTR + pch * 16) = kreg[i_]; } while (0)
; #define AT_STOREV(st) do { _Pragma("unroll") for (int i_ = 0; i_ < 2; ++i_) *(LAS u32x4*)(L + AT_V + (st) * AT_VBYTES + (prow0 + 32 * i_) * AT_VSTR + pch * 16) = vreg[i_]; } while (0)
; __device__ __forceinline__ void attn_unit(const Frame& F, int layer, int qrow0, int ntiles, int b, int head, float lam, float m2, float lam_init) {
;     ...
;         if (t + 2 < ntiles) AT_STOREK(t & 1);
;         if (t + 1 < ntiles) AT_STOREV((t + 1) & 1);
.Latt_kdone_a2:
	s_add_i32 s5, s2, 3
	s_cmp_ge_u32 s5, 36
	s_cbranch_scc1 .Latt_vscr_a2
	ds_write_b128 v194, v[170:173] offset:34816
	ds_write_b128 v194, v[174:177] offset:45056
	s_branch .Latt_vdone_a2

; #define LAS __attribute__((address_space(3)))
; __device__ __forceinline__ unsigned pk2(float lo, float hi) { f32x2_t v = {lo, hi}; bf16x2_t b = __builtin_convertvector(v, bf16x2_t); return __builtin_bit_cast(unsigned, b); }
; #define MFMA32(a, b, c) __builtin_amdgcn_mfma_f32_32x32x16_bf16((a), (b), (c), 0, 0, 0)
; __device__ __forceinline__ void attn_unit(const Frame& F, int layer, int qrow0, int ntiles, int b, int head, float lam, float m2, float lam_init) {
;     ...
;         if (t + 1 < ntiles) AT_QK(na, nb, (t + 1) & 1);
;         float ls = 0.f;
; #pragma unroll
;         for (int i = 0; i < 16; ++i) { sa[i] = __builtin_amdgcn_exp2f(sa[i]); sb[i] = __builtin_amdgcn_exp2f(sb[i]); ls += sa[i] + sb[i]; }
;         lsum += ls;
;         bf16x8 pk[4];
;         { u32x4 w0, w1, w2, w3;
; #pragma unroll
;           for (int i = 0; i < 4; ++i) { w0[i] = pk2(sa[2 * i], sa[2 * i + 1]); w1[i] = pk2(sa[8 + 2 * i], sa[9 + 2 * i]); w2[i] = pk2(sb[2 * i], sb[2 * i + 1]); w3[i] = pk2(sb[8 + 2 * i], sb[9 + 2 * i]); }
;           pk[0] = __builtin_bit_cast(bf16x8, w0); pk[1] = __builtin_bit_cast(bf16x8, w1); pk[2] = __builtin_bit_cast(bf16x8, w2); pk[3] = __builtin_bit_cast(bf16x8, w3); }
;         LAS const unsigned char* Vt = L + AT_V + (t & 1) * AT_VBYTES;
;         __builtin_amdgcn_sched_barrier(0);
;         bf16x8 vfa[4], vfb[4];
; #pragma unroll
;         for (int j = 0; j < 4; ++j) vfa[j] = frag_tr_acc(Vt, AT_VSTR, 0, 32 * j, lane);
; #pragma unroll
;         for (int ks = 0; ks < 4; ks += 2) {
; #pragma unroll
;             for (int j = 0; j < 4; ++j) vfb[j] = frag_tr_acc(Vt, AT_VSTR, 16 * (ks + 1), 32 * j, lane);
; #pragma unroll
;             for (int j = 0; j < 4; ++j) o[j] = MFMA32(pk[ks], vfa[j], o[j]);
;             __builtin_amdgcn_sched_barrier(0);
;             if (ks + 2 < 4) {
; #pragma unroll
;                 for (int j = 0; j < 4; ++j) vfa[j] = frag_tr_acc(Vt, AT_VSTR, 16 * (ks + 2), 32 * j, lane);
;             }
; #pragma unroll
;             for (int j = 0; j < 4; ++j) o[j] = MFMA32(pk[ks + 1], vfb[j], o[j]);
;             __builtin_amdgcn_sched_barrier(0);
;         }
.Latt_vdone_a2:
	s_add_i32 s5, s2, 3
	s_cmp_ge_u32 s5, 36
	s_cbranch_scc1 .Latt_noqkw_a2
	ds_read_b128 v[128:131], v197 offset:0
	ds_read_b128 v[132:135], v197 offset:8704
	ds_read_b128 v[136:139], v197 offset:32
	ds_read_b128 v[140:143], v197 offset:8736
	s_waitcnt lgkmcnt(2)
	v_mfma_f32_32x32x16_bf16 v[80:95], v[128:131], v[158:161], v[64:79]
	v_mfma_f32_32x32x16_bf16 v[96:111], v[132:135], v[158:161], v[64:79]
	ds_read_b128 v[128:131], v197 offset:64
	ds_read_b128 v[132:135], v197 offset:8768
	s_waitcnt lgkmcnt(2)
	v_mfma_f32_32x32x16_bf16 v[80:95], v[136:139], v[154:157], v[80:95]
	v_mfma_f32_32x32x16_bf16 v[96:111], v[140:143], v[154:157], v[96:111]
	ds_read_b128 v[136:139], v197 offset:96
	ds_read_b128 v[140:143], v197 offset:8800
	s_waitcnt lgkmcnt(2)
	v_mfma_f32_32x32x16_bf16 v[80:95], v[128:131], v[150:153], v[80:95]
	v_mfma_f32_32x32x16_bf16 v[96:111], v[132:135], v[150:153], v[96:111]
	s_waitcnt lgkmcnt(0)
	v_mfma_f32_32x32x16_bf16 v[80:95], v[136:139], v[146:149], v[80:95]
	v_mfma_f32_32x32x16_bf16 v[96:111], v[140:143], v[146:149], v[96:111]
.Latt_noqk_a2:
	ds_read_b64_tr_b16 v[202:203], v184 offset:34816
	ds_read_b64_tr_b16 v[206:207], v184 offset:34880
	ds_read_b64_tr_b16 v[210:211], v184 offset:34944
	ds_read_b64_tr_b16 v[214:215], v184 offset:35008
	ds_read_b64_tr_b16 v[204:205], v184 offset:37376
	ds_read_b64_tr_b16 v[208:209], v184 offset:37440
	ds_read_b64_tr_b16 v[212:213], v184 offset:37504
	ds_read_b64_tr_b16 v[216:217], v184 offset:37568
	ds_read_b64_tr_b16 v[218:219], v184 offset:39936
	ds_read_b64_tr_b16 v[222:223], v184 offset:40000
	ds_read_b64_tr_b16 v[226:227], v184 offset:40064
	ds_read_b64_tr_b16 v[230:231], v184 offset:40128
	ds_read_b64_tr_b16 v[220:221], v184 offset:42496
	ds_read_b64_tr_b16 v[224:225], v184 offset:42560
	ds_read_b64_tr_b16 v[228:229], v184 offset:42624
	s_waitcnt lgkmcnt(14)
	ds_read_b64_tr_b16 v[232:233], v184 offset:42688
	s_waitcnt lgkmcnt(8)
	v_mfma_f32_32x32x16_bf16 v[32:47], v[112:115], v[202:205], v[32:47]
	v_mfma_f32_32x32x16_bf16 v[48:63], v[112:115], v[206:209], v[48:63]
	v_mfma_f32_32x32x16_bf16 v[0:15], v[112:115], v[210:213], v[0:15]
	v_mfma_f32_32x32x16_bf16 v[16:31], v[112:115], v[214:217], v[16:31]
	ds_read_b64_tr_b16 v[202:203], v184 offset:45056
	ds_read_b64_tr_b16 v[206:207], v184 offset:45120
	ds_read_b64_tr_b16 v[210:211], v184 offset:45184
	ds_read_b64_tr_b16 v[214:215], v184 offset:45248
	ds_read_b64_tr_b16 v[204:205], v184 offset:47616
	ds_read_b64_tr_b16 v[208:209], v184 offset:47680
	ds_read_b64_tr_b16 v[212:213], v184 offset:47744
	s_waitcnt lgkmcnt(14)
	ds_read_b64_tr_b16 v[216:217], v184 offset:47808
	s_waitcnt lgkmcnt(8)
	v_mfma_f32_32x32x16_bf16 v[32:47], v[116:119], v[218:221], v[32:47]
	v_mfma_f32_32x32x16_bf16 v[48:63], v[116:119], v[222:225], v[48:63]
	v_mfma_f32_32x32x16_bf16 v[0:15], v[116:119], v[226:229], v[0:15]
	v_mfma_f32_32x32x16_bf16 v[16:31], v[116:119], v[230:233], v[16:31]
	ds_read_b64_tr_b16 v[218:219], v184 offset:50176
	ds_read_b64_tr_b16 v[222:223], v184 offset:50240
	ds_read_b64_tr_b16 v[226:227], v184 offset:50304
	ds_read_b64_tr_b16 v[230:231], v184 offset:50368
	ds_read_b64_tr_b16 v[220:221], v184 offset:52736
	ds_read_b64_tr_b16 v[224:225], v184 offset:52800
	ds_read_b64_tr_b16 v[228:229], v184 offset:52864
	s_waitcnt lgkmcnt(14)
	ds_read_b64_tr_b16 v[232:233], v184 offset:52928
	s_waitcnt lgkmcnt(8)
	v_mfma_f32_32x32x16_bf16 v[32:47], v[120:123], v[202:205], v[32:47]
	v_mfma_f32_32x32x16_bf16 v[48:63], v[120:123], v[206:209], v[48:63]
	v_mfma_f32_32x32x16_bf16 v[0:15], v[120:123], v[210:213], v[0:15]
	v_mfma_f32_32x32x16_bf16 v[16:31], v[120:123], v[214:217], v[16:31]
	s_waitcnt lgkmcnt(0)
	v_mfma_f32_32x32x16_bf16 v[32:47], v[124:127], v[218:221], v[32:47]
	v_mfma_f32_32x32x16_bf16 v[48:63], v[124:127], v[222:225], v[48:63]
	v_mfma_f32_32x32x16_bf16 v[0:15], v[124:127], v[226:229], v[0:15]
	v_mfma_f32_32x32x16_bf16 v[16:31], v[124:127], v[230:233], v[16:31]
	s_barrier
	s_add_i32 s5, s2, 6
	s_cmp_ge_u32 s5, 36
	s_cbranch_scc1 .Latt_nokload_a3
	s_cmp_lt_u32 s5, 4
	s_cselect_b32 s15, s42, s43
	s_lshl_b32 s45, s5, 6
	s_add_i32 s15, s15, s45
	s_lshl_b32 s15, s15, 10
	v_add_u32_e32 v186, s15, v178
	v_add_u32_e32 v187, 0x8000, v186
	global_load_dwordx4 v[162:165], v186, s[72:73]
	global_load_dwordx4 v[166:169], v187, s[72:73]
; __device__ __forceinline__ unsigned pk2(float lo, float hi) { f32x2_t v = {lo, hi}; bf16x2_t b = __builtin_convertvector(v, bf16x2_t); return __builtin_bit_cast(unsigned, b); }
; #define AT_LOADK(t) do { const int kr_ = AT_KROW(t); _Pragma("unroll") for (int i_ = 0; i_ < 2; ++i_) kreg[i_] = *(const u32x4*)(Kp + (size_t)(kr_ + prow0 + 32 * i_) * 512 + pch * 8); } while (0)
; #define AT_LOADV(t) do { const int kr_ = AT_KROW(t); _Pragma("unroll") for (int i_ = 0; i_ < 2; ++i_) vreg[i_] = *(const u32x4*)(Vp + (size_t)(kr_ + prow0 + 32 * i_) * 512 + pch * 8); } while (0)
; __device__ __forceinline__ void attn_unit(const Frame& F, int layer, int qrow0, int ntiles, int b, int head, float lam, float m2, float lam_init) {
;     ...
;         if (t + 2 < ntiles) AT_LOADK(t + 2);
;         if (t + 1 < ntiles) AT_LOADV(t + 1);
;         if (t + 1 < ntiles) AT_QK(na, nb, (t + 1) & 1);
;         float ls = 0.f;
; #pragma unroll
;         for (int i = 0; i < 16; ++i) { sa[i] = __builtin_amdgcn_exp2f(sa[i]); sb[i] = __builtin_amdgcn_exp2f(sb[i]); ls += sa[i] + sb[i]; }
;         lsum += ls;
;         bf16x8 pk[4];
;         { u32x4 w0, w1, w2, w3;
; #pragma unroll
;           for (int i = 0; i < 4; ++i) { w0[i] = pk2(sa[2 * i], sa[2 * i + 1]); w1[i] = pk2(sa[8 + 2 * i], sa[9 + 2 * i]); w2[i] = pk2(sb[2 * i], sb[2 * i + 1]); w3[i] = pk2(sb[8 + 2 * i], sb[9 + 2 * i]); }
;           pk[0] = __builtin_bit_cast(bf16x8, w0); pk[1] = __builtin_bit_cast(bf16x8, w1); pk[2] = __builtin_bit_cast(bf16x8, w2); pk[3] = __builtin_bit_cast(bf16x8, w3); }
.Latt_nokload_a3:
	s_add_i32 s5, s2, 5
	s_cmp_ge_u32 s5, 36
	s_cbranch_scc1 .Latt_novload_a3
	s_cmp_lt_u32 s5, 4
	s_cselect_b32 s15, s42, s43
	s_lshl_b32 s45, s5, 6
	s_add_i32 s15, s15, s45
	s_lshl_b32 s15, s15, 10
	v_add_u32_e32 v188, s15, v178
	v_add_u32_e32 v189, 0x8000, v188
	global_load_dwordx4 v[170:173], v188, s[74:75]
	global_load_dwordx4 v[174:177], v189, s[74:75]
.Latt_novload_a3:
	v_exp_f32_e32 v80, v80
	v_exp_f32_e32 v96, v96
	v_exp_f32_e32 v81, v81
	v_exp_f32_e32 v97, v97
	v_exp_f32_e32 v82, v82
	v_exp_f32_e32 v98, v98
	v_exp_f32_e32 v83, v83
	v_exp_f32_e32 v99, v99
	v_exp_f32_e32 v84, v84
	v_exp_f32_e32 v100, v100
	v_exp_f32_e32 v85, v85
	v_exp_f32_e32 v101, v101
	v_exp_f32_e32 v86, v86
	v_exp_f32_e32 v102, v102
	v_exp_f32_e32 v87, v87
	v_exp_f32_e32 v103, v103
	v_exp_f32_e32 v88, v88
	v_exp_f32_e32 v104, v104
	v_exp_f32_e32 v89, v89
	v_exp_f32_e32 v105, v105
	v_exp_f32_e32 v90, v90
	v_exp_f32_e32 v106, v106
	v_exp_f32_e32 v91, v91
	v_exp_f32_e32 v107, v107
	v_exp_f32_e32 v92, v92
	v_exp_f32_e32 v108, v108
	v_exp_f32_e32 v93, v93
	v_exp_f32_e32 v109, v109
	v_exp_f32_e32 v94, v94
	v_exp_f32_e32 v110, v110
	v_exp_f32_e32 v95, v95
	v_exp_f32_e32 v111, v111
	v_cvt_pk_bf16_f32 v112, v80, v81
	v_cvt_pk_bf16_f32 v113, v82, v83
	v_cvt_pk_bf16_f32 v114, v84, v85
	v_cvt_pk_bf16_f32 v115, v86, v87
	v_cvt_pk_bf16_f32 v116, v88, v89
	v_cvt_pk_bf16_f32 v117, v90, v91
	v_cvt_pk_bf16_f32 v118, v92, v93
	v_cvt_pk_bf16_f32 v119, v94, v95
	v_cvt_pk_bf16_f32 v120, v96, v97
	v_cvt_pk_bf16_f32 v121, v98, v99
	v_cvt_pk_bf16_f32 v122, v100, v101
	v_cvt_pk_bf16_f32 v123, v102, v103
	v_cvt_pk_bf16_f32 v124, v104, v105
	v_cvt_pk_bf16_f32 v125, v106, v107
	v_cvt_pk_bf16_f32 v126, v108, v109
	v_cvt_pk_bf16_f32 v127, v110, v111
	v_add_f32_e32 v80, v80, v96
	v_add_f32_e32 v81, v81, v97
	v_add_f32_e32 v82, v82, v98
	v_add_f32_e32 v83, v83, v99
	v_add_f32_e32 v84, v84, v100
	v_add_f32_e32 v85, v85, v101
	v_add_f32_e32 v86, v86, v102
	v_add_f32_e32 v87, v87, v103
	v_add_f32_e32 v88, v88, v104
	v_add_f32_e32 v89, v89, v105
	v_add_f32_e32 v90, v90, v106
	v_add_f32_e32 v91, v91, v107
	v_add_f32_e32 v92, v92, v108
	v_add_f32_e32 v93, v93, v109
	v_add_f32_e32 v94, v94, v110
	v_add_f32_e32 v95, v95, v111
	v_add_f32_e32 v80, v80, v88
	v_add_f32_e32 v81, v81, v89
	v_add_f32_e32 v82, v82, v90
	v_add_f32_e32 v83, v83, v91
	v_add_f32_e32 v84, v84, v92
	v_add_f32_e32 v85, v85, v93
	v_add_f32_e32 v86, v86, v94
	v_add_f32_e32 v87, v87, v95
	v_add_f32_e32 v80, v80, v84
	v_add_f32_e32 v81, v81, v85
	v_add_f32_e32 v82, v82, v86
	v_add_f32_e32 v83, v83, v87
	v_add_f32_e32 v80, v80, v82
	v_add_f32_e32 v81, v81, v83
	v_add_f32_e32 v80, v80, v81
	v_add_f32_e32 v201, v201, v80
	s_add_i32 s5, s2, 6
	s_cmp_ge_u32 s5, 36
	s_cbranch_scc1 .Latt_drain_a3
	s_waitcnt vmcnt(4)
	s_branch .Latt_stage_a3

; #define AT_STOREK(st) do { _Pragma("unroll") for (int i_ = 0; i_ < 2; ++i_) *(LAS u32x4*)(L + AT_K + (st) * AT_KBYTES + (prow0 + 32 * i_) * AT_KSTR + pch * 16) = kreg[i_]; } while (0)
; #define AT_STOREV(st) do { _Pragma("unroll") for (int i_ = 0; i_ < 2; ++i_) *(LAS u32x4*)(L + AT_V + (st) * AT_VBYTES + (prow0 + 32 * i_) * AT_VSTR + pch * 16) = vreg[i_]; } while (0)
; __device__ __forceinline__ void attn_unit(const Frame& F, int layer, int qrow0, int ntiles, int b, int head, float lam, float m2, float lam_init) {
;     ...
;         if (t + 2 < ntiles) AT_STOREK(t & 1);
;         if (t + 1 < ntiles) AT_STOREV((t + 1) & 1);
.Latt_stage_a3:
	s_add_i32 s5, s2, 5
	s_cmp_ge_u32 s5, 36
	s_cbranch_scc1 .Latt_kscr_a3
	ds_write_b128 v179, v[234:237] offset:0
	ds_write_b128 v179, v[238:241] offset:8704
	s_branch .Latt_kdone_a3

; #define AT_STOREK(st) do { _Pragma("unroll") for (int i_ = 0; i_ < 2; ++i_) *(LAS u32x4*)(L + AT_K + (st) * AT_KBYTES + (prow0 + 32 * i_) * AT_KSTR + pch * 16) = kreg[i_]; } while (0)
; #define AT_STOREV(st) do { _Pragma("unroll") for (int i_ = 0; i_ < 2; ++i_) *(LAS u32x4*)(L + AT_V + (st) * AT_VBYTES + (prow0 + 32 * i_) * AT_VSTR + pch * 16) = vreg[i_]; } while (0)
; __device__ __forceinline__ void attn_unit(const Frame& F, int layer, int qrow0, int ntiles, int b, int head, float lam, float m2, float lam_init) {
;     ...
;         if (t + 2 < ntiles) AT_STOREK(t & 1);
;         if (t + 1 < ntiles) AT_STOREV((t + 1) & 1);
.Latt_kdone_a3:
	s_add_i32 s5, s2, 4
	s_cmp_ge_u32 s5, 36
	s_cbranch_scc1 .Latt_vscr_a3
	ds_write_b128 v185, v[242:245] offset:34816
	ds_write_b128 v185, v[248:251] offset:45056
	s_branch .Latt_vdone_a3

; #define LAS __attribute__((address_space(3)))
; __device__ __forceinline__ unsigned pk2(float lo, float hi) { f32x2_t v = {lo, hi}; bf16x2_t b = __builtin_convertvector(v, bf16x2_t); return __builtin_bit_cast(unsigned, b); }
; #define MFMA32(a, b, c) __builtin_amdgcn_mfma_f32_32x32x16_bf16((a), (b), (c), 0, 0, 0)
; __device__ __forceinline__ void attn_unit(const Frame& F, int layer, int qrow0, int ntiles, int b, int head, float lam, float m2, float lam_init) {
;     ...
;         if (t + 1 < ntiles) AT_QK(na, nb, (t + 1) & 1);
;         float ls = 0.f;
; #pragma unroll
;         for (int i = 0; i < 16; ++i) { sa[i] = __builtin_amdgcn_exp2f(sa[i]); sb[i] = __builtin_amdgcn_exp2f(sb[i]); ls += sa[i] + sb[i]; }
;         lsum += ls;
;         bf16x8 pk[4];
;         { u32x4 w0, w1, w2, w3;
; #pragma unroll
;           for (int i = 0; i < 4; ++i) { w0[i] = pk2(sa[2 * i], sa[2 * i + 1]); w1[i] = pk2(sa[8 + 2 * i], sa[9 + 2 * i]); w2[i] = pk2(sb[2 * i], sb[2 * i + 1]); w3[i] = pk2(sb[8 + 2 * i], sb[9 + 2 * i]); }
;           pk[0] = __builtin_bit_cast(bf16x8, w0); pk[1] = __builtin_bit_cast(bf16x8, w1); pk[2] = __builtin_bit_cast(bf16x8, w2); pk[3] = __builtin_bit_cast(bf16x8, w3); }
;         LAS const unsigned char* Vt = L + AT_V + (t & 1) * AT_VBYTES;
;         __builtin_amdgcn_sched_barrier(0);
;         bf16x8 vfa[4], vfb[4];
; #pragma unroll
;         for (int j = 0; j < 4; ++j) vfa[j] = frag_tr_acc(Vt, AT_VSTR, 0, 32 * j, lane);
; #pragma unroll
;         for (int ks = 0; ks < 4; ks += 2) {
; #pragma unroll
;             for (int j = 0; j < 4; ++j) vfb[j] = frag_tr_acc(Vt, AT_VSTR, 16 * (ks + 1), 32 * j, lane);
; #pragma unroll
;             for (int j = 0; j < 4; ++j) o[j] = MFMA32(pk[ks], vfa[j], o[j]);
;             __builtin_amdgcn_sched_barrier(0);
;             if (ks + 2 < 4) {
; #pragma unroll
;                 for (int j = 0; j < 4; ++j) vfa[j] = frag_tr_acc(Vt, AT_VSTR, 16 * (ks + 2), 32 * j, lane);
;             }
; #pragma unroll
;             for (int j = 0; j < 4; ++j) o[j] = MFMA32(pk[ks + 1], vfb[j], o[j]);
;             __builtin_amdgcn_sched_barrier(0);
;         }
.Latt_vdone_a3:
	s_add_i32 s5, s2, 4
	s_cmp_ge_u32 s5, 36
	s_cbranch_scc1 .Latt_noqkw_a3
	ds_read_b128 v[128:131], v197 offset:17408
	ds_read_b128 v[132:135], v197 offset:26112
	ds_read_b128 v[136:139], v197 offset:17440
	ds_read_b128 v[140:143], v197 offset:26144
	s_waitcnt lgkmcnt(2)
	v_mfma_f32_32x32x16_bf16 v[80:95], v[128:131], v[158:161], v[64:79]
	v_mfma_f32_32x32x16_bf16 v[96:111], v[132:135], v[158:161], v[64:79]
	ds_read_b128 v[128:131], v197 offset:17472
	ds_read_b128 v[132:135], v197 offset:26176
	s_waitcnt lgkmcnt(2)
	v_mfma_f32_32x32x16_bf16 v[80:95], v[136:139], v[154:157], v[80:95]
	v_mfma_f32_32x32x16_bf16 v[96:111], v[140:143], v[154:157], v[96:111]
	ds_read_b128 v[136:139], v197 offset:17504
	ds_read_b128 v[140:143], v197 offset:26208
	s_waitcnt lgkmcnt(2)
	v_mfma_f32_32x32x16_bf16 v[80:95], v[128:131], v[150:153], v[80:95]
	v_mfma_f32_32x32x16_bf16 v[96:111], v[132:135], v[150:153], v[96:111]
	s_waitcnt lgkmcnt(0)
	v_mfma_f32_32x32x16_bf16 v[80:95], v[136:139], v[146:149], v[80:95]
	v_mfma_f32_32x32x16_bf16 v[96:111], v[140:143], v[146:149], v[96:111]
.Latt_noqk_a3:
	ds_read_b64_tr_b16 v[202:203], v196 offset:34816
	ds_read_b64_tr_b16 v[206:207], v196 offset:34880
	ds_read_b64_tr_b16 v[210:211], v196 offset:34944
	ds_read_b64_tr_b16 v[214:215], v196 offset:35008
	ds_read_b64_tr_b16 v[204:205], v196 offset:37376
	ds_read_b64_tr_b16 v[208:209], v196 offset:37440
	ds_read_b64_tr_b16 v[212:213], v196 offset:37504
	ds_read_b64_tr_b16 v[216:217], v196 offset:37568
	ds_read_b64_tr_b16 v[218:219], v196 offset:39936
	ds_read_b64_tr_b16 v[222:223], v196 offset:40000
	ds_read_b64_tr_b16 v[226:227], v196 offset:40064
	ds_read_b64_tr_b16 v[230:231], v196 offset:40128
	ds_read_b64_tr_b16 v[220:221], v196 offset:42496
	ds_read_b64_tr_b16 v[224:225], v196 offset:42560
	ds_read_b64_tr_b16 v[228:229], v196 offset:42624
	s_waitcnt lgkmcnt(14)
	ds_read_b64_tr_b16 v[232:233], v196 offset:42688
	s_waitcnt lgkmcnt(8)
	v_mfma_f32_32x32x16_bf16 v[32:47], v[112:115], v[202:205], v[32:47]
	v_mfma_f32_32x32x16_bf16 v[48:63], v[112:115], v[206:209], v[48:63]
	v_mfma_f32_32x32x16_bf16 v[0:15], v[112:115], v[210:213], v[0:15]
	v_mfma_f32_32x32x16_bf16 v[16:31], v[112:115], v[214:217], v[16:31]
	ds_read_b64_tr_b16 v[202:203], v196 offset:45056
	ds_read_b64_tr_b16 v[206:207], v196 offset:45120
	ds_read_b64_tr_b16 v[210:211], v196 offset:45184
	ds_read_b64_tr_b16 v[214:215], v196 offset:45248
	ds_read_b64_tr_b16 v[204:205], v196 offset:47616
	ds_read_b64_tr_b16 v[208:209], v196 offset:47680
	ds_read_b64_tr_b16 v[212:213], v196 offset:47744
	s_waitcnt lgkmcnt(14)
	ds_read_b64_tr_b16 v[216:217], v196 offset:47808
	s_waitcnt lgkmcnt(8)
	v_mfma_f32_32x32x16_bf16 v[32:47], v[116:119], v[218:221], v[32:47]
	v_mfma_f32_32x32x16_bf16 v[48:63], v[116:119], v[222:225], v[48:63]
	v_mfma_f32_32x32x16_bf16 v[0:15], v[116:119], v[226:229], v[0:15]
	v_mfma_f32_32x32x16_bf16 v[16:31], v[116:119], v[230:233], v[16:31]
	ds_read_b64_tr_b16 v[218:219], v196 offset:50176
	ds_read_b64_tr_b16 v[222:223], v196 offset:50240
	ds_read_b64_tr_b16 v[226:227], v196 offset:50304
	ds_read_b64_tr_b16 v[230:231], v196 offset:50368
	ds_read_b64_tr_b16 v[220:221], v196 offset:52736
	ds_read_b64_tr_b16 v[224:225], v196 offset:52800
	ds_read_b64_tr_b16 v[228:229], v196 offset:52864
	s_waitcnt lgkmcnt(14)
	ds_read_b64_tr_b16 v[232:233], v196 offset:52928
	s_waitcnt lgkmcnt(8)
	v_mfma_f32_32x32x16_bf16 v[32:47], v[120:123], v[202:205], v[32:47]
	v_mfma_f32_32x32x16_bf16 v[48:63], v[120:123], v[206:209], v[48:63]
	v_mfma_f32_32x32x16_bf16 v[0:15], v[120:123], v[210:213], v[0:15]
	v_mfma_f32_32x32x16_bf16 v[16:31], v[120:123], v[214:217], v[16:31]
	s_waitcnt lgkmcnt(0)
	v_mfma_f32_32x32x16_bf16 v[32:47], v[124:127], v[218:221], v[32:47]
	v_mfma_f32_32x32x16_bf16 v[48:63], v[124:127], v[222:225], v[48:63]
	v_mfma_f32_32x32x16_bf16 v[0:15], v[124:127], v[226:229], v[0:15]
	v_mfma_f32_32x32x16_bf16 v[16:31], v[124:127], v[230:233], v[16:31]
	s_barrier
	s_add_i32 s5, s2, 7
	s_cmp_ge_u32 s5, 36
	s_cbranch_scc1 .Latt_nokload_a4
	s_cmp_lt_u32 s5, 4
	s_cselect_b32 s15, s42, s43
	s_lshl_b32 s45, s5, 6
	s_add_i32 s15, s15, s45
	s_lshl_b32 s15, s15, 10
	v_add_u32_e32 v186, s15, v178
	v_add_u32_e32 v187, 0x8000, v186
	global_load_dwordx4 v[234:237], v186, s[72:73]
	global_load_dwordx4 v[238:241], v187, s[72:73]
; __device__ __forceinline__ unsigned pk2(float lo, float hi) { f32x2_t v = {lo, hi}; bf16x2_t b = __builtin_convertvector(v, bf16x2_t); return __builtin_bit_cast(unsigned, b); }
; #define AT_LOADK(t) do { const int kr_ = AT_KROW(t); _Pragma("unroll") for (int i_ = 0; i_ < 2; ++i_) kreg[i_] = *(const u32x4*)(Kp + (size_t)(kr_ + prow0 + 32 * i_) * 512 + pch * 8); } while (0)
; #define AT_LOADV(t) do { const int kr_ = AT_KROW(t); _Pragma("unroll") for (int i_ = 0; i_ < 2; ++i_) vreg[i_] = *(const u32x4*)(Vp + (size_t)(kr_ + prow0 + 32 * i_) * 512 + pch * 8); } while (0)
; __device__ __forceinline__ void attn_unit(const Frame& F, int layer, int qrow0, int ntiles, int b, int head, float lam, float m2, float lam_init) {
;     ...
;         if (t + 2 < ntiles) AT_LOADK(t + 2);
;         if (t + 1 < ntiles) AT_LOADV(t + 1);
;         if (t + 1 < ntiles) AT_QK(na, nb, (t + 1) & 1);
;         float ls = 0.f;
; #pragma unroll
;         for (int i = 0; i < 16; ++i) { sa[i] = __builtin_amdgcn_exp2f(sa[i]); sb[i] = __builtin_amdgcn_exp2f(sb[i]); ls += sa[i] + sb[i]; }
;         lsum += ls;
;         bf16x8 pk[4];
;         { u32x4 w0, w1, w2, w3;
; #pragma unroll
;           for (int i = 0; i < 4; ++i) { w0[i] = pk2(sa[2 * i], sa[2 * i + 1]); w1[i] = pk2(sa[8 + 2 * i], sa[9 + 2 * i]); w2[i] = pk2(sb[2 * i], sb[2 * i + 1]); w3[i] = pk2(sb[8 + 2 * i], sb[9 + 2 * i]); }
;           pk[0] = __builtin_bit_cast(bf16x8, w0); pk[1] = __builtin_bit_cast(bf16x8, w1); pk[2] = __builtin_bit_cast(bf16x8, w2); pk[3] = __builtin_bit_cast(bf16x8, w3); }
.Latt_nokload_a4:
	s_add_i32 s5, s2, 6
	s_cmp_ge_u32 s5, 36
	s_cbranch_scc1 .Latt_novload_a4
	s_cmp_lt_u32 s5, 4
	s_cselect_b32 s15, s42, s43
	s_lshl_b32 s45, s5, 6
	s_add_i32 s15, s15, s45
	s_lshl_b32 s15, s15, 10
	v_add_u32_e32 v188, s15, v178
	v_add_u32_e32 v189, 0x8000, v188
	global_load_dwordx4 v[242:245], v188, s[74:75]
	global_load_dwordx4 v[248:251], v189, s[74:75]
.Latt_novload_a4:
	v_exp_f32_e32 v80, v80
	v_exp_f32_e32 v96, v96
	v_exp_f32_e32 v81, v81
	v_exp_f32_e32 v97, v97
	v_exp_f32_e32 v82, v82
	v_exp_f32_e32 v98, v98
	v_exp_f32_e32 v83, v83
	v_exp_f32_e32 v99, v99
	v_exp_f32_e32 v84, v84
	v_exp_f32_e32 v100, v100
	v_exp_f32_e32 v85, v85
	v_exp_f32_e32 v101, v101
	v_exp_f32_e32 v86, v86
	v_exp_f32_e32 v102, v102
	v_exp_f32_e32 v87, v87
	v_exp_f32_e32 v103, v103
	v_exp_f32_e32 v88, v88
	v_exp_f32_e32 v104, v104
	v_exp_f32_e32 v89, v89
	v_exp_f32_e32 v105, v105
	v_exp_f32_e32 v90, v90
	v_exp_f32_e32 v106, v106
	v_exp_f32_e32 v91, v91
	v_exp_f32_e32 v107, v107
	v_exp_f32_e32 v92, v92
	v_exp_f32_e32 v108, v108
	v_exp_f32_e32 v93, v93
	v_exp_f32_e32 v109, v109
	v_exp_f32_e32 v94, v94
	v_exp_f32_e32 v110, v110
	v_exp_f32_e32 v95, v95
	v_exp_f32_e32 v111, v111
	v_cvt_pk_bf16_f32 v112, v80, v81
	v_cvt_pk_bf16_f32 v113, v82, v83
	v_cvt_pk_bf16_f32 v114, v84, v85
	v_cvt_pk_bf16_f32 v115, v86, v87
	v_cvt_pk_bf16_f32 v116, v88, v89
	v_cvt_pk_bf16_f32 v117, v90, v91
	v_cvt_pk_bf16_f32 v118, v92, v93
	v_cvt_pk_bf16_f32 v119, v94, v95
	v_cvt_pk_bf16_f32 v120, v96, v97
	v_cvt_pk_bf16_f32 v121, v98, v99
	v_cvt_pk_bf16_f32 v122, v100, v101
	v_cvt_pk_bf16_f32 v123, v102, v103
	v_cvt_pk_bf16_f32 v124, v104, v105
	v_cvt_pk_bf16_f32 v125, v106, v107
	v_cvt_pk_bf16_f32 v126, v108, v109
	v_cvt_pk_bf16_f32 v127, v110, v111
	v_add_f32_e32 v80, v80, v96
	v_add_f32_e32 v81, v81, v97
	v_add_f32_e32 v82, v82, v98
	v_add_f32_e32 v83, v83, v99
	v_add_f32_e32 v84, v84, v100
	v_add_f32_e32 v85, v85, v101
	v_add_f32_e32 v86, v86, v102
	v_add_f32_e32 v87, v87, v103
	v_add_f32_e32 v88, v88, v104
	v_add_f32_e32 v89, v89, v105
	v_add_f32_e32 v90, v90, v106
	v_add_f32_e32 v91, v91, v107
	v_add_f32_e32 v92, v92, v108
	v_add_f32_e32 v93, v93, v109
	v_add_f32_e32 v94, v94, v110
	v_add_f32_e32 v95, v95, v111
	v_add_f32_e32 v80, v80, v88
	v_add_f32_e32 v81, v81, v89
	v_add_f32_e32 v82, v82, v90
	v_add_f32_e32 v83, v83, v91
	v_add_f32_e32 v84, v84, v92
	v_add_f32_e32 v85, v85, v93
	v_add_f32_e32 v86, v86, v94
	v_add_f32_e32 v87, v87, v95
	v_add_f32_e32 v80, v80, v84
	v_add_f32_e32 v81, v81, v85
	v_add_f32_e32 v82, v82, v86
	v_add_f32_e32 v83, v83, v87
	v_add_f32_e32 v80, v80, v82
	v_add_f32_e32 v81, v81, v83
	v_add_f32_e32 v80, v80, v81
	v_add_f32_e32 v201, v201, v80
	s_add_i32 s5, s2, 7
	s_cmp_ge_u32 s5, 36
	s_cbranch_scc1 .Latt_drain_a4
	s_waitcnt vmcnt(4)
	s_branch .Latt_stage_a4

; #define AT_STOREK(st) do { _Pragma("unroll") for (int i_ = 0; i_ < 2; ++i_) *(LAS u32x4*)(L + AT_K + (st) * AT_KBYTES + (prow0 + 32 * i_) * AT_KSTR + pch * 16) = kreg[i_]; } while (0)
; #define AT_STOREV(st) do { _Pragma("unroll") for (int i_ = 0; i_ < 2; ++i_) *(LAS u32x4*)(L + AT_V + (st) * AT_VBYTES + (prow0 + 32 * i_) * AT_VSTR + pch * 16) = vreg[i_]; } while (0)
; __device__ __forceinline__ void attn_unit(const Frame& F, int layer, int qrow0, int ntiles, int b, int head, float lam, float m2, float lam_init) {
;     ...
;         if (t + 2 < ntiles) AT_STOREK(t & 1);
;         if (t + 1 < ntiles) AT_STOREV((t + 1) & 1);
.Latt_stage_a4:
	s_add_i32 s5, s2, 6
	s_cmp_ge_u32 s5, 36
	s_cbranch_scc1 .Latt_kscr_a4
	ds_write_b128 v144, v[162:165] offset:0
	ds_write_b128 v144, v[166:169] offset:8704
	s_branch .Latt_kdone_a4

; #define AT_STOREK(st) do { _Pragma("unroll") for (int i_ = 0; i_ < 2; ++i_) *(LAS u32x4*)(L + AT_K + (st) * AT_KBYTES + (prow0 + 32 * i_) * AT_KSTR + pch * 16) = kreg[i_]; } while (0)
; #define AT_STOREV(st) do { _Pragma("unroll") for (int i_ = 0; i_ < 2; ++i_) *(LAS u32x4*)(L + AT_V + (st) * AT_VBYTES + (prow0 + 32 * i_) * AT_VSTR + pch * 16) = vreg[i_]; } while (0)
; __device__ __forceinline__ void attn_unit(const Frame& F, int layer, int qrow0, int ntiles, int b, int head, float lam, float m2, float lam_init) {
;     ...
;         if (t + 2 < ntiles) AT_STOREK(t & 1);
;         if (t + 1 < ntiles) AT_STOREV((t + 1) & 1);
.Latt_kdone_a4:
	s_add_i32 s5, s2, 5
	s_cmp_ge_u32 s5, 36
	s_cbranch_scc1 .Latt_vscr_a4
	ds_write_b128 v195, v[170:173] offset:34816
	ds_write_b128 v195, v[174:177] offset:45056
	s_branch .Latt_vdone_a4

; #define LAS __attribute__((address_space(3)))
; __device__ __forceinline__ unsigned pk2(float lo, float hi) { f32x2_t v = {lo, hi}; bf16x2_t b = __builtin_convertvector(v, bf16x2_t); return __builtin_bit_cast(unsigned, b); }
; #define MFMA32(a, b, c) __builtin_amdgcn_mfma_f32_32x32x16_bf16((a), (b), (c), 0, 0, 0)
; __device__ __forceinline__ void attn_unit(const Frame& F, int layer, int qrow0, int ntiles, int b, int head, float lam, float m2, float lam_init) {
;     ...
;         if (t + 1 < ntiles) AT_QK(na, nb, (t + 1) & 1);
;         float ls = 0.f;
; #pragma unroll
;         for (int i = 0; i < 16; ++i) { sa[i] = __builtin_amdgcn_exp2f(sa[i]); sb[i] = __builtin_amdgcn_exp2f(sb[i]); ls += sa[i] + sb[i]; }
;         lsum += ls;
;         bf16x8 pk[4];
;         { u32x4 w0, w1, w2, w3;
; #pragma unroll
;           for (int i = 0; i < 4; ++i) { w0[i] = pk2(sa[2 * i], sa[2 * i + 1]); w1[i] = pk2(sa[8 + 2 * i], sa[9 + 2 * i]); w2[i] = pk2(sb[2 * i], sb[2 * i + 1]); w3[i] = pk2(sb[8 + 2 * i], sb[9 + 2 * i]); }
;           pk[0] = __builtin_bit_cast(bf16x8, w0); pk[1] = __builtin_bit_cast(bf16x8, w1); pk[2] = __builtin_bit_cast(bf16x8, w2); pk[3] = __builtin_bit_cast(bf16x8, w3); }
;         LAS const unsigned char* Vt = L + AT_V + (t & 1) * AT_VBYTES;
;         __builtin_amdgcn_sched_barrier(0);
;         bf16x8 vfa[4], vfb[4];
; #pragma unroll
;         for (int j = 0; j < 4; ++j) vfa[j] = frag_tr_acc(Vt, AT_VSTR, 0, 32 * j, lane);
; #pragma unroll
;         for (int ks = 0; ks < 4; ks += 2) {
; #pragma unroll
;             for (int j = 0; j < 4; ++j) vfb[j] = frag_tr_acc(Vt, AT_VSTR, 16 * (ks + 1), 32 * j, lane);
; #pragma unroll
;             for (int j = 0; j < 4; ++j) o[j] = MFMA32(pk[ks], vfa[j], o[j]);
;             __builtin_amdgcn_sched_barrier(0);
;             if (ks + 2 < 4) {
; #pragma unroll
;                 for (int j = 0; j < 4; ++j) vfa[j] = frag_tr_acc(Vt, AT_VSTR, 16 * (ks + 2), 32 * j, lane);
;             }
; #pragma unroll
;             for (int j = 0; j < 4; ++j) o[j] = MFMA32(pk[ks + 1], vfb[j], o[j]);
;             __builtin_amdgcn_sched_barrier(0);
;         }
.Latt_vdone_a4:
	s_add_i32 s5, s2, 5
	s_cmp_ge_u32 s5, 36
	s_cbranch_scc1 .Latt_noqkw_a4
	ds_read_b128 v[128:131], v190 offset:0
	ds_read_b128 v[132:135], v190 offset:8704
	ds_read_b128 v[136:139], v190 offset:32
	ds_read_b128 v[140:143], v190 offset:8736
	s_waitcnt lgkmcnt(2)
	v_mfma_f32_32x32x16_bf16 v[80:95], v[128:131], v[158:161], v[64:79]
	v_mfma_f32_32x32x16_bf16 v[96:111], v[132:135], v[158:161], v[64:79]
	ds_read_b128 v[128:131], v190 offset:64
	ds_read_b128 v[132:135], v190 offset:8768
	s_waitcnt lgkmcnt(2)
	v_mfma_f32_32x32x16_bf16 v[80:95], v[136:139], v[154:157], v[80:95]
	v_mfma_f32_32x32x16_bf16 v[96:111], v[140:143], v[154:157], v[96:111]
	ds_read_b128 v[136:139], v190 offset:96
	ds_read_b128 v[140:143], v190 offset:8800
	s_waitcnt lgkmcnt(2)
	v_mfma_f32_32x32x16_bf16 v[80:95], v[128:131], v[150:153], v[80:95]
	v_mfma_f32_32x32x16_bf16 v[96:111], v[132:135], v[150:153], v[96:111]
	s_waitcnt lgkmcnt(0)
	v_mfma_f32_32x32x16_bf16 v[80:95], v[136:139], v[146:149], v[80:95]
	v_mfma_f32_32x32x16_bf16 v[96:111], v[140:143], v[146:149], v[96:111]
.Latt_noqk_a4:
	ds_read_b64_tr_b16 v[202:203], v191 offset:34816
	ds_read_b64_tr_b16 v[206:207], v191 offset:34880
	ds_read_b64_tr_b16 v[210:211], v191 offset:34944
	ds_read_b64_tr_b16 v[214:215], v191 offset:35008
	ds_read_b64_tr_b16 v[204:205], v191 offset:37376
	ds_read_b64_tr_b16 v[208:209], v191 offset:37440
	ds_read_b64_tr_b16 v[212:213], v191 offset:37504
	ds_read_b64_tr_b16 v[216:217], v191 offset:37568
	ds_read_b64_tr_b16 v[218:219], v191 offset:39936
	ds_read_b64_tr_b16 v[222:223], v191 offset:40000
	ds_read_b64_tr_b16 v[226:227], v191 offset:40064
	ds_read_b64_tr_b16 v[230:231], v191 offset:40128
	ds_read_b64_tr_b16 v[220:221], v191 offset:42496
	ds_read_b64_tr_b16 v[224:225], v191 offset:42560
	ds_read_b64_tr_b16 v[228:229], v191 offset:42624
	s_waitcnt lgkmcnt(14)
	ds_read_b64_tr_b16 v[232:233], v191 offset:42688
	s_waitcnt lgkmcnt(8)
	v_mfma_f32_32x32x16_bf16 v[32:47], v[112:115], v[202:205], v[32:47]
	v_mfma_f32_32x32x16_bf16 v[48:63], v[112:115], v[206:209], v[48:63]
	v_mfma_f32_32x32x16_bf16 v[0:15], v[112:115], v[210:213], v[0:15]
	v_mfma_f32_32x32x16_bf16 v[16:31], v[112:115], v[214:217], v[16:31]
	ds_read_b64_tr_b16 v[202:203], v191 offset:45056
	ds_read_b64_tr_b16 v[206:207], v191 offset:45120
	ds_read_b64_tr_b16 v[210:211], v191 offset:45184
	ds_read_b64_tr_b16 v[214:215], v191 offset:45248
	ds_read_b64_tr_b16 v[204:205], v191 offset:47616
	ds_read_b64_tr_b16 v[208:209], v191 offset:47680
	ds_read_b64_tr_b16 v[212:213], v191 offset:47744
	s_waitcnt lgkmcnt(14)
	ds_read_b64_tr_b16 v[216:217], v191 offset:47808
	s_waitcnt lgkmcnt(8)
	v_mfma_f32_32x32x16_bf16 v[32:47], v[116:119], v[218:221], v[32:47]
	v_mfma_f32_32x32x16_bf16 v[48:63], v[116:119], v[222:225], v[48:63]
	v_mfma_f32_32x32x16_bf16 v[0:15], v[116:119], v[226:229], v[0:15]
	v_mfma_f32_32x32x16_bf16 v[16:31], v[116:119], v[230:233], v[16:31]
	ds_read_b64_tr_b16 v[218:219], v191 offset:50176
	ds_read_b64_tr_b16 v[222:223], v191 offset:50240
	ds_read_b64_tr_b16 v[226:227], v191 offset:50304
	ds_read_b64_tr_b16 v[230:231], v191 offset:50368
	ds_read_b64_tr_b16 v[220:221], v191 offset:52736
	ds_read_b64_tr_b16 v[224:225], v191 offset:52800
	ds_read_b64_tr_b16 v[228:229], v191 offset:52864
	s_waitcnt lgkmcnt(14)
	ds_read_b64_tr_b16 v[232:233], v191 offset:52928
	s_waitcnt lgkmcnt(8)
	v_mfma_f32_32x32x16_bf16 v[32:47], v[120:123], v[202:205], v[32:47]
	v_mfma_f32_32x32x16_bf16 v[48:63], v[120:123], v[206:209], v[48:63]
	v_mfma_f32_32x32x16_bf16 v[0:15], v[120:123], v[210:213], v[0:15]
	v_mfma_f32_32x32x16_bf16 v[16:31], v[120:123], v[214:217], v[16:31]
	s_waitcnt lgkmcnt(0)
	v_mfma_f32_32x32x16_bf16 v[32:47], v[124:127], v[218:221], v[32:47]
	v_mfma_f32_32x32x16_bf16 v[48:63], v[124:127], v[222:225], v[48:63]
	v_mfma_f32_32x32x16_bf16 v[0:15], v[124:127], v[226:229], v[0:15]
	v_mfma_f32_32x32x16_bf16 v[16:31], v[124:127], v[230:233], v[16:31]
	s_barrier
	s_add_i32 s5, s2, 8
	s_cmp_ge_u32 s5, 36
	s_cbranch_scc1 .Latt_nokload_a5
	s_cmp_lt_u32 s5, 4
	s_cselect_b32 s15, s42, s43
	s_lshl_b32 s45, s5, 6
	s_add_i32 s15, s15, s45
	s_lshl_b32 s15, s15, 10
	v_add_u32_e32 v186, s15, v178
	v_add_u32_e32 v187, 0x8000, v186
	global_load_dwordx4 v[162:165], v186, s[72:73]
	global_load_dwordx4 v[166:169], v187, s[72:73]
; __device__ __forceinline__ unsigned pk2(float lo, float hi) { f32x2_t v = {lo, hi}; bf16x2_t b = __builtin_convertvector(v, bf16x2_t); return __builtin_bit_cast(unsigned, b); }
; #define AT_LOADK(t) do { const int kr_ = AT_KROW(t); _Pragma("unroll") for (int i_ = 0; i_ < 2; ++i_) kreg[i_] = *(const u32x4*)(Kp + (size_t)(kr_ + prow0 + 32 * i_) * 512 + pch * 8); } while (0)
; #define AT_LOADV(t) do { const int kr_ = AT_KROW(t); _Pragma("unroll") for (int i_ = 0; i_ < 2; ++i_) vreg[i_] = *(const u32x4*)(Vp + (size_t)(kr_ + prow0 + 32 * i_) * 512 + pch * 8); } while (0)
; __device__ __forceinline__ void attn_unit(const Frame& F, int layer, int qrow0, int ntiles, int b, int head, float lam, float m2, float lam_init) {
;     ...
;         if (t + 2 < ntiles) AT_LOADK(t + 2);
;         if (t + 1 < ntiles) AT_LOADV(t + 1);
;         if (t + 1 < ntiles) AT_QK(na, nb, (t + 1) & 1);
;         float ls = 0.f;
; #pragma unroll
;         for (int i = 0; i < 16; ++i) { sa[i] = __builtin_amdgcn_exp2f(sa[i]); sb[i] = __builtin_amdgcn_exp2f(sb[i]); ls += sa[i] + sb[i]; }
;         lsum += ls;
;         bf16x8 pk[4];
;         { u32x4 w0, w1, w2, w3;
; #pragma unroll
;           for (int i = 0; i < 4; ++i) { w0[i] = pk2(sa[2 * i], sa[2 * i + 1]); w1[i] = pk2(sa[8 + 2 * i], sa[9 + 2 * i]); w2[i] = pk2(sb[2 * i], sb[2 * i + 1]); w3[i] = pk2(sb[8 + 2 * i], sb[9 + 2 * i]); }
;           pk[0] = __builtin_bit_cast(bf16x8, w0); pk[1] = __builtin_bit_cast(bf16x8, w1); pk[2] = __builtin_bit_cast(bf16x8, w2); pk[3] = __builtin_bit_cast(bf16x8, w3); }
.Latt_nokload_a5:
	s_add_i32 s5, s2, 7
	s_cmp_ge_u32 s5, 36
	s_cbranch_scc1 .Latt_novload_a5
	s_cmp_lt_u32 s5, 4
	s_cselect_b32 s15, s42, s43
	s_lshl_b32 s45, s5, 6
	s_add_i32 s15, s15, s45
	s_lshl_b32 s15, s15, 10
	v_add_u32_e32 v188, s15, v178
	v_add_u32_e32 v189, 0x8000, v188
	global_load_dwordx4 v[170:173], v188, s[74:75]
	global_load_dwordx4 v[174:177], v189, s[74:75]
.Latt_novload_a5:
	v_exp_f32_e32 v80, v80
	v_exp_f32_e32 v96, v96
	v_exp_f32_e32 v81, v81
	v_exp_f32_e32 v97, v97
	v_exp_f32_e32 v82, v82
	v_exp_f32_e32 v98, v98
	v_exp_f32_e32 v83, v83
	v_exp_f32_e32 v99, v99
	v_exp_f32_e32 v84, v84
	v_exp_f32_e32 v100, v100
	v_exp_f32_e32 v85, v85
	v_exp_f32_e32 v101, v101
	v_exp_f32_e32 v86, v86
	v_exp_f32_e32 v102, v102
	v_exp_f32_e32 v87, v87
	v_exp_f32_e32 v103, v103
	v_exp_f32_e32 v88, v88
	v_exp_f32_e32 v104, v104
	v_exp_f32_e32 v89, v89
	v_exp_f32_e32 v105, v105
	v_exp_f32_e32 v90, v90
	v_exp_f32_e32 v106, v106
	v_exp_f32_e32 v91, v91
	v_exp_f32_e32 v107, v107
	v_exp_f32_e32 v92, v92
	v_exp_f32_e32 v108, v108
	v_exp_f32_e32 v93, v93
	v_exp_f32_e32 v109, v109
	v_exp_f32_e32 v94, v94
	v_exp_f32_e32 v110, v110
	v_exp_f32_e32 v95, v95
	v_exp_f32_e32 v111, v111
	v_cvt_pk_bf16_f32 v112, v80, v81
	v_cvt_pk_bf16_f32 v113, v82, v83
	v_cvt_pk_bf16_f32 v114, v84, v85
	v_cvt_pk_bf16_f32 v115, v86, v87
	v_cvt_pk_bf16_f32 v116, v88, v89
	v_cvt_pk_bf16_f32 v117, v90, v91
	v_cvt_pk_bf16_f32 v118, v92, v93
	v_cvt_pk_bf16_f32 v119, v94, v95
	v_cvt_pk_bf16_f32 v120, v96, v97
	v_cvt_pk_bf16_f32 v121, v98, v99
	v_cvt_pk_bf16_f32 v122, v100, v101
	v_cvt_pk_bf16_f32 v123, v102, v103
	v_cvt_pk_bf16_f32 v124, v104, v105
	v_cvt_pk_bf16_f32 v125, v106, v107
	v_cvt_pk_bf16_f32 v126, v108, v109
	v_cvt_pk_bf16_f32 v127, v110, v111
	v_add_f32_e32 v80, v80, v96
	v_add_f32_e32 v81, v81, v97
	v_add_f32_e32 v82, v82, v98
	v_add_f32_e32 v83, v83, v99
	v_add_f32_e32 v84, v84, v100
	v_add_f32_e32 v85, v85, v101
	v_add_f32_e32 v86, v86, v102
	v_add_f32_e32 v87, v87, v103
	v_add_f32_e32 v88, v88, v104
	v_add_f32_e32 v89, v89, v105
	v_add_f32_e32 v90, v90, v106
	v_add_f32_e32 v91, v91, v107
	v_add_f32_e32 v92, v92, v108
	v_add_f32_e32 v93, v93, v109
	v_add_f32_e32 v94, v94, v110
	v_add_f32_e32 v95, v95, v111
	v_add_f32_e32 v80, v80, v88
	v_add_f32_e32 v81, v81, v89
	v_add_f32_e32 v82, v82, v90
	v_add_f32_e32 v83, v83, v91
	v_add_f32_e32 v84, v84, v92
	v_add_f32_e32 v85, v85, v93
	v_add_f32_e32 v86, v86, v94
	v_add_f32_e32 v87, v87, v95
	v_add_f32_e32 v80, v80, v84
	v_add_f32_e32 v81, v81, v85
	v_add_f32_e32 v82, v82, v86
	v_add_f32_e32 v83, v83, v87
	v_add_f32_e32 v80, v80, v82
	v_add_f32_e32 v81, v81, v83
	v_add_f32_e32 v80, v80, v81
	v_add_f32_e32 v201, v201, v80
	s_add_i32 s5, s2, 8
	s_cmp_ge_u32 s5, 36
	s_cbranch_scc1 .Latt_drain_a5
	s_waitcnt vmcnt(4)
	s_branch .Latt_stage_a5

; #define AT_STOREK(st) do { _Pragma("unroll") for (int i_ = 0; i_ < 2; ++i_) *(LAS u32x4*)(L + AT_K + (st) * AT_KBYTES + (prow0 + 32 * i_) * AT_KSTR + pch * 16) = kreg[i_]; } while (0)
; #define AT_STOREV(st) do { _Pragma("unroll") for (int i_ = 0; i_ < 2; ++i_) *(LAS u32x4*)(L + AT_V + (st) * AT_VBYTES + (prow0 + 32 * i_) * AT_VSTR + pch * 16) = vreg[i_]; } while (0)
; __device__ __forceinline__ void attn_unit(const Frame& F, int layer, int qrow0, int ntiles, int b, int head, float lam, float m2, float lam_init) {
;     ...
;         if (t + 2 < ntiles) AT_STOREK(t & 1);
;         if (t + 1 < ntiles) AT_STOREV((t + 1) & 1);
.Latt_stage_a5:
	s_add_i32 s5, s2, 7
	s_cmp_ge_u32 s5, 36
	s_cbranch_scc1 .Latt_kscr_a5
	ds_write_b128 v144, v[234:237] offset:17408
	ds_write_b128 v144, v[238:241] offset:26112
	s_branch .Latt_kdone_a5

; #define AT_STOREK(st) do { _Pragma("unroll") for (int i_ = 0; i_ < 2; ++i_) *(LAS u32x4*)(L + AT_K + (st) * AT_KBYTES + (prow0 + 32 * i_) * AT_KSTR + pch * 16) = kreg[i_]; } while (0)
; #define AT_STOREV(st) do { _Pragma("unroll") for (int i_ = 0; i_ < 2; ++i_) *(LAS u32x4*)(L + AT_V + (st) * AT_VBYTES + (prow0 + 32 * i_) * AT_VSTR + pch * 16) = vreg[i_]; } while (0)
; __device__ __forceinline__ void attn_unit(const Frame& F, int layer, int qrow0, int ntiles, int b, int head, float lam, float m2, float lam_init) {
;     ...
;         if (t + 2 < ntiles) AT_STOREK(t & 1);
;         if (t + 1 < ntiles) AT_STOREV((t + 1) & 1);
.Latt_kdone_a5:
	s_add_i32 s5, s2, 6
	s_cmp_ge_u32 s5, 36
	s_cbranch_scc1 .Latt_vscr_a5
	ds_write_b128 v194, v[242:245] offset:34816
	ds_write_b128 v194, v[248:251] offset:45056
	s_branch .Latt_vdone_a5

; #define LAS __attribute__((address_space(3)))
; __device__ __forceinline__ unsigned pk2(float lo, float hi) { f32x2_t v = {lo, hi}; bf16x2_t b = __builtin_convertvector(v, bf16x2_t); return __builtin_bit_cast(unsigned, b); }
; #define MFMA32(a, b, c) __builtin_amdgcn_mfma_f32_32x32x16_bf16((a), (b), (c), 0, 0, 0)
; __device__ __forceinline__ void attn_unit(const Frame& F, int layer, int qrow0, int ntiles, int b, int head, float lam, float m2, float lam_init) {
;     ...
;         if (t + 1 < ntiles) AT_QK(na, nb, (t + 1) & 1);
;         float ls = 0.f;
; #pragma unroll
;         for (int i = 0; i < 16; ++i) { sa[i] = __builtin_amdgcn_exp2f(sa[i]); sb[i] = __builtin_amdgcn_exp2f(sb[i]); ls += sa[i] + sb[i]; }
;         lsum += ls;
;         bf16x8 pk[4];
;         { u32x4 w0, w1, w2, w3;
; #pragma unroll
;           for (int i = 0; i < 4; ++i) { w0[i] = pk2(sa[2 * i], sa[2 * i + 1]); w1[i] = pk2(sa[8 + 2 * i], sa[9 + 2 * i]); w2[i] = pk2(sb[2 * i], sb[2 * i + 1]); w3[i] = pk2(sb[8 + 2 * i], sb[9 + 2 * i]); }
;           pk[0] = __builtin_bit_cast(bf16x8, w0); pk[1] = __builtin_bit_cast(bf16x8, w1); pk[2] = __builtin_bit_cast(bf16x8, w2); pk[3] = __builtin_bit_cast(bf16x8, w3); }
;         LAS const unsigned char* Vt = L + AT_V + (t & 1) * AT_VBYTES;
;         __builtin_amdgcn_sched_barrier(0);
;         bf16x8 vfa[4], vfb[4];
; #pragma unroll
;         for (int j = 0; j < 4; ++j) vfa[j] = frag_tr_acc(Vt, AT_VSTR, 0, 32 * j, lane);
; #pragma unroll
;         for (int ks = 0; ks < 4; ks += 2) {
; #pragma unroll
;             for (int j = 0; j < 4; ++j) vfb[j] = frag_tr_acc(Vt, AT_VSTR, 16 * (ks + 1), 32 * j, lane);
; #pragma unroll
;             for (int j = 0; j < 4; ++j) o[j] = MFMA32(pk[ks], vfa[j], o[j]);
;             __builtin_amdgcn_sched_barrier(0);
;             if (ks + 2 < 4) {
; #pragma unroll
;                 for (int j = 0; j < 4; ++j) vfa[j] = frag_tr_acc(Vt, AT_VSTR, 16 * (ks + 2), 32 * j, lane);
;             }
; #pragma unroll
;             for (int j = 0; j < 4; ++j) o[j] = MFMA32(pk[ks + 1], vfb[j], o[j]);
;             __builtin_amdgcn_sched_barrier(0);
;         }
;         if (t + 2 < ntiles) AT_STOREK(t & 1);
;         if (t + 1 < ntiles) AT_STOREV((t + 1) & 1);
;         __syncthreads();
;         sa = na; sb = nb;
;     }
.Latt_vdone_a5:
	s_add_i32 s5, s2, 6
	s_cmp_ge_u32 s5, 36
	s_cbranch_scc1 .Latt_noqkw_a5
	ds_read_b128 v[128:131], v197 offset:0
	ds_read_b128 v[132:135], v197 offset:8704
	ds_read_b128 v[136:139], v197 offset:32
	ds_read_b128 v[140:143], v197 offset:8736
	s_waitcnt lgkmcnt(2)
	v_mfma_f32_32x32x16_bf16 v[80:95], v[128:131], v[158:161], v[64:79]
	v_mfma_f32_32x32x16_bf16 v[96:111], v[132:135], v[158:161], v[64:79]
	ds_read_b128 v[128:131], v197 offset:64
	ds_read_b128 v[132:135], v197 offset:8768
	s_waitcnt lgkmcnt(2)
	v_mfma_f32_32x32x16_bf16 v[80:95], v[136:139], v[154:157], v[80:95]
	v_mfma_f32_32x32x16_bf16 v[96:111], v[140:143], v[154:157], v[96:111]
	ds_read_b128 v[136:139], v197 offset:96
	ds_read_b128 v[140:143], v197 offset:8800
	s_waitcnt lgkmcnt(2)
	v_mfma_f32_32x32x16_bf16 v[80:95], v[128:131], v[150:153], v[80:95]
	v_mfma_f32_32x32x16_bf16 v[96:111], v[132:135], v[150:153], v[96:111]
	s_waitcnt lgkmcnt(0)
	v_mfma_f32_32x32x16_bf16 v[80:95], v[136:139], v[146:149], v[80:95]
	v_mfma_f32_32x32x16_bf16 v[96:111], v[140:143], v[146:149], v[96:111]
.Latt_noqk_a5:
	ds_read_b64_tr_b16 v[202:203], v184 offset:34816
	ds_read_b64_tr_b16 v[206:207], v184 offset:34880
	ds_read_b64_tr_b16 v[210:211], v184 offset:34944
	ds_read_b64_tr_b16 v[214:215], v184 offset:35008
	ds_read_b64_tr_b16 v[204:205], v184 offset:37376
	ds_read_b64_tr_b16 v[208:209], v184 offset:37440
	ds_read_b64_tr_b16 v[212:213], v184 offset:37504
	ds_read_b64_tr_b16 v[216:217], v184 offset:37568
	ds_read_b64_tr_b16 v[218:219], v184 offset:39936
	ds_read_b64_tr_b16 v[222:223], v184 offset:40000
	ds_read_b64_tr_b16 v[226:227], v184 offset:40064
	ds_read_b64_tr_b16 v[230:231], v184 offset:40128
	ds_read_b64_tr_b16 v[220:221], v184 offset:42496
	ds_read_b64_tr_b16 v[224:225], v184 offset:42560
	ds_read_b64_tr_b16 v[228:229], v184 offset:42624
	s_waitcnt lgkmcnt(14)
	ds_read_b64_tr_b16 v[232:233], v184 offset:42688
	s_waitcnt lgkmcnt(8)
	v_mfma_f32_32x32x16_bf16 v[32:47], v[112:115], v[202:205], v[32:47]
	v_mfma_f32_32x32x16_bf16 v[48:63], v[112:115], v[206:209], v[48:63]
	v_mfma_f32_32x32x16_bf16 v[0:15], v[112:115], v[210:213], v[0:15]
	v_mfma_f32_32x32x16_bf16 v[16:31], v[112:115], v[214:217], v[16:31]
	ds_read_b64_tr_b16 v[202:203], v184 offset:45056
	ds_read_b64_tr_b16 v[206:207], v184 offset:45120
	ds_read_b64_tr_b16 v[210:211], v184 offset:45184
	ds_read_b64_tr_b16 v[214:215], v184 offset:45248
	ds_read_b64_tr_b16 v[204:205], v184 offset:47616
	ds_read_b64_tr_b16 v[208:209], v184 offset:47680
	ds_read_b64_tr_b16 v[212:213], v184 offset:47744
	s_waitcnt lgkmcnt(14)
	ds_read_b64_tr_b16 v[216:217], v184 offset:47808
	s_waitcnt lgkmcnt(8)
	v_mfma_f32_32x32x16_bf16 v[32:47], v[116:119], v[218:221], v[32:47]
	v_mfma_f32_32x32x16_bf16 v[48:63], v[116:119], v[222:225], v[48:63]
	v_mfma_f32_32x32x16_bf16 v[0:15], v[116:119], v[226:229], v[0:15]
	v_mfma_f32_32x32x16_bf16 v[16:31], v[116:119], v[230:233], v[16:31]
	ds_read_b64_tr_b16 v[218:219], v184 offset:50176
	ds_read_b64_tr_b16 v[222:223], v184 offset:50240
	ds_read_b64_tr_b16 v[226:227], v184 offset:50304
	ds_read_b64_tr_b16 v[230:231], v184 offset:50368
	ds_read_b64_tr_b16 v[220:221], v184 offset:52736
	ds_read_b64_tr_b16 v[224:225], v184 offset:52800
	ds_read_b64_tr_b16 v[228:229], v184 offset:52864
	s_waitcnt lgkmcnt(14)
	ds_read_b64_tr_b16 v[232:233], v184 offset:52928
	s_waitcnt lgkmcnt(8)
	v_mfma_f32_32x32x16_bf16 v[32:47], v[120:123], v[202:205], v[32:47]
	v_mfma_f32_32x32x16_bf16 v[48:63], v[120:123], v[206:209], v[48:63]
	v_mfma_f32_32x32x16_bf16 v[0:15], v[120:123], v[210:213], v[0:15]
	v_mfma_f32_32x32x16_bf16 v[16:31], v[120:123], v[214:217], v[16:31]
	s_waitcnt lgkmcnt(0)
	v_mfma_f32_32x32x16_bf16 v[32:47], v[124:127], v[218:221], v[32:47]
	v_mfma_f32_32x32x16_bf16 v[48:63], v[124:127], v[222:225], v[48:63]
	v_mfma_f32_32x32x16_bf16 v[0:15], v[124:127], v[226:229], v[0:15]
	v_mfma_f32_32x32x16_bf16 v[16:31], v[124:127], v[230:233], v[16:31]
	s_barrier
	s_add_i32 s2, s2, 6
	s_cmp_lt_u32 s2, 36
	s_cbranch_scc1 .Latt_lead_loop
	s_branch .Latt_exit
.Latt_noqkw_a0:
	s_waitcnt lgkmcnt(0)
	s_branch .Latt_noqk_a0

; #define LAS __attribute__((address_space(3)))
; __device__ __forceinline__ unsigned pk2(float lo, float hi) { f32x2_t v = {lo, hi}; bf16x2_t b = __builtin_convertvector(v, bf16x2_t); return __builtin_bit_cast(unsigned, b); }
; __device__ __forceinline__ void attn_unit(const Frame& F, int layer, int qrow0, int ntiles, int b, int head, float lam, float m2, float lam_init) {
;     ...
;         if (t + 1 < ntiles) AT_QK(na, nb, (t + 1) & 1);
;         float ls = 0.f;
; #pragma unroll
;         for (int i = 0; i < 16; ++i) { sa[i] = __builtin_amdgcn_exp2f(sa[i]); sb[i] = __builtin_amdgcn_exp2f(sb[i]); ls += sa[i] + sb[i]; }
;         lsum += ls;
;         bf16x8 pk[4];
;         { u32x4 w0, w1, w2, w3;
; #pragma unroll
;           for (int i = 0; i < 4; ++i) { w0[i] = pk2(sa[2 * i], sa[2 * i + 1]); w1[i] = pk2(sa[8 + 2 * i], sa[9 + 2 * i]); w2[i] = pk2(sb[2 * i], sb[2 * i + 1]); w3[i] = pk2(sb[8 + 2 * i], sb[9 + 2 * i]); }
;           pk[0] = __builtin_bit_cast(bf16x8, w0); pk[1] = __builtin_bit_cast(bf16x8, w1); pk[2] = __builtin_bit_cast(bf16x8, w2); pk[3] = __builtin_bit_cast(bf16x8, w3); }
;         LAS const unsigned char* Vt = L + AT_V + (t & 1) * AT_VBYTES;
.Latt_noqkw_a5:
	s_waitcnt lgkmcnt(0)
	s_branch .Latt_noqk_a5
	.p2align 6

; #define AT_LOADK(t) do { const int kr_ = AT_KROW(t); _Pragma("unroll") for (int i_ = 0; i_ < 2; ++i_) kreg[i_] = *(const u32x4*)(Kp + (size_t)(kr_ + prow0 + 32 * i_) * 512 + pch * 8); } while (0)
; #define AT_LOADV(t) do { const int kr_ = AT_KROW(t); _Pragma("unroll") for (int i_ = 0; i_ < 2; ++i_) vreg[i_] = *(const u32x4*)(Vp + (size_t)(kr_ + prow0 + 32 * i_) * 512 + pch * 8); } while (0)
; __device__ __forceinline__ void attn_unit(const Frame& F, int layer, int qrow0, int ntiles, int b, int head, float lam, float m2, float lam_init) {
;     ...
;         if (t + 2 < ntiles) AT_LOADK(t + 2);
;         if (t + 1 < ntiles) AT_LOADV(t + 1);
.Latt_novload_b0:
	s_add_i32 s5, s2, 3
	s_cmp_ge_u32 s5, 36
	s_cbranch_scc1 .Latt_drain_b0
	s_waitcnt vmcnt(4)
	s_branch .Latt_stage_b0

; __device__ __forceinline__ unsigned pk2(float lo, float hi) { f32x2_t v = {lo, hi}; bf16x2_t b = __builtin_convertvector(v, bf16x2_t); return __builtin_bit_cast(unsigned, b); }
; __device__ __forceinline__ void lds_barrier() { asm volatile("s_waitcnt lgkmcnt(0)" ::: "memory"); __builtin_amdgcn_s_barrier(); asm volatile("" ::: "memory"); }
; #define AT_LOADK(t) do { const int kr_ = AT_KROW(t); _Pragma("unroll") for (int i_ = 0; i_ < 2; ++i_) kreg[i_] = *(const u32x4*)(Kp + (size_t)(kr_ + prow0 + 32 * i_) * 512 + pch * 8); } while (0)
; #define AT_LOADV(t) do { const int kr_ = AT_KROW(t); _Pragma("unroll") for (int i_ = 0; i_ < 2; ++i_) vreg[i_] = *(const u32x4*)(Vp + (size_t)(kr_ + prow0 + 32 * i_) * 512 + pch * 8); } while (0)
; #define AT_STOREK(st) do { _Pragma("unroll") for (int i_ = 0; i_ < 2; ++i_) *(LAS u32x4*)(L + AT_K + (st) * AT_KBYTES + (prow0 + 32 * i_) * AT_KSTR + pch * 16) = kreg[i_]; } while (0)
; #define AT_STOREV(st) do { _Pragma("unroll") for (int i_ = 0; i_ < 2; ++i_) *(LAS u32x4*)(L + AT_V + (st) * AT_VBYTES + (prow0 + 32 * i_) * AT_VSTR + pch * 16) = vreg[i_]; } while (0)
; __device__ __forceinline__ void attn_unit(const Frame& F, int layer, int qrow0, int ntiles, int b, int head, float lam, float m2, float lam_init) {
;     ...
;     if (wave >= 4) __builtin_amdgcn_s_setprio(1);
;     AT_LOADK(0); AT_LOADV(0); AT_STOREK(0); AT_STOREV(0);
;     if (ntiles > 1) { AT_LOADK(1); AT_STOREK(1); }
;     __syncthreads();
;     f32x16 sa, sb, na, nb;
;     AT_QK(sa, sb, 0);
;     lds_barrier();
;     for (int t = 0; t < ntiles; ++t) {
;         if (t + 2 < ntiles) AT_LOADK(t + 2);
;         if (t + 1 < ntiles) AT_LOADV(t + 1);
;         if (t + 1 < ntiles) AT_QK(na, nb, (t + 1) & 1);
;         float ls = 0.f;
; #pragma unroll
;         for (int i = 0; i < 16; ++i) { sa[i] = __builtin_amdgcn_exp2f(sa[i]); sb[i] = __builtin_amdgcn_exp2f(sb[i]); ls += sa[i] + sb[i]; }
;         lsum += ls;
;         bf16x8 pk[4];
;         { u32x4 w0, w1, w2, w3;
; #pragma unroll
;           for (int i = 0; i < 4; ++i) { w0[i] = pk2(sa[2 * i], sa[2 * i + 1]); w1[i] = pk2(sa[8 + 2 * i], sa[9 + 2 * i]); w2[i] = pk2(sb[2 * i], sb[2 * i + 1]); w3[i] = pk2(sb[8 + 2 * i], sb[9 + 2 * i]); }
;           pk[0] = __builtin_bit_cast(bf16x8, w0); pk[1] = __builtin_bit_cast(bf16x8, w1); pk[2] = __builtin_bit_cast(bf16x8, w2); pk[3] = __builtin_bit_cast(bf16x8, w3); }
.Latt_vdone_b0:
	ds_read_b128 v[128:131], v197 offset:0
	ds_read_b128 v[132:135], v197 offset:8704
	ds_read_b128 v[136:139], v197 offset:32
	ds_read_b128 v[140:143], v197 offset:8736
	s_waitcnt lgkmcnt(2)
	v_mfma_f32_32x32x16_bf16 v[80:95], v[128:131], v[158:161], v[64:79]
	v_mfma_f32_32x32x16_bf16 v[96:111], v[132:135], v[158:161], v[64:79]
	ds_read_b128 v[128:131], v197 offset:64
	ds_read_b128 v[132:135], v197 offset:8768
	s_waitcnt lgkmcnt(2)
	v_mfma_f32_32x32x16_bf16 v[80:95], v[136:139], v[154:157], v[80:95]
	v_mfma_f32_32x32x16_bf16 v[96:111], v[140:143], v[154:157], v[96:111]
	ds_read_b128 v[136:139], v197 offset:96
	ds_read_b128 v[140:143], v197 offset:8800
	s_waitcnt lgkmcnt(2)
	v_mfma_f32_32x32x16_bf16 v[80:95], v[128:131], v[150:153], v[80:95]
	v_mfma_f32_32x32x16_bf16 v[96:111], v[132:135], v[150:153], v[96:111]
	s_waitcnt lgkmcnt(0)
	v_mfma_f32_32x32x16_bf16 v[80:95], v[136:139], v[146:149], v[80:95]
	v_mfma_f32_32x32x16_bf16 v[96:111], v[140:143], v[146:149], v[96:111]
	s_cmp_eq_u32 s2, 0
	s_cbranch_scc1 .Latt_nopv_b0
	ds_read_b64_tr_b16 v[202:203], v184 offset:34816
	ds_read_b64_tr_b16 v[206:207], v184 offset:34880
	ds_read_b64_tr_b16 v[210:211], v184 offset:34944
	ds_read_b64_tr_b16 v[214:215], v184 offset:35008
	ds_read_b64_tr_b16 v[204:205], v184 offset:37376
	ds_read_b64_tr_b16 v[208:209], v184 offset:37440
	ds_read_b64_tr_b16 v[212:213], v184 offset:37504
	ds_read_b64_tr_b16 v[216:217], v184 offset:37568
	ds_read_b64_tr_b16 v[218:219], v184 offset:39936
	ds_read_b64_tr_b16 v[222:223], v184 offset:40000
	ds_read_b64_tr_b16 v[226:227], v184 offset:40064
	ds_read_b64_tr_b16 v[230:231], v184 offset:40128
	ds_read_b64_tr_b16 v[220:221], v184 offset:42496
	ds_read_b64_tr_b16 v[224:225], v184 offset:42560
	ds_read_b64_tr_b16 v[228:229], v184 offset:42624
	s_waitcnt lgkmcnt(14)
	ds_read_b64_tr_b16 v[232:233], v184 offset:42688
	s_waitcnt lgkmcnt(8)
	v_mfma_f32_32x32x16_bf16 v[32:47], v[112:115], v[202:205], v[32:47]
	v_mfma_f32_32x32x16_bf16 v[48:63], v[112:115], v[206:209], v[48:63]
	v_mfma_f32_32x32x16_bf16 v[0:15], v[112:115], v[210:213], v[0:15]
	v_mfma_f32_32x32x16_bf16 v[16:31], v[112:115], v[214:217], v[16:31]
	ds_read_b64_tr_b16 v[202:203], v184 offset:45056
	ds_read_b64_tr_b16 v[206:207], v184 offset:45120
	ds_read_b64_tr_b16 v[210:211], v184 offset:45184
	ds_read_b64_tr_b16 v[214:215], v184 offset:45248
	ds_read_b64_tr_b16 v[204:205], v184 offset:47616
	ds_read_b64_tr_b16 v[208:209], v184 offset:47680
	ds_read_b64_tr_b16 v[212:213], v184 offset:47744
	s_waitcnt lgkmcnt(14)
	ds_read_b64_tr_b16 v[216:217], v184 offset:47808
	s_waitcnt lgkmcnt(8)
	v_mfma_f32_32x32x16_bf16 v[32:47], v[116:119], v[218:221], v[32:47]
	v_mfma_f32_32x32x16_bf16 v[48:63], v[116:119], v[222:225], v[48:63]
	v_mfma_f32_32x32x16_bf16 v[0:15], v[116:119], v[226:229], v[0:15]
	v_mfma_f32_32x32x16_bf16 v[16:31], v[116:119], v[230:233], v[16:31]
	ds_read_b64_tr_b16 v[218:219], v184 offset:50176
	ds_read_b64_tr_b16 v[222:223], v184 offset:50240
	ds_read_b64_tr_b16 v[226:227], v184 offset:50304
	ds_read_b64_tr_b16 v[230:231], v184 offset:50368
	ds_read_b64_tr_b16 v[220:221], v184 offset:52736
	ds_read_b64_tr_b16 v[224:225], v184 offset:52800
	ds_read_b64_tr_b16 v[228:229], v184 offset:52864
	s_waitcnt lgkmcnt(14)
	ds_read_b64_tr_b16 v[232:233], v184 offset:52928
	s_waitcnt lgkmcnt(8)
	v_mfma_f32_32x32x16_bf16 v[32:47], v[120:123], v[202:205], v[32:47]
	v_mfma_f32_32x32x16_bf16 v[48:63], v[120:123], v[206:209], v[48:63]
	v_mfma_f32_32x32x16_bf16 v[0:15], v[120:123], v[210:213], v[0:15]
	v_mfma_f32_32x32x16_bf16 v[16:31], v[120:123], v[214:217], v[16:31]
	s_waitcnt lgkmcnt(0)
	v_mfma_f32_32x32x16_bf16 v[32:47], v[124:127], v[218:221], v[32:47]
	v_mfma_f32_32x32x16_bf16 v[48:63], v[124:127], v[222:225], v[48:63]
	v_mfma_f32_32x32x16_bf16 v[0:15], v[124:127], v[226:229], v[0:15]
	v_mfma_f32_32x32x16_bf16 v[16:31], v[124:127], v[230:233], v[16:31]
.Latt_nopv_b0:
	s_waitcnt lgkmcnt(0)
	s_nop 7
	s_nop 7
	v_exp_f32_e32 v80, v80
	v_exp_f32_e32 v96, v96
	v_exp_f32_e32 v81, v81
	v_exp_f32_e32 v97, v97
	v_exp_f32_e32 v82, v82
	v_exp_f32_e32 v98, v98
	v_exp_f32_e32 v83, v83
	v_exp_f32_e32 v99, v99
	v_exp_f32_e32 v84, v84
	v_exp_f32_e32 v100, v100
	v_exp_f32_e32 v85, v85
	v_exp_f32_e32 v101, v101
	v_exp_f32_e32 v86, v86
	v_exp_f32_e32 v102, v102
	v_exp_f32_e32 v87, v87
	v_exp_f32_e32 v103, v103
	v_exp_f32_e32 v88, v88
	v_exp_f32_e32 v104, v104
	v_exp_f32_e32 v89, v89
	v_exp_f32_e32 v105, v105
	v_exp_f32_e32 v90, v90
	v_exp_f32_e32 v106, v106
	v_exp_f32_e32 v91, v91
	v_exp_f32_e32 v107, v107
	v_exp_f32_e32 v92, v92
	v_exp_f32_e32 v108, v108
	v_exp_f32_e32 v93, v93
	v_exp_f32_e32 v109, v109
	v_exp_f32_e32 v94, v94
	v_exp_f32_e32 v110, v110
	v_exp_f32_e32 v95, v95
	v_exp_f32_e32 v111, v111
	v_cvt_pk_bf16_f32 v112, v80, v81
	v_cvt_pk_bf16_f32 v113, v82, v83
	v_cvt_pk_bf16_f32 v114, v84, v85
	v_cvt_pk_bf16_f32 v115, v86, v87
	v_cvt_pk_bf16_f32 v116, v88, v89
	v_cvt_pk_bf16_f32 v117, v90, v91
	v_cvt_pk_bf16_f32 v118, v92, v93
	v_cvt_pk_bf16_f32 v119, v94, v95
	v_cvt_pk_bf16_f32 v120, v96, v97
	v_cvt_pk_bf16_f32 v121, v98, v99
	v_cvt_pk_bf16_f32 v122, v100, v101
	v_cvt_pk_bf16_f32 v123, v102, v103
	v_cvt_pk_bf16_f32 v124, v104, v105
	v_cvt_pk_bf16_f32 v125, v106, v107
	v_cvt_pk_bf16_f32 v126, v108, v109
	v_cvt_pk_bf16_f32 v127, v110, v111
	v_add_f32_e32 v80, v80, v96
	v_add_f32_e32 v81, v81, v97
	v_add_f32_e32 v82, v82, v98
	v_add_f32_e32 v83, v83, v99
	v_add_f32_e32 v84, v84, v100
	v_add_f32_e32 v85, v85, v101
	v_add_f32_e32 v86, v86, v102
	v_add_f32_e32 v87, v87, v103
	v_add_f32_e32 v88, v88, v104
	v_add_f32_e32 v89, v89, v105
	v_add_f32_e32 v90, v90, v106
	v_add_f32_e32 v91, v91, v107
	v_add_f32_e32 v92, v92, v108
	v_add_f32_e32 v93, v93, v109
	v_add_f32_e32 v94, v94, v110
	v_add_f32_e32 v95, v95, v111
	v_add_f32_e32 v80, v80, v88
	v_add_f32_e32 v81, v81, v89
	v_add_f32_e32 v82, v82, v90
	v_add_f32_e32 v83, v83, v91
	v_add_f32_e32 v84, v84, v92
	v_add_f32_e32 v85, v85, v93
	v_add_f32_e32 v86, v86, v94
	v_add_f32_e32 v87, v87, v95
	v_add_f32_e32 v80, v80, v84
	v_add_f32_e32 v81, v81, v85
	v_add_f32_e32 v82, v82, v86
	v_add_f32_e32 v83, v83, v87
	v_add_f32_e32 v80, v80, v82
	v_add_f32_e32 v81, v81, v83
	v_add_f32_e32 v80, v80, v81
	v_add_f32_e32 v201, v201, v80
	s_barrier
	s_add_i32 s5, s2, 4
	s_cmp_ge_u32 s5, 36
	s_cbranch_scc1 .Latt_nokload_b1
	s_cmp_lt_u32 s5, 4
	s_cselect_b32 s15, s42, s43
	s_lshl_b32 s45, s5, 6
	s_add_i32 s15, s15, s45
	s_lshl_b32 s15, s15, 10
	v_add_u32_e32 v186, s15, v178
	v_add_u32_e32 v187, 0x8000, v186
	global_load_dwordx4 v[162:165], v186, s[72:73]
	global_load_dwordx4 v[166:169], v187, s[72:73]

; #define AT_LOADK(t) do { const int kr_ = AT_KROW(t); _Pragma("unroll") for (int i_ = 0; i_ < 2; ++i_) kreg[i_] = *(const u32x4*)(Kp + (size_t)(kr_ + prow0 + 32 * i_) * 512 + pch * 8); } while (0)
; #define AT_LOADV(t) do { const int kr_ = AT_KROW(t); _Pragma("unroll") for (int i_ = 0; i_ < 2; ++i_) vreg[i_] = *(const u32x4*)(Vp + (size_t)(kr_ + prow0 + 32 * i_) * 512 + pch * 8); } while (0)
; __device__ __forceinline__ void attn_unit(const Frame& F, int layer, int qrow0, int ntiles, int b, int head, float lam, float m2, float lam_init) {
;     ...
;         if (t + 2 < ntiles) AT_LOADK(t + 2);
;         if (t + 1 < ntiles) AT_LOADV(t + 1);
.Latt_novload_b1:
	s_add_i32 s5, s2, 4
	s_cmp_ge_u32 s5, 36
	s_cbranch_scc1 .Latt_drain_b1
	s_waitcnt vmcnt(4)
	s_branch .Latt_stage_b1

; __device__ __forceinline__ unsigned pk2(float lo, float hi) { f32x2_t v = {lo, hi}; bf16x2_t b = __builtin_convertvector(v, bf16x2_t); return __builtin_bit_cast(unsigned, b); }
; __device__ __forceinline__ void lds_barrier() { asm volatile("s_waitcnt lgkmcnt(0)" ::: "memory"); __builtin_amdgcn_s_barrier(); asm volatile("" ::: "memory"); }
; #define AT_LOADK(t) do { const int kr_ = AT_KROW(t); _Pragma("unroll") for (int i_ = 0; i_ < 2; ++i_) kreg[i_] = *(const u32x4*)(Kp + (size_t)(kr_ + prow0 + 32 * i_) * 512 + pch * 8); } while (0)
; #define AT_LOADV(t) do { const int kr_ = AT_KROW(t); _Pragma("unroll") for (int i_ = 0; i_ < 2; ++i_) vreg[i_] = *(const u32x4*)(Vp + (size_t)(kr_ + prow0 + 32 * i_) * 512 + pch * 8); } while (0)
; #define AT_STOREK(st) do { _Pragma("unroll") for (int i_ = 0; i_ < 2; ++i_) *(LAS u32x4*)(L + AT_K + (st) * AT_KBYTES + (prow0 + 32 * i_) * AT_KSTR + pch * 16) = kreg[i_]; } while (0)
; #define AT_STOREV(st) do { _Pragma("unroll") for (int i_ = 0; i_ < 2; ++i_) *(LAS u32x4*)(L + AT_V + (st) * AT_VBYTES + (prow0 + 32 * i_) * AT_VSTR + pch * 16) = vreg[i_]; } while (0)
; __device__ __forceinline__ void attn_unit(const Frame& F, int layer, int qrow0, int ntiles, int b, int head, float lam, float m2, float lam_init) {
;     ...
;     if (wave >= 4) __builtin_amdgcn_s_setprio(1);
;     AT_LOADK(0); AT_LOADV(0); AT_STOREK(0); AT_STOREV(0);
;     if (ntiles > 1) { AT_LOADK(1); AT_STOREK(1); }
;     __syncthreads();
;     f32x16 sa, sb, na, nb;
;     AT_QK(sa, sb, 0);
;     lds_barrier();
;     for (int t = 0; t < ntiles; ++t) {
;         if (t + 2 < ntiles) AT_LOADK(t + 2);
;         if (t + 1 < ntiles) AT_LOADV(t + 1);
;         if (t + 1 < ntiles) AT_QK(na, nb, (t + 1) & 1);
;         float ls = 0.f;
; #pragma unroll
;         for (int i = 0; i < 16; ++i) { sa[i] = __builtin_amdgcn_exp2f(sa[i]); sb[i] = __builtin_amdgcn_exp2f(sb[i]); ls += sa[i] + sb[i]; }
;         lsum += ls;
;         bf16x8 pk[4];
;         { u32x4 w0, w1, w2, w3;
; #pragma unroll
;           for (int i = 0; i < 4; ++i) { w0[i] = pk2(sa[2 * i], sa[2 * i + 1]); w1[i] = pk2(sa[8 + 2 * i], sa[9 + 2 * i]); w2[i] = pk2(sb[2 * i], sb[2 * i + 1]); w3[i] = pk2(sb[8 + 2 * i], sb[9 + 2 * i]); }
;           pk[0] = __builtin_bit_cast(bf16x8, w0); pk[1] = __builtin_bit_cast(bf16x8, w1); pk[2] = __builtin_bit_cast(bf16x8, w2); pk[3] = __builtin_bit_cast(bf16x8, w3); }
.Latt_vdone_b1:
	ds_read_b128 v[128:131], v197 offset:17408
	ds_read_b128 v[132:135], v197 offset:26112
	ds_read_b128 v[136:139], v197 offset:17440
	ds_read_b128 v[140:143], v197 offset:26144
	s_waitcnt lgkmcnt(2)
	v_mfma_f32_32x32x16_bf16 v[80:95], v[128:131], v[158:161], v[64:79]
	v_mfma_f32_32x32x16_bf16 v[96:111], v[132:135], v[158:161], v[64:79]
	ds_read_b128 v[128:131], v197 offset:17472
	ds_read_b128 v[132:135], v197 offset:26176
	s_waitcnt lgkmcnt(2)
	v_mfma_f32_32x32x16_bf16 v[80:95], v[136:139], v[154:157], v[80:95]
	v_mfma_f32_32x32x16_bf16 v[96:111], v[140:143], v[154:157], v[96:111]
	ds_read_b128 v[136:139], v197 offset:17504
	ds_read_b128 v[140:143], v197 offset:26208
	s_waitcnt lgkmcnt(2)
	v_mfma_f32_32x32x16_bf16 v[80:95], v[128:131], v[150:153], v[80:95]
	v_mfma_f32_32x32x16_bf16 v[96:111], v[132:135], v[150:153], v[96:111]
	s_waitcnt lgkmcnt(0)
	v_mfma_f32_32x32x16_bf16 v[80:95], v[136:139], v[146:149], v[80:95]
	v_mfma_f32_32x32x16_bf16 v[96:111], v[140:143], v[146:149], v[96:111]
	ds_read_b64_tr_b16 v[202:203], v196 offset:34816
	ds_read_b64_tr_b16 v[206:207], v196 offset:34880
	ds_read_b64_tr_b16 v[210:211], v196 offset:34944
	ds_read_b64_tr_b16 v[214:215], v196 offset:35008
	ds_read_b64_tr_b16 v[204:205], v196 offset:37376
	ds_read_b64_tr_b16 v[208:209], v196 offset:37440
	ds_read_b64_tr_b16 v[212:213], v196 offset:37504
	ds_read_b64_tr_b16 v[216:217], v196 offset:37568
	ds_read_b64_tr_b16 v[218:219], v196 offset:39936
	ds_read_b64_tr_b16 v[222:223], v196 offset:40000
	ds_read_b64_tr_b16 v[226:227], v196 offset:40064
	ds_read_b64_tr_b16 v[230:231], v196 offset:40128
	ds_read_b64_tr_b16 v[220:221], v196 offset:42496
	ds_read_b64_tr_b16 v[224:225], v196 offset:42560
	ds_read_b64_tr_b16 v[228:229], v196 offset:42624
	s_waitcnt lgkmcnt(14)
	ds_read_b64_tr_b16 v[232:233], v196 offset:42688
	s_waitcnt lgkmcnt(8)
	v_mfma_f32_32x32x16_bf16 v[32:47], v[112:115], v[202:205], v[32:47]
	v_mfma_f32_32x32x16_bf16 v[48:63], v[112:115], v[206:209], v[48:63]
	v_mfma_f32_32x32x16_bf16 v[0:15], v[112:115], v[210:213], v[0:15]
	v_mfma_f32_32x32x16_bf16 v[16:31], v[112:115], v[214:217], v[16:31]
	ds_read_b64_tr_b16 v[202:203], v196 offset:45056
	ds_read_b64_tr_b16 v[206:207], v196 offset:45120
	ds_read_b64_tr_b16 v[210:211], v196 offset:45184
	ds_read_b64_tr_b16 v[214:215], v196 offset:45248
	ds_read_b64_tr_b16 v[204:205], v196 offset:47616
	ds_read_b64_tr_b16 v[208:209], v196 offset:47680
	ds_read_b64_tr_b16 v[212:213], v196 offset:47744
	s_waitcnt lgkmcnt(14)
	ds_read_b64_tr_b16 v[216:217], v196 offset:47808
	s_waitcnt lgkmcnt(8)
	v_mfma_f32_32x32x16_bf16 v[32:47], v[116:119], v[218:221], v[32:47]
	v_mfma_f32_32x32x16_bf16 v[48:63], v[116:119], v[222:225], v[48:63]
	v_mfma_f32_32x32x16_bf16 v[0:15], v[116:119], v[226:229], v[0:15]
	v_mfma_f32_32x32x16_bf16 v[16:31], v[116:119], v[230:233], v[16:31]
	ds_read_b64_tr_b16 v[218:219], v196 offset:50176
	ds_read_b64_tr_b16 v[222:223], v196 offset:50240
	ds_read_b64_tr_b16 v[226:227], v196 offset:50304
	ds_read_b64_tr_b16 v[230:231], v196 offset:50368
	ds_read_b64_tr_b16 v[220:221], v196 offset:52736
	ds_read_b64_tr_b16 v[224:225], v196 offset:52800
	ds_read_b64_tr_b16 v[228:229], v196 offset:52864
	s_waitcnt lgkmcnt(14)
	ds_read_b64_tr_b16 v[232:233], v196 offset:52928
	s_waitcnt lgkmcnt(8)
	v_mfma_f32_32x32x16_bf16 v[32:47], v[120:123], v[202:205], v[32:47]
	v_mfma_f32_32x32x16_bf16 v[48:63], v[120:123], v[206:209], v[48:63]
	v_mfma_f32_32x32x16_bf16 v[0:15], v[120:123], v[210:213], v[0:15]
	v_mfma_f32_32x32x16_bf16 v[16:31], v[120:123], v[214:217], v[16:31]
	s_waitcnt lgkmcnt(0)
	v_mfma_f32_32x32x16_bf16 v[32:47], v[124:127], v[218:221], v[32:47]
	v_mfma_f32_32x32x16_bf16 v[48:63], v[124:127], v[222:225], v[48:63]
	v_mfma_f32_32x32x16_bf16 v[0:15], v[124:127], v[226:229], v[0:15]
	v_mfma_f32_32x32x16_bf16 v[16:31], v[124:127], v[230:233], v[16:31]
	s_nop 7
	s_nop 7
	v_exp_f32_e32 v80, v80
	v_exp_f32_e32 v96, v96
	v_exp_f32_e32 v81, v81
	v_exp_f32_e32 v97, v97
	v_exp_f32_e32 v82, v82
	v_exp_f32_e32 v98, v98
	v_exp_f32_e32 v83, v83
	v_exp_f32_e32 v99, v99
	v_exp_f32_e32 v84, v84
	v_exp_f32_e32 v100, v100
	v_exp_f32_e32 v85, v85
	v_exp_f32_e32 v101, v101
	v_exp_f32_e32 v86, v86
	v_exp_f32_e32 v102, v102
	v_exp_f32_e32 v87, v87
	v_exp_f32_e32 v103, v103
	v_exp_f32_e32 v88, v88
	v_exp_f32_e32 v104, v104
	v_exp_f32_e32 v89, v89
	v_exp_f32_e32 v105, v105
	v_exp_f32_e32 v90, v90
	v_exp_f32_e32 v106, v106
	v_exp_f32_e32 v91, v91
	v_exp_f32_e32 v107, v107
	v_exp_f32_e32 v92, v92
	v_exp_f32_e32 v108, v108
	v_exp_f32_e32 v93, v93
	v_exp_f32_e32 v109, v109
	v_exp_f32_e32 v94, v94
	v_exp_f32_e32 v110, v110
	v_exp_f32_e32 v95, v95
	v_exp_f32_e32 v111, v111
	v_cvt_pk_bf16_f32 v112, v80, v81
	v_cvt_pk_bf16_f32 v113, v82, v83
	v_cvt_pk_bf16_f32 v114, v84, v85
	v_cvt_pk_bf16_f32 v115, v86, v87
	v_cvt_pk_bf16_f32 v116, v88, v89
	v_cvt_pk_bf16_f32 v117, v90, v91
	v_cvt_pk_bf16_f32 v118, v92, v93
	v_cvt_pk_bf16_f32 v119, v94, v95
	v_cvt_pk_bf16_f32 v120, v96, v97
	v_cvt_pk_bf16_f32 v121, v98, v99
	v_cvt_pk_bf16_f32 v122, v100, v101
	v_cvt_pk_bf16_f32 v123, v102, v103
	v_cvt_pk_bf16_f32 v124, v104, v105
	v_cvt_pk_bf16_f32 v125, v106, v107
	v_cvt_pk_bf16_f32 v126, v108, v109
	v_cvt_pk_bf16_f32 v127, v110, v111
	v_add_f32_e32 v80, v80, v96
	v_add_f32_e32 v81, v81, v97
	v_add_f32_e32 v82, v82, v98
	v_add_f32_e32 v83, v83, v99
	v_add_f32_e32 v84, v84, v100
	v_add_f32_e32 v85, v85, v101
	v_add_f32_e32 v86, v86, v102
	v_add_f32_e32 v87, v87, v103
	v_add_f32_e32 v88, v88, v104
	v_add_f32_e32 v89, v89, v105
	v_add_f32_e32 v90, v90, v106
	v_add_f32_e32 v91, v91, v107
	v_add_f32_e32 v92, v92, v108
	v_add_f32_e32 v93, v93, v109
	v_add_f32_e32 v94, v94, v110
	v_add_f32_e32 v95, v95, v111
	v_add_f32_e32 v80, v80, v88
	v_add_f32_e32 v81, v81, v89
	v_add_f32_e32 v82, v82, v90
	v_add_f32_e32 v83, v83, v91
	v_add_f32_e32 v84, v84, v92
	v_add_f32_e32 v85, v85, v93
	v_add_f32_e32 v86, v86, v94
	v_add_f32_e32 v87, v87, v95
	v_add_f32_e32 v80, v80, v84
	v_add_f32_e32 v81, v81, v85
	v_add_f32_e32 v82, v82, v86
	v_add_f32_e32 v83, v83, v87
	v_add_f32_e32 v80, v80, v82
	v_add_f32_e32 v81, v81, v83
	v_add_f32_e32 v80, v80, v81
	v_add_f32_e32 v201, v201, v80
	s_barrier
	s_add_i32 s5, s2, 5
	s_cmp_ge_u32 s5, 36
	s_cbranch_scc1 .Latt_nokload_b2
	s_cmp_lt_u32 s5, 4
	s_cselect_b32 s15, s42, s43
	s_lshl_b32 s45, s5, 6
	s_add_i32 s15, s15, s45
	s_lshl_b32 s15, s15, 10
	v_add_u32_e32 v186, s15, v178
	v_add_u32_e32 v187, 0x8000, v186
	global_load_dwordx4 v[234:237], v186, s[72:73]
	global_load_dwordx4 v[238:241], v187, s[72:73]

; #define AT_LOADK(t) do { const int kr_ = AT_KROW(t); _Pragma("unroll") for (int i_ = 0; i_ < 2; ++i_) kreg[i_] = *(const u32x4*)(Kp + (size_t)(kr_ + prow0 + 32 * i_) * 512 + pch * 8); } while (0)
; #define AT_LOADV(t) do { const int kr_ = AT_KROW(t); _Pragma("unroll") for (int i_ = 0; i_ < 2; ++i_) vreg[i_] = *(const u32x4*)(Vp + (size_t)(kr_ + prow0 + 32 * i_) * 512 + pch * 8); } while (0)
; __device__ __forceinline__ void attn_unit(const Frame& F, int layer, int qrow0, int ntiles, int b, int head, float lam, float m2, float lam_init) {
;     ...
;         if (t + 2 < ntiles) AT_LOADK(t + 2);
;         if (t + 1 < ntiles) AT_LOADV(t + 1);
.Latt_novload_b2:
	s_add_i32 s5, s2, 5
	s_cmp_ge_u32 s5, 36
	s_cbranch_scc1 .Latt_drain_b2
	s_waitcnt vmcnt(4)
	s_branch .Latt_stage_b2

; __device__ __forceinline__ void attn_unit(const Frame& F, int layer, int qrow0, int ntiles, int b, int head, float lam, float m2, float lam_init) {
;     ...
;     if (wave >= 4) __builtin_amdgcn_s_setprio(1);
;     AT_LOADK(0); AT_LOADV(0); AT_STOREK(0); AT_STOREV(0);
;     if (ntiles > 1) { AT_LOADK(1); AT_STOREK(1); }
;     __syncthreads();
;     f32x16 sa, sb, na, nb;
;     AT_QK(sa, sb, 0);
;     lds_barrier();
;     for (int t = 0; t < ntiles; ++t) {
;         if (t + 2 < ntiles) AT_LOADK(t + 2);
;         if (t + 1 < ntiles) AT_LOADV(t + 1);
;         if (t + 1 < ntiles) AT_QK(na, nb, (t + 1) & 1);
;         float ls = 0.f;
; #pragma unroll
;         for (int i = 0; i < 16; ++i) { sa[i] = __builtin_amdgcn_exp2f(sa[i]); sb[i] = __builtin_amdgcn_exp2f(sb[i]); ls += sa[i] + sb[i]; }
;         lsum += ls;
;         bf16x8 pk[4];
;         { u32x4 w0, w1, w2, w3;
; #pragma unroll
;           for (int i = 0; i < 4; ++i) { w0[i] = pk2(sa[2 * i], sa[2 * i + 1]); w1[i] = pk2(sa[8 + 2 * i], sa[9 + 2 * i]); w2[i] = pk2(sb[2 * i], sb[2 * i + 1]); w3[i] = pk2(sb[8 + 2 * i], sb[9 + 2 * i]); }
;           pk[0] = __builtin_bit_cast(bf16x8, w0); pk[1] = __builtin_bit_cast(bf16x8, w1); pk[2] = __builtin_bit_cast(bf16x8, w2); pk[3] = __builtin_bit_cast(bf16x8, w3); }
;         LAS const unsigned char* Vt = L + AT_V + (t & 1) * AT_VBYTES;
;         __builtin_amdgcn_sched_barrier(0);
;         bf16x8 vfa[4], vfb[4];
; #pragma unroll
;         for (int j = 0; j < 4; ++j) vfa[j] = frag_tr_acc(Vt, AT_VSTR, 0, 32 * j, lane);
; #pragma unroll
;         for (int ks = 0; ks < 4; ks += 2) {
; #pragma unroll
;             for (int j = 0; j < 4; ++j) vfb[j] = frag_tr_acc(Vt, AT_VSTR, 16 * (ks + 1), 32 * j, lane);
; #pragma unroll
;             for (int j = 0; j < 4; ++j) o[j] = MFMA32(pk[ks], vfa[j], o[j]);
;             __builtin_amdgcn_sched_barrier(0);
;             if (ks + 2 < 4) {
; #pragma unroll
;                 for (int j = 0; j < 4; ++j) vfa[j] = frag_tr_acc(Vt, AT_VSTR, 16 * (ks + 2), 32 * j, lane);
;             }
; #pragma unroll
;             for (int j = 0; j < 4; ++j) o[j] = MFMA32(pk[ks + 1], vfb[j], o[j]);
;             __builtin_amdgcn_sched_barrier(0);
;         }
;         if (t + 2 < ntiles) AT_STOREK(t & 1);
;         if (t + 1 < ntiles) AT_STOREV((t + 1) & 1);
;         __syncthreads();
;         sa = na; sb = nb;
;     }
.Latt_vdone_b2:
	ds_read_b128 v[128:131], v190 offset:0
	ds_read_b128 v[132:135], v190 offset:8704
	ds_read_b128 v[136:139], v190 offset:32
	ds_read_b128 v[140:143], v190 offset:8736
	s_waitcnt lgkmcnt(2)
	v_mfma_f32_32x32x16_bf16 v[80:95], v[128:131], v[158:161], v[64:79]
	v_mfma_f32_32x32x16_bf16 v[96:111], v[132:135], v[158:161], v[64:79]
	ds_read_b128 v[128:131], v190 offset:64
	ds_read_b128 v[132:135], v190 offset:8768
	s_waitcnt lgkmcnt(2)
	v_mfma_f32_32x32x16_bf16 v[80:95], v[136:139], v[154:157], v[80:95]
	v_mfma_f32_32x32x16_bf16 v[96:111], v[140:143], v[154:157], v[96:111]
	ds_read_b128 v[136:139], v190 offset:96
	ds_read_b128 v[140:143], v190 offset:8800
	s_waitcnt lgkmcnt(2)
	v_mfma_f32_32x32x16_bf16 v[80:95], v[128:131], v[150:153], v[80:95]
	v_mfma_f32_32x32x16_bf16 v[96:111], v[132:135], v[150:153], v[96:111]
	s_waitcnt lgkmcnt(0)
	v_mfma_f32_32x32x16_bf16 v[80:95], v[136:139], v[146:149], v[80:95]
	v_mfma_f32_32x32x16_bf16 v[96:111], v[140:143], v[146:149], v[96:111]
	ds_read_b64_tr_b16 v[202:203], v191 offset:34816
	ds_read_b64_tr_b16 v[206:207], v191 offset:34880
	ds_read_b64_tr_b16 v[210:211], v191 offset:34944
	ds_read_b64_tr_b16 v[214:215], v191 offset:35008
	ds_read_b64_tr_b16 v[204:205], v191 offset:37376
	ds_read_b64_tr_b16 v[208:209], v191 offset:37440
	ds_read_b64_tr_b16 v[212:213], v191 offset:37504
	ds_read_b64_tr_b16 v[216:217], v191 offset:37568
	ds_read_b64_tr_b16 v[218:219], v191 offset:39936
	ds_read_b64_tr_b16 v[222:223], v191 offset:40000
	ds_read_b64_tr_b16 v[226:227], v191 offset:40064
	ds_read_b64_tr_b16 v[230:231], v191 offset:40128
	ds_read_b64_tr_b16 v[220:221], v191 offset:42496
	ds_read_b64_tr_b16 v[224:225], v191 offset:42560
	ds_read_b64_tr_b16 v[228:229], v191 offset:42624
	s_waitcnt lgkmcnt(14)
	ds_read_b64_tr_b16 v[232:233], v191 offset:42688
	s_waitcnt lgkmcnt(8)
	v_mfma_f32_32x32x16_bf16 v[32:47], v[112:115], v[202:205], v[32:47]
	v_mfma_f32_32x32x16_bf16 v[48:63], v[112:115], v[206:209], v[48:63]
	v_mfma_f32_32x32x16_bf16 v[0:15], v[112:115], v[210:213], v[0:15]
	v_mfma_f32_32x32x16_bf16 v[16:31], v[112:115], v[214:217], v[16:31]
	ds_read_b64_tr_b16 v[202:203], v191 offset:45056
	ds_read_b64_tr_b16 v[206:207], v191 offset:45120
	ds_read_b64_tr_b16 v[210:211], v191 offset:45184
	ds_read_b64_tr_b16 v[214:215], v191 offset:45248
	ds_read_b64_tr_b16 v[204:205], v191 offset:47616
	ds_read_b64_tr_b16 v[208:209], v191 offset:47680
	ds_read_b64_tr_b16 v[212:213], v191 offset:47744
	s_waitcnt lgkmcnt(14)
	ds_read_b64_tr_b16 v[216:217], v191 offset:47808
	s_waitcnt lgkmcnt(8)
	v_mfma_f32_32x32x16_bf16 v[32:47], v[116:119], v[218:221], v[32:47]
	v_mfma_f32_32x32x16_bf16 v[48:63], v[116:119], v[222:225], v[48:63]
	v_mfma_f32_32x32x16_bf16 v[0:15], v[116:119], v[226:229], v[0:15]
	v_mfma_f32_32x32x16_bf16 v[16:31], v[116:119], v[230:233], v[16:31]
	ds_read_b64_tr_b16 v[218:219], v191 offset:50176
	ds_read_b64_tr_b16 v[222:223], v191 offset:50240
	ds_read_b64_tr_b16 v[226:227], v191 offset:50304
	ds_read_b64_tr_b16 v[230:231], v191 offset:50368
	ds_read_b64_tr_b16 v[220:221], v191 offset:52736
	ds_read_b64_tr_b16 v[224:225], v191 offset:52800
	ds_read_b64_tr_b16 v[228:229], v191 offset:52864
	s_waitcnt lgkmcnt(14)
	ds_read_b64_tr_b16 v[232:233], v191 offset:52928
	s_waitcnt lgkmcnt(8)
	v_mfma_f32_32x32x16_bf16 v[32:47], v[120:123], v[202:205], v[32:47]
	v_mfma_f32_32x32x16_bf16 v[48:63], v[120:123], v[206:209], v[48:63]
	v_mfma_f32_32x32x16_bf16 v[0:15], v[120:123], v[210:213], v[0:15]
	v_mfma_f32_32x32x16_bf16 v[16:31], v[120:123], v[214:217], v[16:31]
	s_waitcnt lgkmcnt(0)
	v_mfma_f32_32x32x16_bf16 v[32:47], v[124:127], v[218:221], v[32:47]
	v_mfma_f32_32x32x16_bf16 v[48:63], v[124:127], v[222:225], v[48:63]
	v_mfma_f32_32x32x16_bf16 v[0:15], v[124:127], v[226:229], v[0:15]
	v_mfma_f32_32x32x16_bf16 v[16:31], v[124:127], v[230:233], v[16:31]
	s_nop 7
	s_nop 7
	v_exp_f32_e32 v80, v80
	v_exp_f32_e32 v96, v96
	v_exp_f32_e32 v81, v81
	v_exp_f32_e32 v97, v97
	v_exp_f32_e32 v82, v82
	v_exp_f32_e32 v98, v98
	v_exp_f32_e32 v83, v83
	v_exp_f32_e32 v99, v99
	v_exp_f32_e32 v84, v84
	v_exp_f32_e32 v100, v100
	v_exp_f32_e32 v85, v85
	v_exp_f32_e32 v101, v101
	v_exp_f32_e32 v86, v86
	v_exp_f32_e32 v102, v102
	v_exp_f32_e32 v87, v87
	v_exp_f32_e32 v103, v103
	v_exp_f32_e32 v88, v88
	v_exp_f32_e32 v104, v104
	v_exp_f32_e32 v89, v89
	v_exp_f32_e32 v105, v105
	v_exp_f32_e32 v90, v90
	v_exp_f32_e32 v106, v106
	v_exp_f32_e32 v91, v91
	v_exp_f32_e32 v107, v107
	v_exp_f32_e32 v92, v92
	v_exp_f32_e32 v108, v108
	v_exp_f32_e32 v93, v93
	v_exp_f32_e32 v109, v109
	v_exp_f32_e32 v94, v94
	v_exp_f32_e32 v110, v110
	v_exp_f32_e32 v95, v95
	v_exp_f32_e32 v111, v111
	v_cvt_pk_bf16_f32 v112, v80, v81
	v_cvt_pk_bf16_f32 v113, v82, v83
	v_cvt_pk_bf16_f32 v114, v84, v85
	v_cvt_pk_bf16_f32 v115, v86, v87
	v_cvt_pk_bf16_f32 v116, v88, v89
	v_cvt_pk_bf16_f32 v117, v90, v91
	v_cvt_pk_bf16_f32 v118, v92, v93
	v_cvt_pk_bf16_f32 v119, v94, v95
	v_cvt_pk_bf16_f32 v120, v96, v97
	v_cvt_pk_bf16_f32 v121, v98, v99
	v_cvt_pk_bf16_f32 v122, v100, v101
	v_cvt_pk_bf16_f32 v123, v102, v103
	v_cvt_pk_bf16_f32 v124, v104, v105
	v_cvt_pk_bf16_f32 v125, v106, v107
	v_cvt_pk_bf16_f32 v126, v108, v109
	v_cvt_pk_bf16_f32 v127, v110, v111
	v_add_f32_e32 v80, v80, v96
	v_add_f32_e32 v81, v81, v97
	v_add_f32_e32 v82, v82, v98
	v_add_f32_e32 v83, v83, v99
	v_add_f32_e32 v84, v84, v100
	v_add_f32_e32 v85, v85, v101
	v_add_f32_e32 v86, v86, v102
	v_add_f32_e32 v87, v87, v103
	v_add_f32_e32 v88, v88, v104
	v_add_f32_e32 v89, v89, v105
	v_add_f32_e32 v90, v90, v106
	v_add_f32_e32 v91, v91, v107
	v_add_f32_e32 v92, v92, v108
	v_add_f32_e32 v93, v93, v109
	v_add_f32_e32 v94, v94, v110
	v_add_f32_e32 v95, v95, v111
	v_add_f32_e32 v80, v80, v88
	v_add_f32_e32 v81, v81, v89
	v_add_f32_e32 v82, v82, v90
	v_add_f32_e32 v83, v83, v91
	v_add_f32_e32 v84, v84, v92
	v_add_f32_e32 v85, v85, v93
	v_add_f32_e32 v86, v86, v94
	v_add_f32_e32 v87, v87, v95
	v_add_f32_e32 v80, v80, v84
	v_add_f32_e32 v81, v81, v85
	v_add_f32_e32 v82, v82, v86
	v_add_f32_e32 v83, v83, v87
	v_add_f32_e32 v80, v80, v82
	v_add_f32_e32 v81, v81, v83
	v_add_f32_e32 v80, v80, v81
	v_add_f32_e32 v201, v201, v80
	s_barrier
	s_add_i32 s5, s2, 6
	s_cmp_ge_u32 s5, 36
	s_cbranch_scc1 .Latt_nokload_b3
	s_cmp_lt_u32 s5, 4
	s_cselect_b32 s15, s42, s43
	s_lshl_b32 s45, s5, 6
	s_add_i32 s15, s15, s45
	s_lshl_b32 s15, s15, 10
	v_add_u32_e32 v186, s15, v178
	v_add_u32_e32 v187, 0x8000, v186
	global_load_dwordx4 v[162:165], v186, s[72:73]
	global_load_dwordx4 v[166:169], v187, s[72:73]

; #define AT_LOADK(t) do { const int kr_ = AT_KROW(t); _Pragma("unroll") for (int i_ = 0; i_ < 2; ++i_) kreg[i_] = *(const u32x4*)(Kp + (size_t)(kr_ + prow0 + 32 * i_) * 512 + pch * 8); } while (0)
; #define AT_LOADV(t) do { const int kr_ = AT_KROW(t); _Pragma("unroll") for (int i_ = 0; i_ < 2; ++i_) vreg[i_] = *(const u32x4*)(Vp + (size_t)(kr_ + prow0 + 32 * i_) * 512 + pch * 8); } while (0)
; #define AT_STOREK(st) do { _Pragma("unroll") for (int i_ = 0; i_ < 2; ++i_) *(LAS u32x4*)(L + AT_K + (st) * AT_KBYTES + (prow0 + 32 * i_) * AT_KSTR + pch * 16) = kreg[i_]; } while (0)
; #define AT_STOREV(st) do { _Pragma("unroll") for (int i_ = 0; i_ < 2; ++i_) *(LAS u32x4*)(L + AT_V + (st) * AT_VBYTES + (prow0 + 32 * i_) * AT_VSTR + pch * 16) = vreg[i_]; } while (0)
; __device__ __forceinline__ void attn_unit(const Frame& F, int layer, int qrow0, int ntiles, int b, int head, float lam, float m2, float lam_init) {
;     ...
;     for (int t = 0; t < ntiles; ++t) {
;         if (t + 2 < ntiles) AT_LOADK(t + 2);
;         if (t + 1 < ntiles) AT_LOADV(t + 1);
;     ...
;         if (t + 2 < ntiles) AT_STOREK(t & 1);
;         if (t + 1 < ntiles) AT_STOREV((t + 1) & 1);
;         __syncthreads();
.Latt_novload_b3:
	s_add_i32 s5, s2, 6
	s_cmp_ge_u32 s5, 36
	s_cbranch_scc1 .Latt_drain_b3
	s_waitcnt vmcnt(4)
	s_branch .Latt_stage_b3

; __device__ __forceinline__ void attn_unit(const Frame& F, int layer, int qrow0, int ntiles, int b, int head, float lam, float m2, float lam_init) {
;     ...
;     if (wave >= 4) __builtin_amdgcn_s_setprio(1);
;     AT_LOADK(0); AT_LOADV(0); AT_STOREK(0); AT_STOREV(0);
;     if (ntiles > 1) { AT_LOADK(1); AT_STOREK(1); }
;     __syncthreads();
;     f32x16 sa, sb, na, nb;
;     AT_QK(sa, sb, 0);
;     lds_barrier();
;     for (int t = 0; t < ntiles; ++t) {
;         if (t + 2 < ntiles) AT_LOADK(t + 2);
;         if (t + 1 < ntiles) AT_LOADV(t + 1);
;         if (t + 1 < ntiles) AT_QK(na, nb, (t + 1) & 1);
;         float ls = 0.f;
; #pragma unroll
;         for (int i = 0; i < 16; ++i) { sa[i] = __builtin_amdgcn_exp2f(sa[i]); sb[i] = __builtin_amdgcn_exp2f(sb[i]); ls += sa[i] + sb[i]; }
;         lsum += ls;
;         bf16x8 pk[4];
;         { u32x4 w0, w1, w2, w3;
; #pragma unroll
;           for (int i = 0; i < 4; ++i) { w0[i] = pk2(sa[2 * i], sa[2 * i + 1]); w1[i] = pk2(sa[8 + 2 * i], sa[9 + 2 * i]); w2[i] = pk2(sb[2 * i], sb[2 * i + 1]); w3[i] = pk2(sb[8 + 2 * i], sb[9 + 2 * i]); }
;           pk[0] = __builtin_bit_cast(bf16x8, w0); pk[1] = __builtin_bit_cast(bf16x8, w1); pk[2] = __builtin_bit_cast(bf16x8, w2); pk[3] = __builtin_bit_cast(bf16x8, w3); }
;         LAS const unsigned char* Vt = L + AT_V + (t & 1) * AT_VBYTES;
;         __builtin_amdgcn_sched_barrier(0);
;         bf16x8 vfa[4], vfb[4];
; #pragma unroll
;         for (int j = 0; j < 4; ++j) vfa[j] = frag_tr_acc(Vt, AT_VSTR, 0, 32 * j, lane);
; #pragma unroll
;         for (int ks = 0; ks < 4; ks += 2) {
; #pragma unroll
;             for (int j = 0; j < 4; ++j) vfb[j] = frag_tr_acc(Vt, AT_VSTR, 16 * (ks + 1), 32 * j, lane);
; #pragma unroll
;             for (int j = 0; j < 4; ++j) o[j] = MFMA32(pk[ks], vfa[j], o[j]);
;             __builtin_amdgcn_sched_barrier(0);
;             if (ks + 2 < 4) {
; #pragma unroll
;                 for (int j = 0; j < 4; ++j) vfa[j] = frag_tr_acc(Vt, AT_VSTR, 16 * (ks + 2), 32 * j, lane);
;             }
; #pragma unroll
;             for (int j = 0; j < 4; ++j) o[j] = MFMA32(pk[ks + 1], vfb[j], o[j]);
;             __builtin_amdgcn_sched_barrier(0);
;         }
;         if (t + 2 < ntiles) AT_STOREK(t & 1);
;         if (t + 1 < ntiles) AT_STOREV((t + 1) & 1);
;         __syncthreads();
;         sa = na; sb = nb;
;     }
.Latt_vdone_b3:
	ds_read_b128 v[128:131], v197 offset:0
	ds_read_b128 v[132:135], v197 offset:8704
	ds_read_b128 v[136:139], v197 offset:32
	ds_read_b128 v[140:143], v197 offset:8736
	s_waitcnt lgkmcnt(2)
	v_mfma_f32_32x32x16_bf16 v[80:95], v[128:131], v[158:161], v[64:79]
	v_mfma_f32_32x32x16_bf16 v[96:111], v[132:135], v[158:161], v[64:79]
	ds_read_b128 v[128:131], v197 offset:64
	ds_read_b128 v[132:135], v197 offset:8768
	s_waitcnt lgkmcnt(2)
	v_mfma_f32_32x32x16_bf16 v[80:95], v[136:139], v[154:157], v[80:95]
	v_mfma_f32_32x32x16_bf16 v[96:111], v[140:143], v[154:157], v[96:111]
	ds_read_b128 v[136:139], v197 offset:96
	ds_read_b128 v[140:143], v197 offset:8800
	s_waitcnt lgkmcnt(2)
	v_mfma_f32_32x32x16_bf16 v[80:95], v[128:131], v[150:153], v[80:95]
	v_mfma_f32_32x32x16_bf16 v[96:111], v[132:135], v[150:153], v[96:111]
	s_waitcnt lgkmcnt(0)
	v_mfma_f32_32x32x16_bf16 v[80:95], v[136:139], v[146:149], v[80:95]
	v_mfma_f32_32x32x16_bf16 v[96:111], v[140:143], v[146:149], v[96:111]
	ds_read_b64_tr_b16 v[202:203], v184 offset:34816
	ds_read_b64_tr_b16 v[206:207], v184 offset:34880
	ds_read_b64_tr_b16 v[210:211], v184 offset:34944
	ds_read_b64_tr_b16 v[214:215], v184 offset:35008
	ds_read_b64_tr_b16 v[204:205], v184 offset:37376
	ds_read_b64_tr_b16 v[208:209], v184 offset:37440
	ds_read_b64_tr_b16 v[212:213], v184 offset:37504
	ds_read_b64_tr_b16 v[216:217], v184 offset:37568
	ds_read_b64_tr_b16 v[218:219], v184 offset:39936
	ds_read_b64_tr_b16 v[222:223], v184 offset:40000
	ds_read_b64_tr_b16 v[226:227], v184 offset:40064
	ds_read_b64_tr_b16 v[230:231], v184 offset:40128
	ds_read_b64_tr_b16 v[220:221], v184 offset:42496
	ds_read_b64_tr_b16 v[224:225], v184 offset:42560
	ds_read_b64_tr_b16 v[228:229], v184 offset:42624
	s_waitcnt lgkmcnt(14)
	ds_read_b64_tr_b16 v[232:233], v184 offset:42688
	s_waitcnt lgkmcnt(8)
	v_mfma_f32_32x32x16_bf16 v[32:47], v[112:115], v[202:205], v[32:47]
	v_mfma_f32_32x32x16_bf16 v[48:63], v[112:115], v[206:209], v[48:63]
	v_mfma_f32_32x32x16_bf16 v[0:15], v[112:115], v[210:213], v[0:15]
	v_mfma_f32_32x32x16_bf16 v[16:31], v[112:115], v[214:217], v[16:31]
	ds_read_b64_tr_b16 v[202:203], v184 offset:45056
	ds_read_b64_tr_b16 v[206:207], v184 offset:45120
	ds_read_b64_tr_b16 v[210:211], v184 offset:45184
	ds_read_b64_tr_b16 v[214:215], v184 offset:45248
	ds_read_b64_tr_b16 v[204:205], v184 offset:47616
	ds_read_b64_tr_b16 v[208:209], v184 offset:47680
	ds_read_b64_tr_b16 v[212:213], v184 offset:47744
	s_waitcnt lgkmcnt(14)
	ds_read_b64_tr_b16 v[216:217], v184 offset:47808
	s_waitcnt lgkmcnt(8)
	v_mfma_f32_32x32x16_bf16 v[32:47], v[116:119], v[218:221], v[32:47]
	v_mfma_f32_32x32x16_bf16 v[48:63], v[116:119], v[222:225], v[48:63]
	v_mfma_f32_32x32x16_bf16 v[0:15], v[116:119], v[226:229], v[0:15]
	v_mfma_f32_32x32x16_bf16 v[16:31], v[116:119], v[230:233], v[16:31]
	ds_read_b64_tr_b16 v[218:219], v184 offset:50176
	ds_read_b64_tr_b16 v[222:223], v184 offset:50240
	ds_read_b64_tr_b16 v[226:227], v184 offset:50304
	ds_read_b64_tr_b16 v[230:231], v184 offset:50368
	ds_read_b64_tr_b16 v[220:221], v184 offset:52736
	ds_read_b64_tr_b16 v[224:225], v184 offset:52800
	ds_read_b64_tr_b16 v[228:229], v184 offset:52864
	s_waitcnt lgkmcnt(14)
	ds_read_b64_tr_b16 v[232:233], v184 offset:52928
	s_waitcnt lgkmcnt(8)
	v_mfma_f32_32x32x16_bf16 v[32:47], v[120:123], v[202:205], v[32:47]
	v_mfma_f32_32x32x16_bf16 v[48:63], v[120:123], v[206:209], v[48:63]
	v_mfma_f32_32x32x16_bf16 v[0:15], v[120:123], v[210:213], v[0:15]
	v_mfma_f32_32x32x16_bf16 v[16:31], v[120:123], v[214:217], v[16:31]
	s_waitcnt lgkmcnt(0)
	v_mfma_f32_32x32x16_bf16 v[32:47], v[124:127], v[218:221], v[32:47]
	v_mfma_f32_32x32x16_bf16 v[48:63], v[124:127], v[222:225], v[48:63]
	v_mfma_f32_32x32x16_bf16 v[0:15], v[124:127], v[226:229], v[0:15]
	v_mfma_f32_32x32x16_bf16 v[16:31], v[124:127], v[230:233], v[16:31]
	s_nop 7
	s_nop 7
	v_exp_f32_e32 v80, v80
	v_exp_f32_e32 v96, v96
	v_exp_f32_e32 v81, v81
	v_exp_f32_e32 v97, v97
	v_exp_f32_e32 v82, v82
	v_exp_f32_e32 v98, v98
	v_exp_f32_e32 v83, v83
	v_exp_f32_e32 v99, v99
	v_exp_f32_e32 v84, v84
	v_exp_f32_e32 v100, v100
	v_exp_f32_e32 v85, v85
	v_exp_f32_e32 v101, v101
	v_exp_f32_e32 v86, v86
	v_exp_f32_e32 v102, v102
	v_exp_f32_e32 v87, v87
	v_exp_f32_e32 v103, v103
	v_exp_f32_e32 v88, v88
	v_exp_f32_e32 v104, v104
	v_exp_f32_e32 v89, v89
	v_exp_f32_e32 v105, v105
	v_exp_f32_e32 v90, v90
	v_exp_f32_e32 v106, v106
	v_exp_f32_e32 v91, v91
	v_exp_f32_e32 v107, v107
	v_exp_f32_e32 v92, v92
	v_exp_f32_e32 v108, v108
	v_exp_f32_e32 v93, v93
	v_exp_f32_e32 v109, v109
	v_exp_f32_e32 v94, v94
	v_exp_f32_e32 v110, v110
	v_exp_f32_e32 v95, v95
	v_exp_f32_e32 v111, v111
	v_cvt_pk_bf16_f32 v112, v80, v81
	v_cvt_pk_bf16_f32 v113, v82, v83
	v_cvt_pk_bf16_f32 v114, v84, v85
	v_cvt_pk_bf16_f32 v115, v86, v87
	v_cvt_pk_bf16_f32 v116, v88, v89
	v_cvt_pk_bf16_f32 v117, v90, v91
	v_cvt_pk_bf16_f32 v118, v92, v93
	v_cvt_pk_bf16_f32 v119, v94, v95
	v_cvt_pk_bf16_f32 v120, v96, v97
	v_cvt_pk_bf16_f32 v121, v98, v99
	v_cvt_pk_bf16_f32 v122, v100, v101
	v_cvt_pk_bf16_f32 v123, v102, v103
	v_cvt_pk_bf16_f32 v124, v104, v105
	v_cvt_pk_bf16_f32 v125, v106, v107
	v_cvt_pk_bf16_f32 v126, v108, v109
	v_cvt_pk_bf16_f32 v127, v110, v111
	v_add_f32_e32 v80, v80, v96
	v_add_f32_e32 v81, v81, v97
	v_add_f32_e32 v82, v82, v98
	v_add_f32_e32 v83, v83, v99
	v_add_f32_e32 v84, v84, v100
	v_add_f32_e32 v85, v85, v101
	v_add_f32_e32 v86, v86, v102
	v_add_f32_e32 v87, v87, v103
	v_add_f32_e32 v88, v88, v104
	v_add_f32_e32 v89, v89, v105
	v_add_f32_e32 v90, v90, v106
	v_add_f32_e32 v91, v91, v107
	v_add_f32_e32 v92, v92, v108
	v_add_f32_e32 v93, v93, v109
	v_add_f32_e32 v94, v94, v110
	v_add_f32_e32 v95, v95, v111
	v_add_f32_e32 v80, v80, v88
	v_add_f32_e32 v81, v81, v89
	v_add_f32_e32 v82, v82, v90
	v_add_f32_e32 v83, v83, v91
	v_add_f32_e32 v84, v84, v92
	v_add_f32_e32 v85, v85, v93
	v_add_f32_e32 v86, v86, v94
	v_add_f32_e32 v87, v87, v95
	v_add_f32_e32 v80, v80, v84
	v_add_f32_e32 v81, v81, v85
	v_add_f32_e32 v82, v82, v86
	v_add_f32_e32 v83, v83, v87
	v_add_f32_e32 v80, v80, v82
	v_add_f32_e32 v81, v81, v83
	v_add_f32_e32 v80, v80, v81
	v_add_f32_e32 v201, v201, v80
	s_barrier
	s_add_i32 s5, s2, 7
	s_cmp_ge_u32 s5, 36
	s_cbranch_scc1 .Latt_nokload_b4
	s_cmp_lt_u32 s5, 4
	s_cselect_b32 s15, s42, s43
	s_lshl_b32 s45, s5, 6
	s_add_i32 s15, s15, s45
	s_lshl_b32 s15, s15, 10
	v_add_u32_e32 v186, s15, v178
	v_add_u32_e32 v187, 0x8000, v186
	global_load_dwordx4 v[234:237], v186, s[72:73]
	global_load_dwordx4 v[238:241], v187, s[72:73]

; #define AT_LOADK(t) do { const int kr_ = AT_KROW(t); _Pragma("unroll") for (int i_ = 0; i_ < 2; ++i_) kreg[i_] = *(const u32x4*)(Kp + (size_t)(kr_ + prow0 + 32 * i_) * 512 + pch * 8); } while (0)
; #define AT_LOADV(t) do { const int kr_ = AT_KROW(t); _Pragma("unroll") for (int i_ = 0; i_ < 2; ++i_) vreg[i_] = *(const u32x4*)(Vp + (size_t)(kr_ + prow0 + 32 * i_) * 512 + pch * 8); } while (0)
; #define AT_STOREK(st) do { _Pragma("unroll") for (int i_ = 0; i_ < 2; ++i_) *(LAS u32x4*)(L + AT_K + (st) * AT_KBYTES + (prow0 + 32 * i_) * AT_KSTR + pch * 16) = kreg[i_]; } while (0)
; #define AT_STOREV(st) do { _Pragma("unroll") for (int i_ = 0; i_ < 2; ++i_) *(LAS u32x4*)(L + AT_V + (st) * AT_VBYTES + (prow0 + 32 * i_) * AT_VSTR + pch * 16) = vreg[i_]; } while (0)
; __device__ __forceinline__ void attn_unit(const Frame& F, int layer, int qrow0, int ntiles, int b, int head, float lam, float m2, float lam_init) {
;     ...
;     for (int t = 0; t < ntiles; ++t) {
;         if (t + 2 < ntiles) AT_LOADK(t + 2);
;         if (t + 1 < ntiles) AT_LOADV(t + 1);
;     ...
;         if (t + 2 < ntiles) AT_STOREK(t & 1);
;         if (t + 1 < ntiles) AT_STOREV((t + 1) & 1);
;         __syncthreads();
.Latt_novload_b4:
	s_add_i32 s5, s2, 7
	s_cmp_ge_u32 s5, 36
	s_cbranch_scc1 .Latt_drain_b4
	s_waitcnt vmcnt(4)
	s_branch .Latt_stage_b4

; __device__ __forceinline__ void attn_unit(const Frame& F, int layer, int qrow0, int ntiles, int b, int head, float lam, float m2, float lam_init) {
;     ...
;     if (wave >= 4) __builtin_amdgcn_s_setprio(1);
;     AT_LOADK(0); AT_LOADV(0); AT_STOREK(0); AT_STOREV(0);
;     if (ntiles > 1) { AT_LOADK(1); AT_STOREK(1); }
;     __syncthreads();
;     f32x16 sa, sb, na, nb;
;     AT_QK(sa, sb, 0);
;     lds_barrier();
;     for (int t = 0; t < ntiles; ++t) {
;         if (t + 2 < ntiles) AT_LOADK(t + 2);
;         if (t + 1 < ntiles) AT_LOADV(t + 1);
;         if (t + 1 < ntiles) AT_QK(na, nb, (t + 1) & 1);
;         float ls = 0.f;
; #pragma unroll
;         for (int i = 0; i < 16; ++i) { sa[i] = __builtin_amdgcn_exp2f(sa[i]); sb[i] = __builtin_amdgcn_exp2f(sb[i]); ls += sa[i] + sb[i]; }
;         lsum += ls;
;         bf16x8 pk[4];
;         { u32x4 w0, w1, w2, w3;
; #pragma unroll
;           for (int i = 0; i < 4; ++i) { w0[i] = pk2(sa[2 * i], sa[2 * i + 1]); w1[i] = pk2(sa[8 + 2 * i], sa[9 + 2 * i]); w2[i] = pk2(sb[2 * i], sb[2 * i + 1]); w3[i] = pk2(sb[8 + 2 * i], sb[9 + 2 * i]); }
;           pk[0] = __builtin_bit_cast(bf16x8, w0); pk[1] = __builtin_bit_cast(bf16x8, w1); pk[2] = __builtin_bit_cast(bf16x8, w2); pk[3] = __builtin_bit_cast(bf16x8, w3); }
;         LAS const unsigned char* Vt = L + AT_V + (t & 1) * AT_VBYTES;
;         __builtin_amdgcn_sched_barrier(0);
;         bf16x8 vfa[4], vfb[4];
; #pragma unroll
;         for (int j = 0; j < 4; ++j) vfa[j] = frag_tr_acc(Vt, AT_VSTR, 0, 32 * j, lane);
; #pragma unroll
;         for (int ks = 0; ks < 4; ks += 2) {
; #pragma unroll
;             for (int j = 0; j < 4; ++j) vfb[j] = frag_tr_acc(Vt, AT_VSTR, 16 * (ks + 1), 32 * j, lane);
; #pragma unroll
;             for (int j = 0; j < 4; ++j) o[j] = MFMA32(pk[ks], vfa[j], o[j]);
;             __builtin_amdgcn_sched_barrier(0);
;             if (ks + 2 < 4) {
; #pragma unroll
;                 for (int j = 0; j < 4; ++j) vfa[j] = frag_tr_acc(Vt, AT_VSTR, 16 * (ks + 2), 32 * j, lane);
;             }
; #pragma unroll
;             for (int j = 0; j < 4; ++j) o[j] = MFMA32(pk[ks + 1], vfb[j], o[j]);
;             __builtin_amdgcn_sched_barrier(0);
;         }
;         if (t + 2 < ntiles) AT_STOREK(t & 1);
;         if (t + 1 < ntiles) AT_STOREV((t + 1) & 1);
;         __syncthreads();
;         sa = na; sb = nb;
;     }
.Latt_vdone_b4:
	ds_read_b128 v[128:131], v197 offset:17408
	ds_read_b128 v[132:135], v197 offset:26112
	ds_read_b128 v[136:139], v197 offset:17440
	ds_read_b128 v[140:143], v197 offset:26144
	s_waitcnt lgkmcnt(2)
	v_mfma_f32_32x32x16_bf16 v[80:95], v[128:131], v[158:161], v[64:79]
	v_mfma_f32_32x32x16_bf16 v[96:111], v[132:135], v[158:161], v[64:79]
	ds_read_b128 v[128:131], v197 offset:17472
	ds_read_b128 v[132:135], v197 offset:26176
	s_waitcnt lgkmcnt(2)
	v_mfma_f32_32x32x16_bf16 v[80:95], v[136:139], v[154:157], v[80:95]
	v_mfma_f32_32x32x16_bf16 v[96:111], v[140:143], v[154:157], v[96:111]
	ds_read_b128 v[136:139], v197 offset:17504
	ds_read_b128 v[140:143], v197 offset:26208
	s_waitcnt lgkmcnt(2)
	v_mfma_f32_32x32x16_bf16 v[80:95], v[128:131], v[150:153], v[80:95]
	v_mfma_f32_32x32x16_bf16 v[96:111], v[132:135], v[150:153], v[96:111]
	s_waitcnt lgkmcnt(0)
	v_mfma_f32_32x32x16_bf16 v[80:95], v[136:139], v[146:149], v[80:95]
	v_mfma_f32_32x32x16_bf16 v[96:111], v[140:143], v[146:149], v[96:111]
	ds_read_b64_tr_b16 v[202:203], v196 offset:34816
	ds_read_b64_tr_b16 v[206:207], v196 offset:34880
	ds_read_b64_tr_b16 v[210:211], v196 offset:34944
	ds_read_b64_tr_b16 v[214:215], v196 offset:35008
	ds_read_b64_tr_b16 v[204:205], v196 offset:37376
	ds_read_b64_tr_b16 v[208:209], v196 offset:37440
	ds_read_b64_tr_b16 v[212:213], v196 offset:37504
	ds_read_b64_tr_b16 v[216:217], v196 offset:37568
	ds_read_b64_tr_b16 v[218:219], v196 offset:39936
	ds_read_b64_tr_b16 v[222:223], v196 offset:40000
	ds_read_b64_tr_b16 v[226:227], v196 offset:40064
	ds_read_b64_tr_b16 v[230:231], v196 offset:40128
	ds_read_b64_tr_b16 v[220:221], v196 offset:42496
	ds_read_b64_tr_b16 v[224:225], v196 offset:42560
	ds_read_b64_tr_b16 v[228:229], v196 offset:42624
	s_waitcnt lgkmcnt(14)
	ds_read_b64_tr_b16 v[232:233], v196 offset:42688
	s_waitcnt lgkmcnt(8)
	v_mfma_f32_32x32x16_bf16 v[32:47], v[112:115], v[202:205], v[32:47]
	v_mfma_f32_32x32x16_bf16 v[48:63], v[112:115], v[206:209], v[48:63]
	v_mfma_f32_32x32x16_bf16 v[0:15], v[112:115], v[210:213], v[0:15]
	v_mfma_f32_32x32x16_bf16 v[16:31], v[112:115], v[214:217], v[16:31]
	ds_read_b64_tr_b16 v[202:203], v196 offset:45056
	ds_read_b64_tr_b16 v[206:207], v196 offset:45120
	ds_read_b64_tr_b16 v[210:211], v196 offset:45184
	ds_read_b64_tr_b16 v[214:215], v196 offset:45248
	ds_read_b64_tr_b16 v[204:205], v196 offset:47616
	ds_read_b64_tr_b16 v[208:209], v196 offset:47680
	ds_read_b64_tr_b16 v[212:213], v196 offset:47744
	s_waitcnt lgkmcnt(14)
	ds_read_b64_tr_b16 v[216:217], v196 offset:47808
	s_waitcnt lgkmcnt(8)
	v_mfma_f32_32x32x16_bf16 v[32:47], v[116:119], v[218:221], v[32:47]
	v_mfma_f32_32x32x16_bf16 v[48:63], v[116:119], v[222:225], v[48:63]
	v_mfma_f32_32x32x16_bf16 v[0:15], v[116:119], v[226:229], v[0:15]
	v_mfma_f32_32x32x16_bf16 v[16:31], v[116:119], v[230:233], v[16:31]
	ds_read_b64_tr_b16 v[218:219], v196 offset:50176
	ds_read_b64_tr_b16 v[222:223], v196 offset:50240
	ds_read_b64_tr_b16 v[226:227], v196 offset:50304
	ds_read_b64_tr_b16 v[230:231], v196 offset:50368
	ds_read_b64_tr_b16 v[220:221], v196 offset:52736
	ds_read_b64_tr_b16 v[224:225], v196 offset:52800
	ds_read_b64_tr_b16 v[228:229], v196 offset:52864
	s_waitcnt lgkmcnt(14)
	ds_read_b64_tr_b16 v[232:233], v196 offset:52928
	s_waitcnt lgkmcnt(8)
	v_mfma_f32_32x32x16_bf16 v[32:47], v[120:123], v[202:205], v[32:47]
	v_mfma_f32_32x32x16_bf16 v[48:63], v[120:123], v[206:209], v[48:63]
	v_mfma_f32_32x32x16_bf16 v[0:15], v[120:123], v[210:213], v[0:15]
	v_mfma_f32_32x32x16_bf16 v[16:31], v[120:123], v[214:217], v[16:31]
	s_waitcnt lgkmcnt(0)
	v_mfma_f32_32x32x16_bf16 v[32:47], v[124:127], v[218:221], v[32:47]
	v_mfma_f32_32x32x16_bf16 v[48:63], v[124:127], v[222:225], v[48:63]
	v_mfma_f32_32x32x16_bf16 v[0:15], v[124:127], v[226:229], v[0:15]
	v_mfma_f32_32x32x16_bf16 v[16:31], v[124:127], v[230:233], v[16:31]
	s_nop 7
	s_nop 7
	v_exp_f32_e32 v80, v80
	v_exp_f32_e32 v96, v96
	v_exp_f32_e32 v81, v81
	v_exp_f32_e32 v97, v97
	v_exp_f32_e32 v82, v82
	v_exp_f32_e32 v98, v98
	v_exp_f32_e32 v83, v83
	v_exp_f32_e32 v99, v99
	v_exp_f32_e32 v84, v84
	v_exp_f32_e32 v100, v100
	v_exp_f32_e32 v85, v85
	v_exp_f32_e32 v101, v101
	v_exp_f32_e32 v86, v86
	v_exp_f32_e32 v102, v102
	v_exp_f32_e32 v87, v87
	v_exp_f32_e32 v103, v103
	v_exp_f32_e32 v88, v88
	v_exp_f32_e32 v104, v104
	v_exp_f32_e32 v89, v89
	v_exp_f32_e32 v105, v105
	v_exp_f32_e32 v90, v90
	v_exp_f32_e32 v106, v106
	v_exp_f32_e32 v91, v91
	v_exp_f32_e32 v107, v107
	v_exp_f32_e32 v92, v92
	v_exp_f32_e32 v108, v108
	v_exp_f32_e32 v93, v93
	v_exp_f32_e32 v109, v109
	v_exp_f32_e32 v94, v94
	v_exp_f32_e32 v110, v110
	v_exp_f32_e32 v95, v95
	v_exp_f32_e32 v111, v111
	v_cvt_pk_bf16_f32 v112, v80, v81
	v_cvt_pk_bf16_f32 v113, v82, v83
	v_cvt_pk_bf16_f32 v114, v84, v85
	v_cvt_pk_bf16_f32 v115, v86, v87
	v_cvt_pk_bf16_f32 v116, v88, v89
	v_cvt_pk_bf16_f32 v117, v90, v91
	v_cvt_pk_bf16_f32 v118, v92, v93
	v_cvt_pk_bf16_f32 v119, v94, v95
	v_cvt_pk_bf16_f32 v120, v96, v97
	v_cvt_pk_bf16_f32 v121, v98, v99
	v_cvt_pk_bf16_f32 v122, v100, v101
	v_cvt_pk_bf16_f32 v123, v102, v103
	v_cvt_pk_bf16_f32 v124, v104, v105
	v_cvt_pk_bf16_f32 v125, v106, v107
	v_cvt_pk_bf16_f32 v126, v108, v109
	v_cvt_pk_bf16_f32 v127, v110, v111
	v_add_f32_e32 v80, v80, v96
	v_add_f32_e32 v81, v81, v97
	v_add_f32_e32 v82, v82, v98
	v_add_f32_e32 v83, v83, v99
	v_add_f32_e32 v84, v84, v100
	v_add_f32_e32 v85, v85, v101
	v_add_f32_e32 v86, v86, v102
	v_add_f32_e32 v87, v87, v103
	v_add_f32_e32 v88, v88, v104
	v_add_f32_e32 v89, v89, v105
	v_add_f32_e32 v90, v90, v106
	v_add_f32_e32 v91, v91, v107
	v_add_f32_e32 v92, v92, v108
	v_add_f32_e32 v93, v93, v109
	v_add_f32_e32 v94, v94, v110
	v_add_f32_e32 v95, v95, v111
	v_add_f32_e32 v80, v80, v88
	v_add_f32_e32 v81, v81, v89
	v_add_f32_e32 v82, v82, v90
	v_add_f32_e32 v83, v83, v91
	v_add_f32_e32 v84, v84, v92
	v_add_f32_e32 v85, v85, v93
	v_add_f32_e32 v86, v86, v94
	v_add_f32_e32 v87, v87, v95
	v_add_f32_e32 v80, v80, v84
	v_add_f32_e32 v81, v81, v85
	v_add_f32_e32 v82, v82, v86
	v_add_f32_e32 v83, v83, v87
	v_add_f32_e32 v80, v80, v82
	v_add_f32_e32 v81, v81, v83
	v_add_f32_e32 v80, v80, v81
	v_add_f32_e32 v201, v201, v80
	s_barrier
	s_add_i32 s5, s2, 8
	s_cmp_ge_u32 s5, 36
	s_cbranch_scc1 .Latt_nokload_b5
	s_cmp_lt_u32 s5, 4
	s_cselect_b32 s15, s42, s43
	s_lshl_b32 s45, s5, 6
	s_add_i32 s15, s15, s45
	s_lshl_b32 s15, s15, 10
	v_add_u32_e32 v186, s15, v178
	v_add_u32_e32 v187, 0x8000, v186
	global_load_dwordx4 v[162:165], v186, s[72:73]
	global_load_dwordx4 v[166:169], v187, s[72:73]

; #define AT_LOADK(t) do { const int kr_ = AT_KROW(t); _Pragma("unroll") for (int i_ = 0; i_ < 2; ++i_) kreg[i_] = *(const u32x4*)(Kp + (size_t)(kr_ + prow0 + 32 * i_) * 512 + pch * 8); } while (0)
; #define AT_LOADV(t) do { const int kr_ = AT_KROW(t); _Pragma("unroll") for (int i_ = 0; i_ < 2; ++i_) vreg[i_] = *(const u32x4*)(Vp + (size_t)(kr_ + prow0 + 32 * i_) * 512 + pch * 8); } while (0)
; #define AT_STOREK(st) do { _Pragma("unroll") for (int i_ = 0; i_ < 2; ++i_) *(LAS u32x4*)(L + AT_K + (st) * AT_KBYTES + (prow0 + 32 * i_) * AT_KSTR + pch * 16) = kreg[i_]; } while (0)
; #define AT_STOREV(st) do { _Pragma("unroll") for (int i_ = 0; i_ < 2; ++i_) *(LAS u32x4*)(L + AT_V + (st) * AT_VBYTES + (prow0 + 32 * i_) * AT_VSTR + pch * 16) = vreg[i_]; } while (0)
; __device__ __forceinline__ void attn_unit(const Frame& F, int layer, int qrow0, int ntiles, int b, int head, float lam, float m2, float lam_init) {
;     ...
;     for (int t = 0; t < ntiles; ++t) {
;         if (t + 2 < ntiles) AT_LOADK(t + 2);
;         if (t + 1 < ntiles) AT_LOADV(t + 1);
;     ...
;         if (t + 2 < ntiles) AT_STOREK(t & 1);
;         if (t + 1 < ntiles) AT_STOREV((t + 1) & 1);
;         __syncthreads();
.Latt_novload_b5:
	s_add_i32 s5, s2, 8
	s_cmp_ge_u32 s5, 36
	s_cbranch_scc1 .Latt_drain_b5
	s_waitcnt vmcnt(4)
	s_branch .Latt_stage_b5

; __device__ __forceinline__ void attn_unit(const Frame& F, int layer, int qrow0, int ntiles, int b, int head, float lam, float m2, float lam_init) {
;     ...
;     if (wave >= 4) __builtin_amdgcn_s_setprio(1);
;     AT_LOADK(0); AT_LOADV(0); AT_STOREK(0); AT_STOREV(0);
;     if (ntiles > 1) { AT_LOADK(1); AT_STOREK(1); }
;     __syncthreads();
;     f32x16 sa, sb, na, nb;
;     AT_QK(sa, sb, 0);
;     lds_barrier();
;     for (int t = 0; t < ntiles; ++t) {
;         if (t + 2 < ntiles) AT_LOADK(t + 2);
;         if (t + 1 < ntiles) AT_LOADV(t + 1);
;         if (t + 1 < ntiles) AT_QK(na, nb, (t + 1) & 1);
;         float ls = 0.f;
; #pragma unroll
;         for (int i = 0; i < 16; ++i) { sa[i] = __builtin_amdgcn_exp2f(sa[i]); sb[i] = __builtin_amdgcn_exp2f(sb[i]); ls += sa[i] + sb[i]; }
;         lsum += ls;
;         bf16x8 pk[4];
;         { u32x4 w0, w1, w2, w3;
; #pragma unroll
;           for (int i = 0; i < 4; ++i) { w0[i] = pk2(sa[2 * i], sa[2 * i + 1]); w1[i] = pk2(sa[8 + 2 * i], sa[9 + 2 * i]); w2[i] = pk2(sb[2 * i], sb[2 * i + 1]); w3[i] = pk2(sb[8 + 2 * i], sb[9 + 2 * i]); }
;           pk[0] = __builtin_bit_cast(bf16x8, w0); pk[1] = __builtin_bit_cast(bf16x8, w1); pk[2] = __builtin_bit_cast(bf16x8, w2); pk[3] = __builtin_bit_cast(bf16x8, w3); }
;         LAS const unsigned char* Vt = L + AT_V + (t & 1) * AT_VBYTES;
;         __builtin_amdgcn_sched_barrier(0);
;         bf16x8 vfa[4], vfb[4];
; #pragma unroll
;         for (int j = 0; j < 4; ++j) vfa[j] = frag_tr_acc(Vt, AT_VSTR, 0, 32 * j, lane);
; #pragma unroll
;         for (int ks = 0; ks < 4; ks += 2) {
; #pragma unroll
;             for (int j = 0; j < 4; ++j) vfb[j] = frag_tr_acc(Vt, AT_VSTR, 16 * (ks + 1), 32 * j, lane);
; #pragma unroll
;             for (int j = 0; j < 4; ++j) o[j] = MFMA32(pk[ks], vfa[j], o[j]);
;             __builtin_amdgcn_sched_barrier(0);
;             if (ks + 2 < 4) {
; #pragma unroll
;                 for (int j = 0; j < 4; ++j) vfa[j] = frag_tr_acc(Vt, AT_VSTR, 16 * (ks + 2), 32 * j, lane);
;             }
; #pragma unroll
;             for (int j = 0; j < 4; ++j) o[j] = MFMA32(pk[ks + 1], vfb[j], o[j]);
;             __builtin_amdgcn_sched_barrier(0);
;         }
;         if (t + 2 < ntiles) AT_STOREK(t & 1);
;         if (t + 1 < ntiles) AT_STOREV((t + 1) & 1);
;         __syncthreads();
;         sa = na; sb = nb;
;     }
.Latt_vdone_b5:
	ds_read_b128 v[128:131], v190 offset:0
	ds_read_b128 v[132:135], v190 offset:8704
	ds_read_b128 v[136:139], v190 offset:32
	ds_read_b128 v[140:143], v190 offset:8736
	s_waitcnt lgkmcnt(2)
	v_mfma_f32_32x32x16_bf16 v[80:95], v[128:131], v[158:161], v[64:79]
	v_mfma_f32_32x32x16_bf16 v[96:111], v[132:135], v[158:161], v[64:79]
	ds_read_b128 v[128:131], v190 offset:64
	ds_read_b128 v[132:135], v190 offset:8768
	s_waitcnt lgkmcnt(2)
	v_mfma_f32_32x32x16_bf16 v[80:95], v[136:139], v[154:157], v[80:95]
	v_mfma_f32_32x32x16_bf16 v[96:111], v[140:143], v[154:157], v[96:111]
	ds_read_b128 v[136:139], v190 offset:96
	ds_read_b128 v[140:143], v190 offset:8800
	s_waitcnt lgkmcnt(2)
	v_mfma_f32_32x32x16_bf16 v[80:95], v[128:131], v[150:153], v[80:95]
	v_mfma_f32_32x32x16_bf16 v[96:111], v[132:135], v[150:153], v[96:111]
	s_waitcnt lgkmcnt(0)
	v_mfma_f32_32x32x16_bf16 v[80:95], v[136:139], v[146:149], v[80:95]
	v_mfma_f32_32x32x16_bf16 v[96:111], v[140:143], v[146:149], v[96:111]
	ds_read_b64_tr_b16 v[202:203], v191 offset:34816
	ds_read_b64_tr_b16 v[206:207], v191 offset:34880
	ds_read_b64_tr_b16 v[210:211], v191 offset:34944
	ds_read_b64_tr_b16 v[214:215], v191 offset:35008
	ds_read_b64_tr_b16 v[204:205], v191 offset:37376
	ds_read_b64_tr_b16 v[208:209], v191 offset:37440
	ds_read_b64_tr_b16 v[212:213], v191 offset:37504
	ds_read_b64_tr_b16 v[216:217], v191 offset:37568
	ds_read_b64_tr_b16 v[218:219], v191 offset:39936
	ds_read_b64_tr_b16 v[222:223], v191 offset:40000
	ds_read_b64_tr_b16 v[226:227], v191 offset:40064
	ds_read_b64_tr_b16 v[230:231], v191 offset:40128
	ds_read_b64_tr_b16 v[220:221], v191 offset:42496
	ds_read_b64_tr_b16 v[224:225], v191 offset:42560
	ds_read_b64_tr_b16 v[228:229], v191 offset:42624
	s_waitcnt lgkmcnt(14)
	ds_read_b64_tr_b16 v[232:233], v191 offset:42688
	s_waitcnt lgkmcnt(8)
	v_mfma_f32_32x32x16_bf16 v[32:47], v[112:115], v[202:205], v[32:47]
	v_mfma_f32_32x32x16_bf16 v[48:63], v[112:115], v[206:209], v[48:63]
	v_mfma_f32_32x32x16_bf16 v[0:15], v[112:115], v[210:213], v[0:15]
	v_mfma_f32_32x32x16_bf16 v[16:31], v[112:115], v[214:217], v[16:31]
	ds_read_b64_tr_b16 v[202:203], v191 offset:45056
	ds_read_b64_tr_b16 v[206:207], v191 offset:45120
	ds_read_b64_tr_b16 v[210:211], v191 offset:45184
	ds_read_b64_tr_b16 v[214:215], v191 offset:45248
	ds_read_b64_tr_b16 v[204:205], v191 offset:47616
	ds_read_b64_tr_b16 v[208:209], v191 offset:47680
	ds_read_b64_tr_b16 v[212:213], v191 offset:47744
	s_waitcnt lgkmcnt(14)
	ds_read_b64_tr_b16 v[216:217], v191 offset:47808
	s_waitcnt lgkmcnt(8)
	v_mfma_f32_32x32x16_bf16 v[32:47], v[116:119], v[218:221], v[32:47]
	v_mfma_f32_32x32x16_bf16 v[48:63], v[116:119], v[222:225], v[48:63]
	v_mfma_f32_32x32x16_bf16 v[0:15], v[116:119], v[226:229], v[0:15]
	v_mfma_f32_32x32x16_bf16 v[16:31], v[116:119], v[230:233], v[16:31]
	ds_read_b64_tr_b16 v[218:219], v191 offset:50176
	ds_read_b64_tr_b16 v[222:223], v191 offset:50240
	ds_read_b64_tr_b16 v[226:227], v191 offset:50304
	ds_read_b64_tr_b16 v[230:231], v191 offset:50368
	ds_read_b64_tr_b16 v[220:221], v191 offset:52736
	ds_read_b64_tr_b16 v[224:225], v191 offset:52800
	ds_read_b64_tr_b16 v[228:229], v191 offset:52864
	s_waitcnt lgkmcnt(14)
	ds_read_b64_tr_b16 v[232:233], v191 offset:52928
	s_waitcnt lgkmcnt(8)
	v_mfma_f32_32x32x16_bf16 v[32:47], v[120:123], v[202:205], v[32:47]
	v_mfma_f32_32x32x16_bf16 v[48:63], v[120:123], v[206:209], v[48:63]
	v_mfma_f32_32x32x16_bf16 v[0:15], v[120:123], v[210:213], v[0:15]
	v_mfma_f32_32x32x16_bf16 v[16:31], v[120:123], v[214:217], v[16:31]
	s_waitcnt lgkmcnt(0)
	v_mfma_f32_32x32x16_bf16 v[32:47], v[124:127], v[218:221], v[32:47]
	v_mfma_f32_32x32x16_bf16 v[48:63], v[124:127], v[222:225], v[48:63]
	v_mfma_f32_32x32x16_bf16 v[0:15], v[124:127], v[226:229], v[0:15]
	v_mfma_f32_32x32x16_bf16 v[16:31], v[124:127], v[230:233], v[16:31]
	s_nop 7
	s_nop 7
	v_exp_f32_e32 v80, v80
	v_exp_f32_e32 v96, v96
	v_exp_f32_e32 v81, v81
	v_exp_f32_e32 v97, v97
	v_exp_f32_e32 v82, v82
	v_exp_f32_e32 v98, v98
	v_exp_f32_e32 v83, v83
	v_exp_f32_e32 v99, v99
	v_exp_f32_e32 v84, v84
	v_exp_f32_e32 v100, v100
	v_exp_f32_e32 v85, v85
	v_exp_f32_e32 v101, v101
	v_exp_f32_e32 v86, v86
	v_exp_f32_e32 v102, v102
	v_exp_f32_e32 v87, v87
	v_exp_f32_e32 v103, v103
	v_exp_f32_e32 v88, v88
	v_exp_f32_e32 v104, v104
	v_exp_f32_e32 v89, v89
	v_exp_f32_e32 v105, v105
	v_exp_f32_e32 v90, v90
	v_exp_f32_e32 v106, v106
	v_exp_f32_e32 v91, v91
	v_exp_f32_e32 v107, v107
	v_exp_f32_e32 v92, v92
	v_exp_f32_e32 v108, v108
	v_exp_f32_e32 v93, v93
	v_exp_f32_e32 v109, v109
	v_exp_f32_e32 v94, v94
	v_exp_f32_e32 v110, v110
	v_exp_f32_e32 v95, v95
	v_exp_f32_e32 v111, v111
	v_cvt_pk_bf16_f32 v112, v80, v81
	v_cvt_pk_bf16_f32 v113, v82, v83
	v_cvt_pk_bf16_f32 v114, v84, v85
	v_cvt_pk_bf16_f32 v115, v86, v87
	v_cvt_pk_bf16_f32 v116, v88, v89
	v_cvt_pk_bf16_f32 v117, v90, v91
	v_cvt_pk_bf16_f32 v118, v92, v93
	v_cvt_pk_bf16_f32 v119, v94, v95
	v_cvt_pk_bf16_f32 v120, v96, v97
	v_cvt_pk_bf16_f32 v121, v98, v99
	v_cvt_pk_bf16_f32 v122, v100, v101
	v_cvt_pk_bf16_f32 v123, v102, v103
	v_cvt_pk_bf16_f32 v124, v104, v105
	v_cvt_pk_bf16_f32 v125, v106, v107
	v_cvt_pk_bf16_f32 v126, v108, v109
	v_cvt_pk_bf16_f32 v127, v110, v111
	v_add_f32_e32 v80, v80, v96
	v_add_f32_e32 v81, v81, v97
	v_add_f32_e32 v82, v82, v98
	v_add_f32_e32 v83, v83, v99
	v_add_f32_e32 v84, v84, v100
	v_add_f32_e32 v85, v85, v101
	v_add_f32_e32 v86, v86, v102
	v_add_f32_e32 v87, v87, v103
	v_add_f32_e32 v88, v88, v104
	v_add_f32_e32 v89, v89, v105
	v_add_f32_e32 v90, v90, v106
	v_add_f32_e32 v91, v91, v107
	v_add_f32_e32 v92, v92, v108
	v_add_f32_e32 v93, v93, v109
	v_add_f32_e32 v94, v94, v110
	v_add_f32_e32 v95, v95, v111
	v_add_f32_e32 v80, v80, v88
	v_add_f32_e32 v81, v81, v89
	v_add_f32_e32 v82, v82, v90
	v_add_f32_e32 v83, v83, v91
	v_add_f32_e32 v84, v84, v92
	v_add_f32_e32 v85, v85, v93
	v_add_f32_e32 v86, v86, v94
	v_add_f32_e32 v87, v87, v95
	v_add_f32_e32 v80, v80, v84
	v_add_f32_e32 v81, v81, v85
	v_add_f32_e32 v82, v82, v86
	v_add_f32_e32 v83, v83, v87
	v_add_f32_e32 v80, v80, v82
	v_add_f32_e32 v81, v81, v83
	v_add_f32_e32 v80, v80, v81
	v_add_f32_e32 v201, v201, v80
	s_barrier
; #define LAS __attribute__((address_space(3)))
; __device__ __forceinline__ float shx(float v, int m, int lane) { return __int_as_float(__builtin_amdgcn_ds_bpermute((lane ^ m) << 2, __float_as_int(v))); }
; #define MFMA32(a, b, c) __builtin_amdgcn_mfma_f32_32x32x16_bf16((a), (b), (c), 0, 0, 0)
; #define AT_STOREK(st) do { _Pragma("unroll") for (int i_ = 0; i_ < 2; ++i_) *(LAS u32x4*)(L + AT_K + (st) * AT_KBYTES + (prow0 + 32 * i_) * AT_KSTR + pch * 16) = kreg[i_]; } while (0)
; #define AT_STOREV(st) do { _Pragma("unroll") for (int i_ = 0; i_ < 2; ++i_) *(LAS u32x4*)(L + AT_V + (st) * AT_VBYTES + (prow0 + 32 * i_) * AT_VSTR + pch * 16) = vreg[i_]; } while (0)
; __device__ __forceinline__ void attn_unit(const Frame& F, int layer, int qrow0, int ntiles, int b, int head, float lam, float m2, float lam_init) {
;     ...
;         for (int j = 0; j < 4; ++j) vfa[j] = frag_tr_acc(Vt, AT_VSTR, 0, 32 * j, lane);
; #pragma unroll
;         for (int ks = 0; ks < 4; ks += 2) {
; #pragma unroll
;             for (int j = 0; j < 4; ++j) vfb[j] = frag_tr_acc(Vt, AT_VSTR, 16 * (ks + 1), 32 * j, lane);
; #pragma unroll
;             for (int j = 0; j < 4; ++j) o[j] = MFMA32(pk[ks], vfa[j], o[j]);
;             __builtin_amdgcn_sched_barrier(0);
;             if (ks + 2 < 4) {
; #pragma unroll
;                 for (int j = 0; j < 4; ++j) vfa[j] = frag_tr_acc(Vt, AT_VSTR, 16 * (ks + 2), 32 * j, lane);
;             }
; #pragma unroll
;             for (int j = 0; j < 4; ++j) o[j] = MFMA32(pk[ks + 1], vfb[j], o[j]);
;             __builtin_amdgcn_sched_barrier(0);
;         }
;         if (t + 2 < ntiles) AT_STOREK(t & 1);
;         if (t + 1 < ntiles) AT_STOREV((t + 1) & 1);
;         __syncthreads();
;         sa = na; sb = nb;
;     }
;     ...
;     __builtin_amdgcn_s_setprio(0);
;     int lane_e = lane; asm volatile("" : "+v"(lane_e));
;     ...
;     const int r32e = lane_e & 31, hhe = lane_e >> 5;
;     LAS float* lx = (LAS float*)(L + AT_LX + wave * 256);
;     { const float l0 = lsum + shx(lsum, 32, lane_e); if (hh == 0) lx[r32] = (mp ? lam : 1.f) / l0; }
	s_add_i32 s2, s2, 6
	s_cmp_lt_u32 s2, 36
	s_cbranch_scc1 .Latt_lag_loop
	ds_read_b64_tr_b16 v[202:203], v184 offset:34816
	ds_read_b64_tr_b16 v[206:207], v184 offset:34880
	ds_read_b64_tr_b16 v[210:211], v184 offset:34944
	ds_read_b64_tr_b16 v[214:215], v184 offset:35008
	ds_read_b64_tr_b16 v[204:205], v184 offset:37376
	ds_read_b64_tr_b16 v[208:209], v184 offset:37440
	ds_read_b64_tr_b16 v[212:213], v184 offset:37504
	ds_read_b64_tr_b16 v[216:217], v184 offset:37568
	ds_read_b64_tr_b16 v[218:219], v184 offset:39936
	ds_read_b64_tr_b16 v[222:223], v184 offset:40000
	ds_read_b64_tr_b16 v[226:227], v184 offset:40064
	ds_read_b64_tr_b16 v[230:231], v184 offset:40128
	ds_read_b64_tr_b16 v[220:221], v184 offset:42496
	ds_read_b64_tr_b16 v[224:225], v184 offset:42560
	ds_read_b64_tr_b16 v[228:229], v184 offset:42624
	s_waitcnt lgkmcnt(14)
	ds_read_b64_tr_b16 v[232:233], v184 offset:42688
	s_waitcnt lgkmcnt(8)
	v_mfma_f32_32x32x16_bf16 v[32:47], v[112:115], v[202:205], v[32:47]
	v_mfma_f32_32x32x16_bf16 v[48:63], v[112:115], v[206:209], v[48:63]
	v_mfma_f32_32x32x16_bf16 v[0:15], v[112:115], v[210:213], v[0:15]
	v_mfma_f32_32x32x16_bf16 v[16:31], v[112:115], v[214:217], v[16:31]
	ds_read_b64_tr_b16 v[202:203], v184 offset:45056
	ds_read_b64_tr_b16 v[206:207], v184 offset:45120
	ds_read_b64_tr_b16 v[210:211], v184 offset:45184
	ds_read_b64_tr_b16 v[214:215], v184 offset:45248
	ds_read_b64_tr_b16 v[204:205], v184 offset:47616
	ds_read_b64_tr_b16 v[208:209], v184 offset:47680
	ds_read_b64_tr_b16 v[212:213], v184 offset:47744
	s_waitcnt lgkmcnt(14)
	ds_read_b64_tr_b16 v[216:217], v184 offset:47808
	s_waitcnt lgkmcnt(8)
	v_mfma_f32_32x32x16_bf16 v[32:47], v[116:119], v[218:221], v[32:47]
	v_mfma_f32_32x32x16_bf16 v[48:63], v[116:119], v[222:225], v[48:63]
	v_mfma_f32_32x32x16_bf16 v[0:15], v[116:119], v[226:229], v[0:15]
	v_mfma_f32_32x32x16_bf16 v[16:31], v[116:119], v[230:233], v[16:31]
	ds_read_b64_tr_b16 v[218:219], v184 offset:50176
	ds_read_b64_tr_b16 v[222:223], v184 offset:50240
	ds_read_b64_tr_b16 v[226:227], v184 offset:50304
	ds_read_b64_tr_b16 v[230:231], v184 offset:50368
	ds_read_b64_tr_b16 v[220:221], v184 offset:52736
	ds_read_b64_tr_b16 v[224:225], v184 offset:52800
	ds_read_b64_tr_b16 v[228:229], v184 offset:52864
	s_waitcnt lgkmcnt(14)
	ds_read_b64_tr_b16 v[232:233], v184 offset:52928
	s_waitcnt lgkmcnt(8)
	v_mfma_f32_32x32x16_bf16 v[32:47], v[120:123], v[202:205], v[32:47]
	v_mfma_f32_32x32x16_bf16 v[48:63], v[120:123], v[206:209], v[48:63]
	v_mfma_f32_32x32x16_bf16 v[0:15], v[120:123], v[210:213], v[0:15]
	v_mfma_f32_32x32x16_bf16 v[16:31], v[120:123], v[214:217], v[16:31]
	s_waitcnt lgkmcnt(0)
	v_mfma_f32_32x32x16_bf16 v[32:47], v[124:127], v[218:221], v[32:47]
	v_mfma_f32_32x32x16_bf16 v[48:63], v[124:127], v[222:225], v[48:63]
	v_mfma_f32_32x32x16_bf16 v[0:15], v[124:127], v[226:229], v[0:15]
	v_mfma_f32_32x32x16_bf16 v[16:31], v[124:127], v[230:233], v[16:31]
.Latt_exit:
	s_barrier
	s_nop 7
	s_nop 7
	v_mov_b32_e32 v64, v201
	s_setprio 0
	s_lshl_b32 s2, s12, 8
	v_lshlrev_b32_e32 v86, 2, v193
	v_xor_b32_e32 v65, 0x80, v86
	ds_bpermute_b32 v65, v65, v64
	s_add_i32 s4, s2, 0
	v_and_b32_e32 v80, 31, v193
	s_add_i32 s4, s4, 0x12800
	v_cmp_gt_u32_e32 vcc, 32, v193
	s_and_saveexec_b64 s[2:3], vcc
	s_cbranch_execz .LBB0_553
	s_cmp_lg_u32 s10, 0
	s_waitcnt lgkmcnt(0)
	v_add_f32_e32 v64, v64, v65
	v_mov_b32_e32 v65, s19
	s_cselect_b64 vcc, -1, 0
	v_cndmask_b32_e32 v65, 1.0, v65, vcc
	v_div_scale_f32 v66, s[12:13], v64, v64, v65
	v_rcp_f32_e32 v67, v66
	s_nop 0
	v_fma_f32 v68, -v66, v67, 1.0
	v_fmac_f32_e32 v67, v68, v67
	v_div_scale_f32 v68, vcc, v65, v64, v65
	v_mul_f32_e32 v69, v68, v67
	v_fma_f32 v70, -v66, v69, v68
	v_fmac_f32_e32 v69, v70, v67
	v_fma_f32 v66, -v66, v69, v68
	v_div_fmas_f32 v66, v66, v67, v69
	v_div_fixup_f32 v64, v66, v64, v65
	v_lshl_add_u32 v65, v80, 2, s4
	ds_write_b32 v65, v64
